# FFT: removed 541 s_nop 0 pads between packed-f32 inline-asm ops (plain VALU dependency, interlocked)
# speedup vs baseline: 1.0402x; 1.0027x over previous
.LBB0_755:
	s_waitcnt vmcnt(58)
	v_pk_add_f32 v[2:3], v[10:11], v[42:43] neg_lo:[0,1] neg_hi:[0,1]
	v_mov_b64_e32 v[102:103], s[4:5]
	v_pk_mul_f32 v[4:5], v[2:3], v[102:103] op_sel_hi:[1,0]
	v_mov_b32_e32 v148, v204
	v_pk_fma_f32 v[116:117], v[2:3], v[102:103], v[4:5] op_sel:[1,1,0] op_sel_hi:[0,1,1] neg_hi:[1,0,0]
	s_waitcnt vmcnt(54)
	v_pk_add_f32 v[4:5], v[14:15], v[46:47] neg_lo:[0,1] neg_hi:[0,1]
	v_mov_b64_e32 v[2:3], s[6:7]
	v_pk_mul_f32 v[104:105], v[4:5], v[2:3] op_sel_hi:[1,0]
	v_pk_add_f32 v[114:115], v[42:43], v[10:11]
	v_pk_fma_f32 v[120:121], v[4:5], v[2:3], v[104:105] op_sel:[1,1,0] op_sel_hi:[0,1,1] neg_hi:[1,0,0]
	s_waitcnt vmcnt(50)
	v_pk_add_f32 v[4:5], v[18:19], v[50:51] neg_lo:[0,1] neg_hi:[0,1]
	v_mov_b64_e32 v[104:105], s[10:11]
	v_pk_mul_f32 v[106:107], v[4:5], v[104:105] op_sel_hi:[1,0]
	v_cmp_ne_u32_e32 vcc, 0, v148
	v_pk_fma_f32 v[124:125], v[4:5], v[104:105], v[106:107] op_sel:[1,1,0] op_sel_hi:[0,1,1] neg_hi:[1,0,0]
	s_waitcnt vmcnt(42)
	v_pk_add_f32 v[4:5], v[26:27], v[58:59] neg_lo:[0,1] neg_hi:[0,1]
	v_mov_b64_e32 v[106:107], s[12:13]
	v_pk_mul_f32 v[108:109], v[4:5], v[106:107] op_sel_hi:[1,0]
	v_cndmask_b32_e32 v38, 0, v205, vcc
	v_pk_fma_f32 v[132:133], v[4:5], v[106:107], v[108:109] op_sel:[1,1,0] op_sel_hi:[0,1,1] neg_hi:[1,0,0]
	s_waitcnt vmcnt(38)
	v_pk_add_f32 v[108:109], v[30:31], v[62:63] neg_lo:[0,1] neg_hi:[0,1]
	v_mov_b64_e32 v[4:5], s[14:15]
	v_pk_mul_f32 v[136:137], v[108:109], v[4:5] op_sel_hi:[1,0]
	v_pk_add_f32 v[110:111], v[6:7], v[38:39]
	v_pk_add_f32 v[126:127], v[54:55], v[22:23]
	v_pk_add_f32 v[130:131], v[58:59], v[26:27]
	v_pk_fma_f32 v[136:137], v[108:109], v[4:5], v[136:137] op_sel:[1,1,0] op_sel_hi:[0,1,1] neg_hi:[1,0,0]
	s_waitcnt vmcnt(34)
	v_pk_add_f32 v[140:141], v[34:35], v[66:67] neg_lo:[0,1] neg_hi:[0,1]
	v_mov_b64_e32 v[108:109], s[16:17]
	v_pk_mul_f32 v[142:143], v[140:141], v[108:109] op_sel_hi:[1,0]
	v_pk_add_f32 v[112:113], v[6:7], v[38:39] neg_lo:[0,1] neg_hi:[0,1]
	v_pk_add_f32 v[118:119], v[46:47], v[14:15]
	v_pk_add_f32 v[122:123], v[50:51], v[18:19]
	v_pk_add_f32 v[134:135], v[62:63], v[30:31]
	v_pk_add_f32 v[138:139], v[66:67], v[34:35]
	v_pk_fma_f32 v[140:141], v[140:141], v[108:109], v[142:143] op_sel:[1,1,0] op_sel_hi:[0,1,1] neg_hi:[1,0,0]
	v_pk_add_f32 v[142:143], v[126:127], v[110:111]
	v_pk_add_f32 v[110:111], v[110:111], v[126:127] neg_lo:[0,1] neg_hi:[0,1]
	v_pk_add_f32 v[126:127], v[114:115], v[130:131]
	v_pk_add_f32 v[114:115], v[114:115], v[130:131] neg_lo:[0,1] neg_hi:[0,1]
	v_cvt_f32_i32_e32 v38, v148
	v_pk_mul_f32 v[130:131], v[114:115], v[2:3] op_sel_hi:[1,0]
	v_pk_add_f32 v[128:129], v[22:23], v[54:55] op_sel:[1,1] op_sel_hi:[0,0] neg_lo:[0,1] neg_hi:[1,0]
	v_and_b32_e32 v149, -8, v148
	v_pk_fma_f32 v[114:115], v[114:115], v[2:3], v[130:131] op_sel:[1,1,0] op_sel_hi:[0,1,1] neg_hi:[1,0,0]
	v_pk_add_f32 v[130:131], v[118:119], v[134:135]
	v_pk_add_f32 v[118:119], v[118:119], v[134:135] op_sel:[1,1] op_sel_hi:[0,0] neg_lo:[0,1] neg_hi:[1,0]
	v_pk_add_f32 v[134:135], v[122:123], v[138:139]
	v_pk_add_f32 v[122:123], v[122:123], v[138:139] neg_lo:[0,1] neg_hi:[0,1]
	v_mul_f32_e32 v38, 0x38800000, v38
	v_pk_mul_f32 v[138:139], v[122:123], v[4:5] op_sel_hi:[1,0]
	v_cos_f32_e32 v144, v38
	v_pk_fma_f32 v[122:123], v[122:123], v[4:5], v[138:139] op_sel:[1,1,0] op_sel_hi:[0,1,1] neg_hi:[1,0,0]
	v_pk_add_f32 v[138:139], v[112:113], v[128:129]
	v_pk_add_f32 v[112:113], v[112:113], v[128:129] neg_lo:[0,1] neg_hi:[0,1]
	v_pk_add_f32 v[128:129], v[116:117], v[132:133]
	v_pk_add_f32 v[116:117], v[116:117], v[132:133] neg_lo:[0,1] neg_hi:[0,1]
	v_sin_f32_e32 v145, v38
	v_pk_mul_f32 v[132:133], v[116:117], v[2:3] op_sel_hi:[1,0]
	v_lshlrev_b32_e32 v38, 3, v148
	v_pk_fma_f32 v[116:117], v[116:117], v[2:3], v[132:133] op_sel:[1,1,0] op_sel_hi:[0,1,1] neg_hi:[1,0,0]
	v_pk_add_f32 v[132:133], v[120:121], v[136:137]
	v_pk_add_f32 v[120:121], v[120:121], v[136:137] op_sel:[1,1] op_sel_hi:[0,0] neg_lo:[0,1] neg_hi:[1,0]
	v_pk_add_f32 v[136:137], v[124:125], v[140:141]
	v_pk_add_f32 v[124:125], v[124:125], v[140:141] neg_lo:[0,1] neg_hi:[0,1]
	s_mov_b64 s[84:85], -1
	v_pk_mul_f32 v[140:141], v[124:125], v[4:5] op_sel_hi:[1,0]
	s_mov_b32 s86, 0
	v_pk_fma_f32 v[124:125], v[124:125], v[4:5], v[140:141] op_sel:[1,1,0] op_sel_hi:[0,1,1] neg_hi:[1,0,0]
	v_pk_add_f32 v[140:141], v[130:131], v[142:143]
	v_pk_add_f32 v[130:131], v[142:143], v[130:131] neg_lo:[0,1] neg_hi:[0,1]
	v_pk_add_f32 v[142:143], v[126:127], v[134:135]
	v_pk_add_f32 v[126:127], v[126:127], v[134:135] op_sel:[1,1] op_sel_hi:[0,0] neg_lo:[0,1] neg_hi:[1,0]
	v_pk_add_f32 v[134:135], v[110:111], v[118:119]
	v_pk_add_f32 v[110:111], v[110:111], v[118:119] neg_lo:[0,1] neg_hi:[0,1]
	v_pk_add_f32 v[118:119], v[114:115], v[122:123]
	v_pk_add_f32 v[114:115], v[114:115], v[122:123] op_sel:[1,1] op_sel_hi:[0,0] neg_lo:[0,1] neg_hi:[1,0]
	v_pk_add_f32 v[122:123], v[138:139], v[132:133]
	v_pk_add_f32 v[132:133], v[138:139], v[132:133] neg_lo:[0,1] neg_hi:[0,1]
	v_pk_add_f32 v[138:139], v[128:129], v[136:137]
	v_pk_add_f32 v[128:129], v[128:129], v[136:137] op_sel:[1,1] op_sel_hi:[0,0] neg_lo:[0,1] neg_hi:[1,0]
	v_pk_add_f32 v[136:137], v[112:113], v[120:121]
	v_pk_add_f32 v[112:113], v[112:113], v[120:121] neg_lo:[0,1] neg_hi:[0,1]
	v_pk_add_f32 v[120:121], v[116:117], v[124:125]
	v_pk_add_f32 v[116:117], v[116:117], v[124:125] op_sel:[1,1] op_sel_hi:[0,0] neg_lo:[0,1] neg_hi:[1,0]
	v_pk_add_f32 v[124:125], v[142:143], v[140:141]
	v_pk_add_f32 v[140:141], v[140:141], v[142:143] neg_lo:[0,1] neg_hi:[0,1]
	v_pk_add_f32 v[142:143], v[130:131], v[126:127]
	v_pk_add_f32 v[126:127], v[130:131], v[126:127] neg_lo:[0,1] neg_hi:[0,1]
	v_pk_add_f32 v[130:131], v[134:135], v[118:119]
	v_pk_add_f32 v[118:119], v[134:135], v[118:119] neg_lo:[0,1] neg_hi:[0,1]
	v_pk_add_f32 v[134:135], v[110:111], v[114:115]
	v_pk_add_f32 v[110:111], v[110:111], v[114:115] neg_lo:[0,1] neg_hi:[0,1]
	v_pk_add_f32 v[114:115], v[122:123], v[138:139]
	v_pk_add_f32 v[122:123], v[122:123], v[138:139] neg_lo:[0,1] neg_hi:[0,1]
	v_pk_add_f32 v[138:139], v[132:133], v[128:129]
	v_pk_add_f32 v[128:129], v[132:133], v[128:129] neg_lo:[0,1] neg_hi:[0,1]
	v_pk_add_f32 v[132:133], v[136:137], v[120:121]
	v_pk_add_f32 v[120:121], v[136:137], v[120:121] neg_lo:[0,1] neg_hi:[0,1]
	v_pk_add_f32 v[136:137], v[112:113], v[116:117]
	v_pk_add_f32 v[112:113], v[112:113], v[116:117] neg_lo:[0,1] neg_hi:[0,1]
	v_pk_mul_f32 v[116:117], v[114:115], v[144:145] op_sel_hi:[1,0]
	v_pk_fma_f32 v[114:115], v[114:115], v[144:145], v[116:117] op_sel:[1,1,0] op_sel_hi:[0,1,1] neg_hi:[1,0,0]
	v_pk_mul_f32 v[116:117], v[144:145], v[144:145] op_sel_hi:[1,0]
	v_pk_fma_f32 v[116:117], v[144:145], v[144:145], v[116:117] op_sel:[1,1,0] op_sel_hi:[0,1,1] neg_lo:[1,0,0]
	v_pk_mul_f32 v[146:147], v[130:131], v[116:117] op_sel_hi:[1,0]
	v_pk_fma_f32 v[130:131], v[130:131], v[116:117], v[146:147] op_sel:[1,1,0] op_sel_hi:[0,1,1] neg_hi:[1,0,0]
	v_pk_mul_f32 v[146:147], v[116:117], v[144:145] op_sel_hi:[1,0]
	v_pk_fma_f32 v[116:117], v[116:117], v[144:145], v[146:147] op_sel:[1,1,0] op_sel_hi:[0,1,1] neg_lo:[1,0,0]
	v_pk_mul_f32 v[146:147], v[132:133], v[116:117] op_sel_hi:[1,0]
	v_pk_fma_f32 v[132:133], v[132:133], v[116:117], v[146:147] op_sel:[1,1,0] op_sel_hi:[0,1,1] neg_hi:[1,0,0]
	v_pk_mul_f32 v[146:147], v[116:117], v[144:145] op_sel_hi:[1,0]
	v_pk_fma_f32 v[116:117], v[116:117], v[144:145], v[146:147] op_sel:[1,1,0] op_sel_hi:[0,1,1] neg_lo:[1,0,0]
	v_pk_mul_f32 v[146:147], v[142:143], v[116:117] op_sel_hi:[1,0]
	v_pk_fma_f32 v[142:143], v[142:143], v[116:117], v[146:147] op_sel:[1,1,0] op_sel_hi:[0,1,1] neg_hi:[1,0,0]
	v_pk_mul_f32 v[146:147], v[116:117], v[144:145] op_sel_hi:[1,0]
	v_pk_fma_f32 v[116:117], v[116:117], v[144:145], v[146:147] op_sel:[1,1,0] op_sel_hi:[0,1,1] neg_lo:[1,0,0]
	v_pk_mul_f32 v[146:147], v[138:139], v[116:117] op_sel_hi:[1,0]
	v_pk_fma_f32 v[138:139], v[138:139], v[116:117], v[146:147] op_sel:[1,1,0] op_sel_hi:[0,1,1] neg_hi:[1,0,0]
	v_pk_mul_f32 v[146:147], v[116:117], v[144:145] op_sel_hi:[1,0]
	v_pk_fma_f32 v[116:117], v[116:117], v[144:145], v[146:147] op_sel:[1,1,0] op_sel_hi:[0,1,1] neg_lo:[1,0,0]
	v_pk_mul_f32 v[146:147], v[134:135], v[116:117] op_sel_hi:[1,0]
	v_pk_fma_f32 v[134:135], v[134:135], v[116:117], v[146:147] op_sel:[1,1,0] op_sel_hi:[0,1,1] neg_hi:[1,0,0]
	v_pk_mul_f32 v[146:147], v[116:117], v[144:145] op_sel_hi:[1,0]
	v_pk_fma_f32 v[116:117], v[116:117], v[144:145], v[146:147] op_sel:[1,1,0] op_sel_hi:[0,1,1] neg_lo:[1,0,0]
	v_pk_mul_f32 v[146:147], v[136:137], v[116:117] op_sel_hi:[1,0]
	v_pk_fma_f32 v[136:137], v[136:137], v[116:117], v[146:147] op_sel:[1,1,0] op_sel_hi:[0,1,1] neg_hi:[1,0,0]
	v_pk_mul_f32 v[146:147], v[116:117], v[144:145] op_sel_hi:[1,0]
	v_pk_fma_f32 v[116:117], v[116:117], v[144:145], v[146:147] op_sel:[1,1,0] op_sel_hi:[0,1,1] neg_lo:[1,0,0]
	v_pk_mul_f32 v[146:147], v[140:141], v[116:117] op_sel_hi:[1,0]
	v_pk_fma_f32 v[140:141], v[140:141], v[116:117], v[146:147] op_sel:[1,1,0] op_sel_hi:[0,1,1] neg_hi:[1,0,0]
	v_pk_mul_f32 v[146:147], v[116:117], v[144:145] op_sel_hi:[1,0]
	v_pk_fma_f32 v[116:117], v[116:117], v[144:145], v[146:147] op_sel:[1,1,0] op_sel_hi:[0,1,1] neg_lo:[1,0,0]
	v_pk_mul_f32 v[146:147], v[122:123], v[116:117] op_sel_hi:[1,0]
	v_pk_fma_f32 v[122:123], v[122:123], v[116:117], v[146:147] op_sel:[1,1,0] op_sel_hi:[0,1,1] neg_hi:[1,0,0]
	v_pk_mul_f32 v[146:147], v[116:117], v[144:145] op_sel_hi:[1,0]
	v_pk_fma_f32 v[116:117], v[116:117], v[144:145], v[146:147] op_sel:[1,1,0] op_sel_hi:[0,1,1] neg_lo:[1,0,0]
	v_pk_mul_f32 v[146:147], v[118:119], v[116:117] op_sel_hi:[1,0]
	v_pk_fma_f32 v[118:119], v[118:119], v[116:117], v[146:147] op_sel:[1,1,0] op_sel_hi:[0,1,1] neg_hi:[1,0,0]
	v_pk_mul_f32 v[146:147], v[116:117], v[144:145] op_sel_hi:[1,0]
	v_pk_fma_f32 v[116:117], v[116:117], v[144:145], v[146:147] op_sel:[1,1,0] op_sel_hi:[0,1,1] neg_lo:[1,0,0]
	v_pk_mul_f32 v[146:147], v[120:121], v[116:117] op_sel_hi:[1,0]
	v_pk_fma_f32 v[120:121], v[120:121], v[116:117], v[146:147] op_sel:[1,1,0] op_sel_hi:[0,1,1] neg_hi:[1,0,0]
	v_pk_mul_f32 v[146:147], v[116:117], v[144:145] op_sel_hi:[1,0]
	v_pk_fma_f32 v[116:117], v[116:117], v[144:145], v[146:147] op_sel:[1,1,0] op_sel_hi:[0,1,1] neg_lo:[1,0,0]
	v_pk_mul_f32 v[146:147], v[126:127], v[116:117] op_sel_hi:[1,0]
	v_pk_fma_f32 v[126:127], v[126:127], v[116:117], v[146:147] op_sel:[1,1,0] op_sel_hi:[0,1,1] neg_hi:[1,0,0]
	v_pk_mul_f32 v[146:147], v[116:117], v[144:145] op_sel_hi:[1,0]
	v_pk_fma_f32 v[116:117], v[116:117], v[144:145], v[146:147] op_sel:[1,1,0] op_sel_hi:[0,1,1] neg_lo:[1,0,0]
	v_pk_mul_f32 v[146:147], v[128:129], v[116:117] op_sel_hi:[1,0]
	v_pk_fma_f32 v[128:129], v[128:129], v[116:117], v[146:147] op_sel:[1,1,0] op_sel_hi:[0,1,1] neg_hi:[1,0,0]
	v_pk_mul_f32 v[146:147], v[116:117], v[144:145] op_sel_hi:[1,0]
	v_pk_fma_f32 v[116:117], v[116:117], v[144:145], v[146:147] op_sel:[1,1,0] op_sel_hi:[0,1,1] neg_lo:[1,0,0]
	v_pk_mul_f32 v[146:147], v[110:111], v[116:117] op_sel_hi:[1,0]
	v_pk_fma_f32 v[110:111], v[110:111], v[116:117], v[146:147] op_sel:[1,1,0] op_sel_hi:[0,1,1] neg_hi:[1,0,0]
	v_pk_mul_f32 v[146:147], v[116:117], v[144:145] op_sel_hi:[1,0]
	v_pk_fma_f32 v[116:117], v[116:117], v[144:145], v[146:147] op_sel:[1,1,0] op_sel_hi:[0,1,1] neg_lo:[1,0,0]
	v_pk_mul_f32 v[144:145], v[112:113], v[116:117] op_sel_hi:[1,0]
	v_pk_fma_f32 v[112:113], v[112:113], v[116:117], v[144:145] op_sel:[1,1,0] op_sel_hi:[0,1,1] neg_hi:[1,0,0]
	v_add3_u32 v116, 0, v149, v38
	ds_write2st64_b64 v116, v[124:125], v[114:115] offset1:18
	ds_write2st64_b64 v116, v[130:131], v[132:133] offset0:36 offset1:54
	ds_write2st64_b64 v116, v[142:143], v[138:139] offset0:72 offset1:90
	ds_write2st64_b64 v116, v[134:135], v[136:137] offset0:108 offset1:126
	v_add_u32_e32 v114, 0x12000, v116
	ds_write_b64 v114, v[140:141]
	v_add_u32_e32 v114, 0x14400, v116
	ds_write_b64 v114, v[122:123]
	v_add_u32_e32 v114, 0x16800, v116
	ds_write_b64 v114, v[118:119]
	v_add_u32_e32 v114, 0x18c00, v116
	ds_write_b64 v114, v[120:121]
	v_add_u32_e32 v114, 0x1b000, v116
	ds_write_b64 v114, v[126:127]
	v_add_u32_e32 v114, 0x1d400, v116
	ds_write_b64 v114, v[128:129]
	v_add_u32_e32 v114, 0x1f800, v116
	ds_write_b64 v114, v[110:111]
	v_add_u32_e32 v110, 0x21c00, v116
	v_pk_add_f32 v[116:117], v[12:13], v[44:45] neg_lo:[0,1] neg_hi:[0,1]
	v_pk_add_f32 v[122:123], v[20:21], v[52:53] neg_lo:[0,1] neg_hi:[0,1]
	v_pk_mul_f32 v[118:119], v[116:117], v[102:103] op_sel_hi:[1,0]
	v_pk_add_f32 v[128:129], v[28:29], v[60:61] neg_lo:[0,1] neg_hi:[0,1]
	ds_write_b64 v110, v[112:113]
	v_pk_mul_f32 v[130:131], v[128:129], v[106:107] op_sel_hi:[1,0]
	v_pk_add_f32 v[110:111], v[40:41], v[8:9]
	v_pk_add_f32 v[114:115], v[44:45], v[12:13]
	v_pk_fma_f32 v[102:103], v[116:117], v[102:103], v[118:119] op_sel:[1,1,0] op_sel_hi:[0,1,1] neg_hi:[1,0,0]
	v_pk_add_f32 v[118:119], v[16:17], v[48:49] neg_lo:[0,1] neg_hi:[0,1]
	v_pk_mul_f32 v[124:125], v[122:123], v[104:105] op_sel_hi:[1,0]
	v_pk_add_f32 v[126:127], v[60:61], v[28:29]
	v_pk_mul_f32 v[120:121], v[118:119], v[2:3] op_sel_hi:[1,0]
	v_pk_fma_f32 v[104:105], v[122:123], v[104:105], v[124:125] op_sel:[1,1,0] op_sel_hi:[0,1,1] neg_hi:[1,0,0]
	v_pk_add_f32 v[122:123], v[56:57], v[24:25]
	v_pk_fma_f32 v[106:107], v[128:129], v[106:107], v[130:131] op_sel:[1,1,0] op_sel_hi:[0,1,1] neg_hi:[1,0,0]
	v_pk_add_f32 v[130:131], v[32:33], v[64:65] neg_lo:[0,1] neg_hi:[0,1]
	s_waitcnt vmcnt(32)
	v_pk_add_f32 v[134:135], v[36:37], v[68:69] neg_lo:[0,1] neg_hi:[0,1]
	v_pk_mul_f32 v[132:133], v[130:131], v[4:5] op_sel_hi:[1,0]
	v_pk_add_f32 v[116:117], v[48:49], v[16:17]
	v_pk_fma_f32 v[118:119], v[118:119], v[2:3], v[120:121] op_sel:[1,1,0] op_sel_hi:[0,1,1] neg_hi:[1,0,0]
	v_pk_add_f32 v[120:121], v[52:53], v[20:21]
	v_pk_add_f32 v[128:129], v[64:65], v[32:33]
	v_pk_fma_f32 v[130:131], v[130:131], v[4:5], v[132:133] op_sel:[1,1,0] op_sel_hi:[0,1,1] neg_hi:[1,0,0]
	v_pk_add_f32 v[132:133], v[68:69], v[36:37]
	v_pk_mul_f32 v[136:137], v[134:135], v[108:109] op_sel_hi:[1,0]
	v_pk_add_f32 v[112:113], v[8:9], v[40:41] neg_lo:[0,1] neg_hi:[0,1]
	v_pk_fma_f32 v[108:109], v[134:135], v[108:109], v[136:137] op_sel:[1,1,0] op_sel_hi:[0,1,1] neg_hi:[1,0,0]
	v_pk_add_f32 v[134:135], v[110:111], v[122:123]
	v_pk_add_f32 v[110:111], v[110:111], v[122:123] neg_lo:[0,1] neg_hi:[0,1]
	v_pk_add_f32 v[122:123], v[114:115], v[126:127]
	v_pk_add_f32 v[114:115], v[114:115], v[126:127] neg_lo:[0,1] neg_hi:[0,1]
	v_pk_add_f32 v[124:125], v[24:25], v[56:57] op_sel:[1,1] op_sel_hi:[0,0] neg_lo:[0,1] neg_hi:[1,0]
	v_add_u32_e32 v138, 0x200, v148
	v_pk_mul_f32 v[126:127], v[114:115], v[2:3] op_sel_hi:[1,0]
	v_and_b32_e32 v139, -8, v138
	v_pk_fma_f32 v[114:115], v[114:115], v[2:3], v[126:127] op_sel:[1,1,0] op_sel_hi:[0,1,1] neg_hi:[1,0,0]
	v_pk_add_f32 v[126:127], v[116:117], v[128:129]
	v_pk_add_f32 v[116:117], v[116:117], v[128:129] op_sel:[1,1] op_sel_hi:[0,0] neg_lo:[0,1] neg_hi:[1,0]
	v_pk_add_f32 v[128:129], v[120:121], v[132:133]
	v_pk_add_f32 v[120:121], v[120:121], v[132:133] neg_lo:[0,1] neg_hi:[0,1]
	v_add3_u32 v38, 0, v139, v38
	v_pk_mul_f32 v[132:133], v[120:121], v[4:5] op_sel_hi:[1,0]
	v_pk_fma_f32 v[120:121], v[120:121], v[4:5], v[132:133] op_sel:[1,1,0] op_sel_hi:[0,1,1] neg_hi:[1,0,0]
	v_pk_add_f32 v[132:133], v[112:113], v[124:125]
	v_pk_add_f32 v[112:113], v[112:113], v[124:125] neg_lo:[0,1] neg_hi:[0,1]
	v_pk_add_f32 v[124:125], v[102:103], v[106:107]
	v_pk_add_f32 v[102:103], v[102:103], v[106:107] neg_lo:[0,1] neg_hi:[0,1]
	s_nop 0
	v_pk_mul_f32 v[106:107], v[102:103], v[2:3] op_sel_hi:[1,0]
	v_pk_fma_f32 v[2:3], v[102:103], v[2:3], v[106:107] op_sel:[1,1,0] op_sel_hi:[0,1,1] neg_hi:[1,0,0]
	v_pk_add_f32 v[102:103], v[118:119], v[130:131]
	v_pk_add_f32 v[106:107], v[118:119], v[130:131] op_sel:[1,1] op_sel_hi:[0,0] neg_lo:[0,1] neg_hi:[1,0]
	v_pk_add_f32 v[118:119], v[104:105], v[108:109]
	v_pk_add_f32 v[104:105], v[104:105], v[108:109] neg_lo:[0,1] neg_hi:[0,1]
	v_pk_add_f32 v[130:131], v[124:125], v[118:119]
	v_pk_mul_f32 v[108:109], v[104:105], v[4:5] op_sel_hi:[1,0]
	v_pk_add_f32 v[118:119], v[124:125], v[118:119] op_sel:[1,1] op_sel_hi:[0,0] neg_lo:[0,1] neg_hi:[1,0]
	v_pk_add_f32 v[124:125], v[112:113], v[106:107]
	v_pk_fma_f32 v[4:5], v[104:105], v[4:5], v[108:109] op_sel:[1,1,0] op_sel_hi:[0,1,1] neg_hi:[1,0,0]
	v_pk_add_f32 v[104:105], v[134:135], v[126:127]
	v_pk_add_f32 v[108:109], v[134:135], v[126:127] neg_lo:[0,1] neg_hi:[0,1]
	v_pk_add_f32 v[126:127], v[122:123], v[128:129]
	v_pk_add_f32 v[122:123], v[122:123], v[128:129] op_sel:[1,1] op_sel_hi:[0,0] neg_lo:[0,1] neg_hi:[1,0]
	v_pk_add_f32 v[128:129], v[110:111], v[116:117]
	v_pk_add_f32 v[110:111], v[110:111], v[116:117] neg_lo:[0,1] neg_hi:[0,1]
	v_pk_add_f32 v[116:117], v[114:115], v[120:121]
	v_pk_add_f32 v[114:115], v[114:115], v[120:121] op_sel:[1,1] op_sel_hi:[0,0] neg_lo:[0,1] neg_hi:[1,0]
	v_pk_add_f32 v[120:121], v[132:133], v[102:103]
	v_pk_add_f32 v[102:103], v[132:133], v[102:103] neg_lo:[0,1] neg_hi:[0,1]
	v_cvt_f32_i32_e32 v132, v138
	v_pk_add_f32 v[106:107], v[112:113], v[106:107] neg_lo:[0,1] neg_hi:[0,1]
	v_pk_add_f32 v[112:113], v[2:3], v[4:5]
	v_pk_add_f32 v[2:3], v[2:3], v[4:5] op_sel:[1,1] op_sel_hi:[0,0] neg_lo:[0,1] neg_hi:[1,0]
	v_mul_f32_e32 v133, 0x38800000, v132
	v_pk_add_f32 v[4:5], v[104:105], v[126:127]
	v_pk_add_f32 v[104:105], v[104:105], v[126:127] neg_lo:[0,1] neg_hi:[0,1]
	v_pk_add_f32 v[126:127], v[108:109], v[122:123]
	v_pk_add_f32 v[108:109], v[108:109], v[122:123] neg_lo:[0,1] neg_hi:[0,1]
	v_pk_add_f32 v[122:123], v[128:129], v[116:117]
	v_pk_add_f32 v[116:117], v[128:129], v[116:117] neg_lo:[0,1] neg_hi:[0,1]
	v_pk_add_f32 v[128:129], v[110:111], v[114:115]
	v_pk_add_f32 v[110:111], v[110:111], v[114:115] neg_lo:[0,1] neg_hi:[0,1]
	v_pk_add_f32 v[114:115], v[120:121], v[130:131]
	v_pk_add_f32 v[120:121], v[120:121], v[130:131] neg_lo:[0,1] neg_hi:[0,1]
	v_pk_add_f32 v[130:131], v[102:103], v[118:119]
	v_pk_add_f32 v[102:103], v[102:103], v[118:119] neg_lo:[0,1] neg_hi:[0,1]
	v_pk_add_f32 v[118:119], v[124:125], v[112:113]
	v_cos_f32_e32 v132, v133
	v_sin_f32_e32 v133, v133
	v_pk_add_f32 v[112:113], v[124:125], v[112:113] neg_lo:[0,1] neg_hi:[0,1]
	v_pk_add_f32 v[124:125], v[106:107], v[2:3]
	v_pk_add_f32 v[2:3], v[106:107], v[2:3] neg_lo:[0,1] neg_hi:[0,1]
	v_pk_mul_f32 v[106:107], v[114:115], v[132:133] op_sel_hi:[1,0]
	v_pk_fma_f32 v[106:107], v[114:115], v[132:133], v[106:107] op_sel:[1,1,0] op_sel_hi:[0,1,1] neg_hi:[1,0,0]
	v_pk_mul_f32 v[114:115], v[132:133], v[132:133] op_sel_hi:[1,0]
	v_pk_fma_f32 v[114:115], v[132:133], v[132:133], v[114:115] op_sel:[1,1,0] op_sel_hi:[0,1,1] neg_lo:[1,0,0]
	v_pk_mul_f32 v[134:135], v[122:123], v[114:115] op_sel_hi:[1,0]
	v_pk_fma_f32 v[122:123], v[122:123], v[114:115], v[134:135] op_sel:[1,1,0] op_sel_hi:[0,1,1] neg_hi:[1,0,0]
	v_pk_mul_f32 v[134:135], v[114:115], v[132:133] op_sel_hi:[1,0]
	v_pk_fma_f32 v[114:115], v[114:115], v[132:133], v[134:135] op_sel:[1,1,0] op_sel_hi:[0,1,1] neg_lo:[1,0,0]
	v_pk_mul_f32 v[134:135], v[118:119], v[114:115] op_sel_hi:[1,0]
	v_pk_fma_f32 v[118:119], v[118:119], v[114:115], v[134:135] op_sel:[1,1,0] op_sel_hi:[0,1,1] neg_hi:[1,0,0]
	v_pk_mul_f32 v[134:135], v[114:115], v[132:133] op_sel_hi:[1,0]
	v_pk_fma_f32 v[114:115], v[114:115], v[132:133], v[134:135] op_sel:[1,1,0] op_sel_hi:[0,1,1] neg_lo:[1,0,0]
	v_pk_mul_f32 v[134:135], v[126:127], v[114:115] op_sel_hi:[1,0]
	v_pk_fma_f32 v[126:127], v[126:127], v[114:115], v[134:135] op_sel:[1,1,0] op_sel_hi:[0,1,1] neg_hi:[1,0,0]
	v_pk_mul_f32 v[134:135], v[114:115], v[132:133] op_sel_hi:[1,0]
	v_pk_fma_f32 v[114:115], v[114:115], v[132:133], v[134:135] op_sel:[1,1,0] op_sel_hi:[0,1,1] neg_lo:[1,0,0]
	v_pk_mul_f32 v[134:135], v[130:131], v[114:115] op_sel_hi:[1,0]
	v_pk_fma_f32 v[130:131], v[130:131], v[114:115], v[134:135] op_sel:[1,1,0] op_sel_hi:[0,1,1] neg_hi:[1,0,0]
	v_pk_mul_f32 v[134:135], v[114:115], v[132:133] op_sel_hi:[1,0]
	v_pk_fma_f32 v[114:115], v[114:115], v[132:133], v[134:135] op_sel:[1,1,0] op_sel_hi:[0,1,1] neg_lo:[1,0,0]
	v_pk_mul_f32 v[134:135], v[128:129], v[114:115] op_sel_hi:[1,0]
	v_pk_fma_f32 v[128:129], v[128:129], v[114:115], v[134:135] op_sel:[1,1,0] op_sel_hi:[0,1,1] neg_hi:[1,0,0]
	v_pk_mul_f32 v[134:135], v[114:115], v[132:133] op_sel_hi:[1,0]
	v_pk_fma_f32 v[114:115], v[114:115], v[132:133], v[134:135] op_sel:[1,1,0] op_sel_hi:[0,1,1] neg_lo:[1,0,0]
	v_pk_mul_f32 v[134:135], v[124:125], v[114:115] op_sel_hi:[1,0]
	v_pk_fma_f32 v[124:125], v[124:125], v[114:115], v[134:135] op_sel:[1,1,0] op_sel_hi:[0,1,1] neg_hi:[1,0,0]
	v_pk_mul_f32 v[134:135], v[114:115], v[132:133] op_sel_hi:[1,0]
	v_pk_fma_f32 v[114:115], v[114:115], v[132:133], v[134:135] op_sel:[1,1,0] op_sel_hi:[0,1,1] neg_lo:[1,0,0]
	v_pk_mul_f32 v[134:135], v[104:105], v[114:115] op_sel_hi:[1,0]
	v_pk_fma_f32 v[104:105], v[104:105], v[114:115], v[134:135] op_sel:[1,1,0] op_sel_hi:[0,1,1] neg_hi:[1,0,0]
	v_pk_mul_f32 v[134:135], v[114:115], v[132:133] op_sel_hi:[1,0]
	v_pk_fma_f32 v[114:115], v[114:115], v[132:133], v[134:135] op_sel:[1,1,0] op_sel_hi:[0,1,1] neg_lo:[1,0,0]
	v_pk_mul_f32 v[134:135], v[120:121], v[114:115] op_sel_hi:[1,0]
	v_pk_fma_f32 v[120:121], v[120:121], v[114:115], v[134:135] op_sel:[1,1,0] op_sel_hi:[0,1,1] neg_hi:[1,0,0]
	v_pk_mul_f32 v[134:135], v[114:115], v[132:133] op_sel_hi:[1,0]
	v_pk_fma_f32 v[114:115], v[114:115], v[132:133], v[134:135] op_sel:[1,1,0] op_sel_hi:[0,1,1] neg_lo:[1,0,0]
	v_pk_mul_f32 v[134:135], v[116:117], v[114:115] op_sel_hi:[1,0]
	v_pk_fma_f32 v[116:117], v[116:117], v[114:115], v[134:135] op_sel:[1,1,0] op_sel_hi:[0,1,1] neg_hi:[1,0,0]
	v_pk_mul_f32 v[134:135], v[114:115], v[132:133] op_sel_hi:[1,0]
	v_pk_fma_f32 v[114:115], v[114:115], v[132:133], v[134:135] op_sel:[1,1,0] op_sel_hi:[0,1,1] neg_lo:[1,0,0]
	v_pk_mul_f32 v[134:135], v[112:113], v[114:115] op_sel_hi:[1,0]
	v_pk_fma_f32 v[112:113], v[112:113], v[114:115], v[134:135] op_sel:[1,1,0] op_sel_hi:[0,1,1] neg_hi:[1,0,0]
	v_pk_mul_f32 v[134:135], v[114:115], v[132:133] op_sel_hi:[1,0]
	v_pk_fma_f32 v[114:115], v[114:115], v[132:133], v[134:135] op_sel:[1,1,0] op_sel_hi:[0,1,1] neg_lo:[1,0,0]
	v_pk_mul_f32 v[134:135], v[108:109], v[114:115] op_sel_hi:[1,0]
	v_pk_fma_f32 v[108:109], v[108:109], v[114:115], v[134:135] op_sel:[1,1,0] op_sel_hi:[0,1,1] neg_hi:[1,0,0]
	v_pk_mul_f32 v[134:135], v[114:115], v[132:133] op_sel_hi:[1,0]
	v_pk_fma_f32 v[114:115], v[114:115], v[132:133], v[134:135] op_sel:[1,1,0] op_sel_hi:[0,1,1] neg_lo:[1,0,0]
	v_pk_mul_f32 v[134:135], v[102:103], v[114:115] op_sel_hi:[1,0]
	v_pk_fma_f32 v[102:103], v[102:103], v[114:115], v[134:135] op_sel:[1,1,0] op_sel_hi:[0,1,1] neg_hi:[1,0,0]
	v_pk_mul_f32 v[134:135], v[114:115], v[132:133] op_sel_hi:[1,0]
	v_pk_fma_f32 v[114:115], v[114:115], v[132:133], v[134:135] op_sel:[1,1,0] op_sel_hi:[0,1,1] neg_lo:[1,0,0]
	v_pk_mul_f32 v[134:135], v[110:111], v[114:115] op_sel_hi:[1,0]
	v_pk_fma_f32 v[110:111], v[110:111], v[114:115], v[134:135] op_sel:[1,1,0] op_sel_hi:[0,1,1] neg_hi:[1,0,0]
	v_pk_mul_f32 v[134:135], v[114:115], v[132:133] op_sel_hi:[1,0]
	v_pk_fma_f32 v[114:115], v[114:115], v[132:133], v[134:135] op_sel:[1,1,0] op_sel_hi:[0,1,1] neg_lo:[1,0,0]
	v_pk_mul_f32 v[132:133], v[2:3], v[114:115] op_sel_hi:[1,0]
	v_pk_fma_f32 v[2:3], v[2:3], v[114:115], v[132:133] op_sel:[1,1,0] op_sel_hi:[0,1,1] neg_hi:[1,0,0]
	v_add_u32_e32 v114, 0x1000, v38
	ds_write2st64_b64 v38, v[4:5], v[106:107] offset0:8 offset1:26
	ds_write2st64_b64 v38, v[122:123], v[118:119] offset0:44 offset1:62
	ds_write2st64_b64 v38, v[126:127], v[130:131] offset0:80 offset1:98
	ds_write_b64 v38, v[128:129] offset:59392
	ds_write_b64 v114, v[124:125] offset:64512
	v_add_u32_e32 v4, 0x13000, v38
	ds_write_b64 v4, v[104:105]
	v_add_u32_e32 v4, 0x15400, v38
	ds_write_b64 v4, v[120:121]
	v_add_u32_e32 v4, 0x17800, v38
	ds_write_b64 v4, v[116:117]
	v_add_u32_e32 v4, 0x19c00, v38
	ds_write_b64 v4, v[112:113]
	v_add_u32_e32 v4, 0x1c000, v38
	ds_write_b64 v4, v[108:109]
	v_add_u32_e32 v4, 0x1e400, v38
	ds_write_b64 v4, v[102:103]
	v_add_u32_e32 v4, 0x20800, v38
	ds_write_b64 v4, v[110:111]
	v_add_u32_e32 v4, 0x22c00, v38
	ds_write_b64 v4, v[2:3]
	v_mov_b32_e32 v4, v204
	s_waitcnt lgkmcnt(0)
	s_barrier
	s_nop 0
	v_and_b32_e32 v38, 63, v4
	v_cvt_f32_ubyte0_e32 v2, v38
	v_mul_f32_e32 v3, 0x3a800000, v2
	v_cos_f32_e32 v2, v3
	v_sin_f32_e32 v3, v3
	v_lshlrev_b32_e32 v132, 4, v4
.LBB0_756:
	v_add_u32_e32 v4, s86, v132
	v_and_b32_e32 v4, 0xfffffc00, v4
	v_or_b32_e32 v5, v4, v38
	v_bitop3_b32 v4, v4, s97, v38 bitop3:0xc8
	v_lshlrev_b32_e32 v5, 3, v5
	v_add3_u32 v133, 0, v4, v5
	v_add_u32_e32 v134, 0x800, v133
	v_add_u32_e32 v135, 0x1000, v133
	ds_read2_b64 v[102:105], v133 offset1:72
	ds_read2_b64 v[106:109], v133 offset0:144 offset1:216
	ds_read2_b64 v[110:113], v134 offset0:32 offset1:104
	ds_read2_b64 v[114:117], v134 offset0:176 offset1:248
	ds_read2_b64 v[118:121], v135 offset0:64 offset1:136
	v_add_u32_e32 v136, 0x1400, v133
	ds_read2_b64 v[122:125], v136 offset0:80 offset1:152
	v_add_u32_e32 v137, 0x1800, v133
	ds_read2_b64 v[126:129], v137 offset0:96 offset1:168
	v_add_u32_e32 v138, 0x1c00, v133
	ds_read2_b64 v[140:143], v138 offset0:112 offset1:184
	s_waitcnt lgkmcnt(3)
	v_pk_add_f32 v[4:5], v[102:103], v[118:119]
	v_pk_add_f32 v[102:103], v[102:103], v[118:119] neg_lo:[0,1] neg_hi:[0,1]
	v_pk_add_f32 v[118:119], v[104:105], v[120:121]
	v_pk_add_f32 v[104:105], v[104:105], v[120:121] neg_lo:[0,1] neg_hi:[0,1]
	v_mov_b64_e32 v[120:121], s[4:5]
	v_pk_mul_f32 v[130:131], v[104:105], v[120:121] op_sel_hi:[1,0]
	s_movk_i32 s86, 0x2000
	v_pk_fma_f32 v[104:105], v[104:105], v[120:121], v[130:131] op_sel:[1,1,0] op_sel_hi:[0,1,1] neg_hi:[1,0,0]
	s_waitcnt lgkmcnt(2)
	v_pk_add_f32 v[120:121], v[106:107], v[122:123]
	v_pk_add_f32 v[106:107], v[106:107], v[122:123] neg_lo:[0,1] neg_hi:[0,1]
	v_mov_b64_e32 v[122:123], s[6:7]
	v_pk_mul_f32 v[130:131], v[106:107], v[122:123] op_sel_hi:[1,0]
	s_and_b64 vcc, exec, s[84:85]
	v_pk_fma_f32 v[106:107], v[106:107], v[122:123], v[130:131] op_sel:[1,1,0] op_sel_hi:[0,1,1] neg_hi:[1,0,0]
	v_pk_add_f32 v[130:131], v[108:109], v[124:125]
	v_pk_add_f32 v[108:109], v[108:109], v[124:125] neg_lo:[0,1] neg_hi:[0,1]
	v_mov_b64_e32 v[124:125], s[10:11]
	v_pk_mul_f32 v[144:145], v[108:109], v[124:125] op_sel_hi:[1,0]
	s_mov_b64 s[84:85], 0
	v_pk_fma_f32 v[108:109], v[108:109], v[124:125], v[144:145] op_sel:[1,1,0] op_sel_hi:[0,1,1] neg_hi:[1,0,0]
	s_waitcnt lgkmcnt(1)
	v_pk_add_f32 v[124:125], v[110:111], v[126:127]
	v_pk_add_f32 v[110:111], v[110:111], v[126:127] op_sel:[1,1] op_sel_hi:[0,0] neg_lo:[0,1] neg_hi:[1,0]
	v_pk_add_f32 v[126:127], v[112:113], v[128:129]
	v_pk_add_f32 v[112:113], v[112:113], v[128:129] neg_lo:[0,1] neg_hi:[0,1]
	v_mov_b64_e32 v[128:129], s[12:13]
	v_pk_mul_f32 v[144:145], v[112:113], v[128:129] op_sel_hi:[1,0]
	v_pk_fma_f32 v[112:113], v[112:113], v[128:129], v[144:145] op_sel:[1,1,0] op_sel_hi:[0,1,1] neg_hi:[1,0,0]
	s_waitcnt lgkmcnt(0)
	v_pk_add_f32 v[128:129], v[114:115], v[140:141]
	v_pk_add_f32 v[114:115], v[114:115], v[140:141] neg_lo:[0,1] neg_hi:[0,1]
	v_mov_b64_e32 v[140:141], s[14:15]
	v_pk_mul_f32 v[144:145], v[114:115], v[140:141] op_sel_hi:[1,0]
	v_pk_fma_f32 v[114:115], v[114:115], v[140:141], v[144:145] op_sel:[1,1,0] op_sel_hi:[0,1,1] neg_hi:[1,0,0]
	v_pk_add_f32 v[144:145], v[116:117], v[142:143]
	v_pk_add_f32 v[116:117], v[116:117], v[142:143] neg_lo:[0,1] neg_hi:[0,1]
	v_mov_b64_e32 v[142:143], s[16:17]
	v_pk_mul_f32 v[146:147], v[116:117], v[142:143] op_sel_hi:[1,0]
	v_pk_fma_f32 v[116:117], v[116:117], v[142:143], v[146:147] op_sel:[1,1,0] op_sel_hi:[0,1,1] neg_hi:[1,0,0]
	v_pk_add_f32 v[142:143], v[4:5], v[124:125]
	v_pk_add_f32 v[4:5], v[4:5], v[124:125] neg_lo:[0,1] neg_hi:[0,1]
	v_pk_add_f32 v[124:125], v[118:119], v[126:127]
	v_pk_add_f32 v[118:119], v[118:119], v[126:127] neg_lo:[0,1] neg_hi:[0,1]
	s_nop 0
	v_pk_mul_f32 v[126:127], v[118:119], v[122:123] op_sel_hi:[1,0]
	v_pk_fma_f32 v[118:119], v[118:119], v[122:123], v[126:127] op_sel:[1,1,0] op_sel_hi:[0,1,1] neg_hi:[1,0,0]
	v_pk_add_f32 v[126:127], v[120:121], v[128:129]
	v_pk_add_f32 v[120:121], v[120:121], v[128:129] op_sel:[1,1] op_sel_hi:[0,0] neg_lo:[0,1] neg_hi:[1,0]
	v_pk_add_f32 v[128:129], v[130:131], v[144:145]
	v_pk_add_f32 v[130:131], v[130:131], v[144:145] neg_lo:[0,1] neg_hi:[0,1]
	s_nop 0
	v_pk_mul_f32 v[144:145], v[130:131], v[140:141] op_sel_hi:[1,0]
	v_pk_fma_f32 v[130:131], v[130:131], v[140:141], v[144:145] op_sel:[1,1,0] op_sel_hi:[0,1,1] neg_hi:[1,0,0]
	v_pk_add_f32 v[144:145], v[102:103], v[110:111]
	v_pk_add_f32 v[102:103], v[102:103], v[110:111] neg_lo:[0,1] neg_hi:[0,1]
	v_pk_add_f32 v[110:111], v[104:105], v[112:113]
	v_pk_add_f32 v[104:105], v[104:105], v[112:113] neg_lo:[0,1] neg_hi:[0,1]
	s_nop 0
	v_pk_mul_f32 v[112:113], v[104:105], v[122:123] op_sel_hi:[1,0]
	v_pk_fma_f32 v[104:105], v[104:105], v[122:123], v[112:113] op_sel:[1,1,0] op_sel_hi:[0,1,1] neg_hi:[1,0,0]
	v_pk_add_f32 v[112:113], v[106:107], v[114:115]
	v_pk_add_f32 v[106:107], v[106:107], v[114:115] op_sel:[1,1] op_sel_hi:[0,0] neg_lo:[0,1] neg_hi:[1,0]
	v_pk_add_f32 v[114:115], v[108:109], v[116:117]
	v_pk_add_f32 v[108:109], v[108:109], v[116:117] neg_lo:[0,1] neg_hi:[0,1]
	v_pk_add_f32 v[122:123], v[124:125], v[128:129]
	v_pk_mul_f32 v[116:117], v[108:109], v[140:141] op_sel_hi:[1,0]
	v_pk_add_f32 v[124:125], v[124:125], v[128:129] op_sel:[1,1] op_sel_hi:[0,0] neg_lo:[0,1] neg_hi:[1,0]
	v_pk_add_f32 v[146:147], v[110:111], v[114:115]
	v_pk_fma_f32 v[108:109], v[108:109], v[140:141], v[116:117] op_sel:[1,1,0] op_sel_hi:[0,1,1] neg_hi:[1,0,0]
	v_pk_add_f32 v[116:117], v[142:143], v[126:127]
	v_pk_add_f32 v[126:127], v[142:143], v[126:127] neg_lo:[0,1] neg_hi:[0,1]
	v_pk_add_f32 v[140:141], v[4:5], v[120:121]
	v_pk_add_f32 v[142:143], v[4:5], v[120:121] neg_lo:[0,1] neg_hi:[0,1]
	v_pk_add_f32 v[120:121], v[118:119], v[130:131]
	v_pk_add_f32 v[118:119], v[118:119], v[130:131] op_sel:[1,1] op_sel_hi:[0,0] neg_lo:[0,1] neg_hi:[1,0]
	v_pk_add_f32 v[130:131], v[144:145], v[112:113]
	v_pk_add_f32 v[148:149], v[102:103], v[106:107]
	v_pk_add_f32 v[106:107], v[102:103], v[106:107] neg_lo:[0,1] neg_hi:[0,1]
	v_pk_add_f32 v[150:151], v[104:105], v[108:109]
	v_pk_add_f32 v[108:109], v[104:105], v[108:109] op_sel:[1,1] op_sel_hi:[0,0] neg_lo:[0,1] neg_hi:[1,0]
	v_pk_add_f32 v[144:145], v[144:145], v[112:113] neg_lo:[0,1] neg_hi:[0,1]
	v_pk_add_f32 v[110:111], v[110:111], v[114:115] op_sel:[1,1] op_sel_hi:[0,0] neg_lo:[0,1] neg_hi:[1,0]
	v_pk_add_f32 v[4:5], v[116:117], v[122:123]
	v_pk_add_f32 v[114:115], v[116:117], v[122:123] neg_lo:[0,1] neg_hi:[0,1]
	v_pk_add_f32 v[122:123], v[126:127], v[124:125]
	v_pk_add_f32 v[104:105], v[126:127], v[124:125] neg_lo:[0,1] neg_hi:[0,1]
	v_pk_add_f32 v[128:129], v[140:141], v[120:121]
	v_pk_add_f32 v[112:113], v[140:141], v[120:121] neg_lo:[0,1] neg_hi:[0,1]
	v_pk_add_f32 v[140:141], v[130:131], v[146:147]
	v_pk_add_f32 v[124:125], v[106:107], v[108:109]
	v_pk_add_f32 v[106:107], v[106:107], v[108:109] neg_lo:[0,1] neg_hi:[0,1]
	v_pk_mul_f32 v[108:109], v[140:141], v[2:3] op_sel_hi:[1,0]
	v_pk_add_f32 v[120:121], v[142:143], v[118:119]
	v_pk_fma_f32 v[108:109], v[140:141], v[2:3], v[108:109] op_sel:[1,1,0] op_sel_hi:[0,1,1] neg_hi:[1,0,0]
	v_pk_mul_f32 v[140:141], v[2:3], v[2:3] op_sel_hi:[1,0]
	v_pk_add_f32 v[102:103], v[142:143], v[118:119] neg_lo:[0,1] neg_hi:[0,1]
	v_pk_fma_f32 v[140:141], v[2:3], v[2:3], v[140:141] op_sel:[1,1,0] op_sel_hi:[0,1,1] neg_lo:[1,0,0]
	v_pk_add_f32 v[118:119], v[130:131], v[146:147] neg_lo:[0,1] neg_hi:[0,1]
	v_pk_mul_f32 v[142:143], v[128:129], v[140:141] op_sel_hi:[1,0]
	v_pk_add_f32 v[130:131], v[148:149], v[150:151]
	v_pk_fma_f32 v[128:129], v[128:129], v[140:141], v[142:143] op_sel:[1,1,0] op_sel_hi:[0,1,1] neg_hi:[1,0,0]
	v_pk_mul_f32 v[142:143], v[140:141], v[2:3] op_sel_hi:[1,0]
	v_pk_add_f32 v[126:127], v[144:145], v[110:111]
	v_pk_fma_f32 v[140:141], v[140:141], v[2:3], v[142:143] op_sel:[1,1,0] op_sel_hi:[0,1,1] neg_lo:[1,0,0]
	v_pk_add_f32 v[116:117], v[148:149], v[150:151] neg_lo:[0,1] neg_hi:[0,1]
	v_pk_mul_f32 v[142:143], v[130:131], v[140:141] op_sel_hi:[1,0]
	v_pk_add_f32 v[110:111], v[144:145], v[110:111] neg_lo:[0,1] neg_hi:[0,1]
	v_pk_fma_f32 v[130:131], v[130:131], v[140:141], v[142:143] op_sel:[1,1,0] op_sel_hi:[0,1,1] neg_hi:[1,0,0]
	v_pk_mul_f32 v[142:143], v[140:141], v[2:3] op_sel_hi:[1,0]
	v_pk_fma_f32 v[140:141], v[140:141], v[2:3], v[142:143] op_sel:[1,1,0] op_sel_hi:[0,1,1] neg_lo:[1,0,0]
	v_pk_mul_f32 v[142:143], v[122:123], v[140:141] op_sel_hi:[1,0]
	v_pk_fma_f32 v[122:123], v[122:123], v[140:141], v[142:143] op_sel:[1,1,0] op_sel_hi:[0,1,1] neg_hi:[1,0,0]
	v_pk_mul_f32 v[142:143], v[140:141], v[2:3] op_sel_hi:[1,0]
	v_pk_fma_f32 v[140:141], v[140:141], v[2:3], v[142:143] op_sel:[1,1,0] op_sel_hi:[0,1,1] neg_lo:[1,0,0]
	v_pk_mul_f32 v[142:143], v[126:127], v[140:141] op_sel_hi:[1,0]
	v_pk_fma_f32 v[126:127], v[126:127], v[140:141], v[142:143] op_sel:[1,1,0] op_sel_hi:[0,1,1] neg_hi:[1,0,0]
	v_pk_mul_f32 v[142:143], v[140:141], v[2:3] op_sel_hi:[1,0]
	v_pk_fma_f32 v[140:141], v[140:141], v[2:3], v[142:143] op_sel:[1,1,0] op_sel_hi:[0,1,1] neg_lo:[1,0,0]
	v_pk_mul_f32 v[142:143], v[120:121], v[140:141] op_sel_hi:[1,0]
	v_pk_fma_f32 v[120:121], v[120:121], v[140:141], v[142:143] op_sel:[1,1,0] op_sel_hi:[0,1,1] neg_hi:[1,0,0]
	v_pk_mul_f32 v[142:143], v[140:141], v[2:3] op_sel_hi:[1,0]
	v_pk_fma_f32 v[140:141], v[140:141], v[2:3], v[142:143] op_sel:[1,1,0] op_sel_hi:[0,1,1] neg_lo:[1,0,0]
	v_pk_mul_f32 v[142:143], v[124:125], v[140:141] op_sel_hi:[1,0]
	v_pk_fma_f32 v[124:125], v[124:125], v[140:141], v[142:143] op_sel:[1,1,0] op_sel_hi:[0,1,1] neg_hi:[1,0,0]
	v_pk_mul_f32 v[142:143], v[140:141], v[2:3] op_sel_hi:[1,0]
	v_pk_fma_f32 v[140:141], v[140:141], v[2:3], v[142:143] op_sel:[1,1,0] op_sel_hi:[0,1,1] neg_lo:[1,0,0]
	v_pk_mul_f32 v[142:143], v[114:115], v[140:141] op_sel_hi:[1,0]
	v_pk_fma_f32 v[114:115], v[114:115], v[140:141], v[142:143] op_sel:[1,1,0] op_sel_hi:[0,1,1] neg_hi:[1,0,0]
	v_pk_mul_f32 v[142:143], v[140:141], v[2:3] op_sel_hi:[1,0]
	v_pk_fma_f32 v[140:141], v[140:141], v[2:3], v[142:143] op_sel:[1,1,0] op_sel_hi:[0,1,1] neg_lo:[1,0,0]
	v_pk_mul_f32 v[142:143], v[118:119], v[140:141] op_sel_hi:[1,0]
	v_pk_fma_f32 v[118:119], v[118:119], v[140:141], v[142:143] op_sel:[1,1,0] op_sel_hi:[0,1,1] neg_hi:[1,0,0]
	v_pk_mul_f32 v[142:143], v[140:141], v[2:3] op_sel_hi:[1,0]
	v_pk_fma_f32 v[140:141], v[140:141], v[2:3], v[142:143] op_sel:[1,1,0] op_sel_hi:[0,1,1] neg_lo:[1,0,0]
	v_pk_mul_f32 v[142:143], v[112:113], v[140:141] op_sel_hi:[1,0]
	v_pk_fma_f32 v[112:113], v[112:113], v[140:141], v[142:143] op_sel:[1,1,0] op_sel_hi:[0,1,1] neg_hi:[1,0,0]
	v_pk_mul_f32 v[142:143], v[140:141], v[2:3] op_sel_hi:[1,0]
	v_pk_fma_f32 v[140:141], v[140:141], v[2:3], v[142:143] op_sel:[1,1,0] op_sel_hi:[0,1,1] neg_lo:[1,0,0]
	v_pk_mul_f32 v[142:143], v[116:117], v[140:141] op_sel_hi:[1,0]
	v_pk_fma_f32 v[116:117], v[116:117], v[140:141], v[142:143] op_sel:[1,1,0] op_sel_hi:[0,1,1] neg_hi:[1,0,0]
	v_pk_mul_f32 v[142:143], v[140:141], v[2:3] op_sel_hi:[1,0]
	v_pk_fma_f32 v[140:141], v[140:141], v[2:3], v[142:143] op_sel:[1,1,0] op_sel_hi:[0,1,1] neg_lo:[1,0,0]
	v_pk_mul_f32 v[142:143], v[104:105], v[140:141] op_sel_hi:[1,0]
	v_pk_fma_f32 v[104:105], v[104:105], v[140:141], v[142:143] op_sel:[1,1,0] op_sel_hi:[0,1,1] neg_hi:[1,0,0]
	v_pk_mul_f32 v[142:143], v[140:141], v[2:3] op_sel_hi:[1,0]
	v_pk_fma_f32 v[140:141], v[140:141], v[2:3], v[142:143] op_sel:[1,1,0] op_sel_hi:[0,1,1] neg_lo:[1,0,0]
	v_pk_mul_f32 v[142:143], v[110:111], v[140:141] op_sel_hi:[1,0]
	v_pk_fma_f32 v[110:111], v[110:111], v[140:141], v[142:143] op_sel:[1,1,0] op_sel_hi:[0,1,1] neg_hi:[1,0,0]
	v_pk_mul_f32 v[142:143], v[140:141], v[2:3] op_sel_hi:[1,0]
	v_pk_fma_f32 v[140:141], v[140:141], v[2:3], v[142:143] op_sel:[1,1,0] op_sel_hi:[0,1,1] neg_lo:[1,0,0]
	v_pk_mul_f32 v[142:143], v[102:103], v[140:141] op_sel_hi:[1,0]
	v_pk_fma_f32 v[102:103], v[102:103], v[140:141], v[142:143] op_sel:[1,1,0] op_sel_hi:[0,1,1] neg_hi:[1,0,0]
	v_pk_mul_f32 v[142:143], v[140:141], v[2:3] op_sel_hi:[1,0]
	v_pk_fma_f32 v[140:141], v[140:141], v[2:3], v[142:143] op_sel:[1,1,0] op_sel_hi:[0,1,1] neg_lo:[1,0,0]
	v_pk_mul_f32 v[142:143], v[106:107], v[140:141] op_sel_hi:[1,0]
	v_pk_fma_f32 v[106:107], v[106:107], v[140:141], v[142:143] op_sel:[1,1,0] op_sel_hi:[0,1,1] neg_hi:[1,0,0]
	ds_write2_b64 v133, v[4:5], v[108:109] offset1:72
	ds_write2_b64 v133, v[128:129], v[130:131] offset0:144 offset1:216
	ds_write2_b64 v134, v[122:123], v[126:127] offset0:32 offset1:104
	ds_write2_b64 v134, v[120:121], v[124:125] offset0:176 offset1:248
	ds_write2_b64 v135, v[114:115], v[118:119] offset0:64 offset1:136
	ds_write2_b64 v136, v[112:113], v[116:117] offset0:80 offset1:152
	ds_write2_b64 v137, v[104:105], v[110:111] offset0:96 offset1:168
	ds_write2_b64 v138, v[102:103], v[106:107] offset0:112 offset1:184
	s_cbranch_vccnz .LBB0_756
	v_mov_b32_e32 v4, v204
	s_waitcnt lgkmcnt(0)
	s_barrier
	s_mov_b32 s84, 0
	v_and_b32_e32 v5, 7, v4
	v_cvt_f32_ubyte0_e32 v2, v5
	v_mul_f32_e32 v3, 0x3c800000, v2
	v_cos_f32_e32 v2, v3
	v_sin_f32_e32 v3, v3
	v_lshlrev_b32_e32 v4, 3, v4
	v_lshl_add_u32 v5, v5, 3, 0
.LBB0_758:
	v_add_u32_e32 v38, s84, v4
	v_and_b32_e32 v38, 0xffffffc0, v38
	v_lshlrev_b32_e32 v102, 3, v38
	v_add3_u32 v38, v5, v38, v102
	ds_read2_b64 v[102:105], v38 offset1:9
	ds_read2_b64 v[106:109], v38 offset0:18 offset1:27
	ds_read2_b64 v[110:113], v38 offset0:36 offset1:45
	ds_read2_b64 v[114:117], v38 offset0:54 offset1:63
	s_addk_i32 s84, 0x1000
	s_cmpk_lg_i32 s84, 0x4000
	s_waitcnt lgkmcnt(1)
	v_pk_add_f32 v[118:119], v[102:103], v[110:111]
	v_pk_add_f32 v[102:103], v[102:103], v[110:111] neg_lo:[0,1] neg_hi:[0,1]
	v_pk_add_f32 v[110:111], v[104:105], v[112:113]
	v_pk_add_f32 v[104:105], v[104:105], v[112:113] neg_lo:[0,1] neg_hi:[0,1]
	v_mov_b64_e32 v[112:113], s[6:7]
	v_pk_mul_f32 v[120:121], v[104:105], v[112:113] op_sel_hi:[1,0]
	v_pk_fma_f32 v[104:105], v[104:105], v[112:113], v[120:121] op_sel:[1,1,0] op_sel_hi:[0,1,1] neg_hi:[1,0,0]
	s_waitcnt lgkmcnt(0)
	v_pk_add_f32 v[112:113], v[106:107], v[114:115]
	v_pk_add_f32 v[106:107], v[106:107], v[114:115] op_sel:[1,1] op_sel_hi:[0,0] neg_lo:[0,1] neg_hi:[1,0]
	v_pk_add_f32 v[114:115], v[108:109], v[116:117]
	v_pk_add_f32 v[108:109], v[108:109], v[116:117] neg_lo:[0,1] neg_hi:[0,1]
	v_mov_b64_e32 v[116:117], s[14:15]
	v_pk_mul_f32 v[120:121], v[108:109], v[116:117] op_sel_hi:[1,0]
	v_pk_fma_f32 v[108:109], v[108:109], v[116:117], v[120:121] op_sel:[1,1,0] op_sel_hi:[0,1,1] neg_hi:[1,0,0]
	v_pk_add_f32 v[116:117], v[118:119], v[112:113]
	v_pk_add_f32 v[112:113], v[118:119], v[112:113] neg_lo:[0,1] neg_hi:[0,1]
	v_pk_add_f32 v[118:119], v[110:111], v[114:115]
	v_pk_add_f32 v[110:111], v[110:111], v[114:115] op_sel:[1,1] op_sel_hi:[0,0] neg_lo:[0,1] neg_hi:[1,0]
	v_pk_add_f32 v[114:115], v[102:103], v[106:107]
	v_pk_add_f32 v[102:103], v[102:103], v[106:107] neg_lo:[0,1] neg_hi:[0,1]
	v_pk_add_f32 v[106:107], v[104:105], v[108:109]
	v_pk_add_f32 v[104:105], v[104:105], v[108:109] op_sel:[1,1] op_sel_hi:[0,0] neg_lo:[0,1] neg_hi:[1,0]
	v_pk_add_f32 v[108:109], v[116:117], v[118:119]
	v_pk_add_f32 v[116:117], v[116:117], v[118:119] neg_lo:[0,1] neg_hi:[0,1]
	v_pk_add_f32 v[118:119], v[112:113], v[110:111]
	v_pk_add_f32 v[110:111], v[112:113], v[110:111] neg_lo:[0,1] neg_hi:[0,1]
	v_pk_add_f32 v[112:113], v[114:115], v[106:107]
	v_pk_add_f32 v[106:107], v[114:115], v[106:107] neg_lo:[0,1] neg_hi:[0,1]
	v_pk_add_f32 v[114:115], v[102:103], v[104:105]
	v_pk_add_f32 v[102:103], v[102:103], v[104:105] neg_lo:[0,1] neg_hi:[0,1]
	v_pk_mul_f32 v[104:105], v[112:113], v[2:3] op_sel_hi:[1,0]
	v_pk_fma_f32 v[104:105], v[112:113], v[2:3], v[104:105] op_sel:[1,1,0] op_sel_hi:[0,1,1] neg_hi:[1,0,0]
	v_pk_mul_f32 v[112:113], v[2:3], v[2:3] op_sel_hi:[1,0]
	v_pk_fma_f32 v[112:113], v[2:3], v[2:3], v[112:113] op_sel:[1,1,0] op_sel_hi:[0,1,1] neg_lo:[1,0,0]
	v_pk_mul_f32 v[120:121], v[118:119], v[112:113] op_sel_hi:[1,0]
	v_pk_fma_f32 v[118:119], v[118:119], v[112:113], v[120:121] op_sel:[1,1,0] op_sel_hi:[0,1,1] neg_hi:[1,0,0]
	v_pk_mul_f32 v[120:121], v[112:113], v[2:3] op_sel_hi:[1,0]
	v_pk_fma_f32 v[112:113], v[112:113], v[2:3], v[120:121] op_sel:[1,1,0] op_sel_hi:[0,1,1] neg_lo:[1,0,0]
	v_pk_mul_f32 v[120:121], v[114:115], v[112:113] op_sel_hi:[1,0]
	v_pk_fma_f32 v[114:115], v[114:115], v[112:113], v[120:121] op_sel:[1,1,0] op_sel_hi:[0,1,1] neg_hi:[1,0,0]
	v_pk_mul_f32 v[120:121], v[112:113], v[2:3] op_sel_hi:[1,0]
	v_pk_fma_f32 v[112:113], v[112:113], v[2:3], v[120:121] op_sel:[1,1,0] op_sel_hi:[0,1,1] neg_lo:[1,0,0]
	v_pk_mul_f32 v[120:121], v[116:117], v[112:113] op_sel_hi:[1,0]
	v_pk_fma_f32 v[116:117], v[116:117], v[112:113], v[120:121] op_sel:[1,1,0] op_sel_hi:[0,1,1] neg_hi:[1,0,0]
	v_pk_mul_f32 v[120:121], v[112:113], v[2:3] op_sel_hi:[1,0]
	v_pk_fma_f32 v[112:113], v[112:113], v[2:3], v[120:121] op_sel:[1,1,0] op_sel_hi:[0,1,1] neg_lo:[1,0,0]
	v_pk_mul_f32 v[120:121], v[106:107], v[112:113] op_sel_hi:[1,0]
	v_pk_fma_f32 v[106:107], v[106:107], v[112:113], v[120:121] op_sel:[1,1,0] op_sel_hi:[0,1,1] neg_hi:[1,0,0]
	v_pk_mul_f32 v[120:121], v[112:113], v[2:3] op_sel_hi:[1,0]
	v_pk_fma_f32 v[112:113], v[112:113], v[2:3], v[120:121] op_sel:[1,1,0] op_sel_hi:[0,1,1] neg_lo:[1,0,0]
	v_pk_mul_f32 v[120:121], v[110:111], v[112:113] op_sel_hi:[1,0]
	v_pk_fma_f32 v[110:111], v[110:111], v[112:113], v[120:121] op_sel:[1,1,0] op_sel_hi:[0,1,1] neg_hi:[1,0,0]
	v_pk_mul_f32 v[120:121], v[112:113], v[2:3] op_sel_hi:[1,0]
	v_pk_fma_f32 v[112:113], v[112:113], v[2:3], v[120:121] op_sel:[1,1,0] op_sel_hi:[0,1,1] neg_lo:[1,0,0]
	v_pk_mul_f32 v[120:121], v[102:103], v[112:113] op_sel_hi:[1,0]
	v_pk_fma_f32 v[102:103], v[102:103], v[112:113], v[120:121] op_sel:[1,1,0] op_sel_hi:[0,1,1] neg_hi:[1,0,0]
	ds_write2_b64 v38, v[108:109], v[104:105] offset1:9
	ds_write2_b64 v38, v[118:119], v[114:115] offset0:18 offset1:27
	ds_write2_b64 v38, v[116:117], v[106:107] offset0:36 offset1:45
	ds_write2_b64 v38, v[110:111], v[102:103] offset0:54 offset1:63
	s_cbranch_scc1 .LBB0_758
	v_mov_b32_e32 v2, v204
	s_waitcnt lgkmcnt(0)
	s_barrier
	s_mov_b32 s84, 0
	v_mul_lo_u32 v2, v2, s33
	v_add_u32_e32 v2, 0, v2
.LBB0_760:
	v_add_u32_e32 v3, s84, v2
	ds_read2_b64 v[102:105], v3 offset1:1
	ds_read2_b64 v[106:109], v3 offset0:2 offset1:3
	ds_read2_b64 v[110:113], v3 offset0:4 offset1:5
	ds_read2_b64 v[114:117], v3 offset0:6 offset1:7
	s_add_i32 s84, s84, 0x9000
	s_cmp_lg_u32 s84, 0x24000
	s_waitcnt lgkmcnt(1)
	v_pk_add_f32 v[4:5], v[102:103], v[110:111]
	v_pk_add_f32 v[102:103], v[102:103], v[110:111] neg_lo:[0,1] neg_hi:[0,1]
	v_pk_add_f32 v[110:111], v[104:105], v[112:113]
	v_pk_add_f32 v[104:105], v[104:105], v[112:113] neg_lo:[0,1] neg_hi:[0,1]
	v_mov_b64_e32 v[112:113], s[6:7]
	v_pk_mul_f32 v[118:119], v[104:105], v[112:113] op_sel_hi:[1,0]
	v_pk_fma_f32 v[104:105], v[104:105], v[112:113], v[118:119] op_sel:[1,1,0] op_sel_hi:[0,1,1] neg_hi:[1,0,0]
	s_waitcnt lgkmcnt(0)
	v_pk_add_f32 v[112:113], v[106:107], v[114:115]
	v_pk_add_f32 v[106:107], v[106:107], v[114:115] op_sel:[1,1] op_sel_hi:[0,0] neg_lo:[0,1] neg_hi:[1,0]
	v_pk_add_f32 v[114:115], v[108:109], v[116:117]
	v_pk_add_f32 v[108:109], v[108:109], v[116:117] neg_lo:[0,1] neg_hi:[0,1]
	v_mov_b64_e32 v[116:117], s[14:15]
	v_pk_mul_f32 v[118:119], v[108:109], v[116:117] op_sel_hi:[1,0]
	v_pk_fma_f32 v[108:109], v[108:109], v[116:117], v[118:119] op_sel:[1,1,0] op_sel_hi:[0,1,1] neg_hi:[1,0,0]
	v_pk_add_f32 v[116:117], v[4:5], v[112:113]
	v_pk_add_f32 v[4:5], v[4:5], v[112:113] neg_lo:[0,1] neg_hi:[0,1]
	v_pk_add_f32 v[112:113], v[110:111], v[114:115]
	v_pk_add_f32 v[110:111], v[110:111], v[114:115] op_sel:[1,1] op_sel_hi:[0,0] neg_lo:[0,1] neg_hi:[1,0]
	v_pk_add_f32 v[114:115], v[102:103], v[106:107]
	v_pk_add_f32 v[102:103], v[102:103], v[106:107] neg_lo:[0,1] neg_hi:[0,1]
	v_pk_add_f32 v[106:107], v[104:105], v[108:109]
	v_pk_add_f32 v[104:105], v[104:105], v[108:109] op_sel:[1,1] op_sel_hi:[0,0] neg_lo:[0,1] neg_hi:[1,0]
	v_pk_add_f32 v[108:109], v[116:117], v[112:113]
	v_pk_add_f32 v[112:113], v[116:117], v[112:113] neg_lo:[0,1] neg_hi:[0,1]
	v_pk_add_f32 v[116:117], v[4:5], v[110:111]
	v_pk_add_f32 v[4:5], v[4:5], v[110:111] neg_lo:[0,1] neg_hi:[0,1]
	v_pk_add_f32 v[110:111], v[114:115], v[106:107]
	v_pk_add_f32 v[106:107], v[114:115], v[106:107] neg_lo:[0,1] neg_hi:[0,1]
	v_pk_add_f32 v[114:115], v[102:103], v[104:105]
	v_pk_add_f32 v[102:103], v[102:103], v[104:105] neg_lo:[0,1] neg_hi:[0,1]
	ds_write2_b64 v3, v[108:109], v[110:111] offset1:1
	ds_write2_b64 v3, v[116:117], v[114:115] offset0:2 offset1:3
	ds_write2_b64 v3, v[112:113], v[106:107] offset0:4 offset1:5
	ds_write2_b64 v3, v[4:5], v[102:103] offset0:6 offset1:7
	s_cbranch_scc1 .LBB0_760
	v_mov_b32_e32 v209, v208
	s_waitcnt lgkmcnt(0)
	s_barrier
	s_nop 0
	v_lshlrev_b32_e32 v3, 10, v209
	v_lshlrev_b32_e32 v4, 2, v209
	v_lshrrev_b32_e32 v5, 5, v209
	v_ashrrev_i32_e32 v38, 11, v209
	v_sub_u32_e32 v2, 0, v209
	v_and_b32_e32 v3, 0x3c00, v3
	v_and_b32_e32 v5, 56, v5
	v_and_or_b32 v4, v4, s9, v38
	v_or3_b32 v3, v4, v3, v5
	v_lshlrev_b32_e32 v4, 10, v2
	v_lshlrev_b32_e32 v5, 2, v2
	v_lshrrev_b32_e32 v38, 5, v2
	v_bfe_u32 v2, v2, 11, 3
	v_and_b32_e32 v4, 0x3c00, v4
	v_and_b32_e32 v5, 0x3c0, v5
	v_and_or_b32 v2, v38, 56, v2
	v_or3_b32 v2, v2, v5, v4
	v_add_u32_e32 v4, 1, v209
	v_lshlrev_b32_e32 v38, 10, v4
	v_lshlrev_b32_e32 v102, 2, v4
	v_lshrrev_b32_e32 v103, 5, v4
	v_ashrrev_i32_e32 v4, 11, v4
	v_not_b32_e32 v5, v209
	v_and_b32_e32 v38, 0x3c00, v38
	v_and_b32_e32 v103, 56, v103
	v_and_or_b32 v4, v102, s9, v4
	v_or3_b32 v4, v4, v38, v103
	v_lshlrev_b32_e32 v38, 10, v5
	v_lshlrev_b32_e32 v102, 2, v5
	v_lshrrev_b32_e32 v103, 5, v5
	v_bfe_u32 v5, v5, 11, 3
	v_and_b32_e32 v38, 0x3c00, v38
	v_and_b32_e32 v102, 0x3c0, v102
	v_and_or_b32 v5, v103, 56, v5
	v_mul_i32_i24_e32 v3, 9, v3
	v_mul_u32_u24_e32 v2, 9, v2
	v_or3_b32 v5, v5, v102, v38
	v_and_b32_e32 v3, -8, v3
	v_and_b32_e32 v2, 0x3fff8, v2
	v_mul_i32_i24_e32 v4, 9, v4
	v_mul_u32_u24_e32 v5, 9, v5
	v_add_u32_e32 v3, 0, v3
	v_add_u32_e32 v2, 0, v2
	v_and_b32_e32 v4, -8, v4
	v_and_b32_e32 v5, 0x3fff8, v5
	v_add_u32_e32 v4, 0, v4
	v_add_u32_e32 v5, 0, v5
	ds_read_b64 v[158:159], v3
	ds_read_b64 v[160:161], v2
	ds_read_b64 v[154:155], v4
	ds_read_b64 v[156:157], v5
	v_add_u32_e32 v2, 2, v209
	v_lshlrev_b32_e32 v4, 10, v2
	v_lshlrev_b32_e32 v5, 2, v2
	v_lshrrev_b32_e32 v38, 5, v2
	v_ashrrev_i32_e32 v2, 11, v2
	v_sub_u32_e32 v3, -2, v209
	v_and_b32_e32 v4, 0x3c00, v4
	v_and_b32_e32 v38, 56, v38
	v_and_or_b32 v2, v5, s9, v2
	v_or3_b32 v2, v2, v4, v38
	v_lshlrev_b32_e32 v4, 10, v3
	v_lshlrev_b32_e32 v5, 2, v3
	v_lshrrev_b32_e32 v38, 5, v3
	v_bfe_u32 v3, v3, 11, 3
	v_and_b32_e32 v4, 0x3c00, v4
	v_and_b32_e32 v5, 0x3c0, v5
	v_and_or_b32 v3, v38, 56, v3
	v_or3_b32 v3, v3, v5, v4
	v_add_u32_e32 v4, 3, v209
	v_lshlrev_b32_e32 v38, 10, v4
	v_lshlrev_b32_e32 v102, 2, v4
	v_lshrrev_b32_e32 v103, 5, v4
	v_ashrrev_i32_e32 v4, 11, v4
	v_sub_u32_e32 v5, -3, v209
	v_and_b32_e32 v38, 0x3c00, v38
	v_and_b32_e32 v103, 56, v103
	v_and_or_b32 v4, v102, s9, v4
	v_or3_b32 v4, v4, v38, v103
	v_lshlrev_b32_e32 v38, 10, v5
	v_lshlrev_b32_e32 v102, 2, v5
	v_lshrrev_b32_e32 v103, 5, v5
	v_bfe_u32 v5, v5, 11, 3
	v_and_b32_e32 v38, 0x3c00, v38
	v_and_b32_e32 v102, 0x3c0, v102
	v_and_or_b32 v5, v103, 56, v5
	v_mul_i32_i24_e32 v2, 9, v2
	v_or3_b32 v5, v5, v102, v38
	v_and_b32_e32 v2, -8, v2
	v_mul_u32_u24_e32 v3, 9, v3
	v_mul_i32_i24_e32 v4, 9, v4
	v_mul_u32_u24_e32 v5, 9, v5
	v_add_u32_e32 v2, 0, v2
	v_and_b32_e32 v3, 0x3fff8, v3
	v_and_b32_e32 v4, -8, v4
	v_and_b32_e32 v5, 0x3fff8, v5
	v_add_u32_e32 v3, 0, v3
	v_add_u32_e32 v4, 0, v4
	v_add_u32_e32 v5, 0, v5
	ds_read_b64 v[150:151], v2
	ds_read_b64 v[152:153], v3
	ds_read_b64 v[146:147], v4
	ds_read_b64 v[148:149], v5
	v_add_u32_e32 v2, 4, v209
	v_lshlrev_b32_e32 v4, 10, v2
	v_lshlrev_b32_e32 v5, 2, v2
	v_lshrrev_b32_e32 v38, 5, v2
	v_ashrrev_i32_e32 v2, 11, v2
	v_sub_u32_e32 v3, -4, v209
	v_and_b32_e32 v4, 0x3c00, v4
	v_and_b32_e32 v38, 56, v38
	v_and_or_b32 v2, v5, s9, v2
	v_or3_b32 v2, v2, v4, v38
	v_lshlrev_b32_e32 v4, 10, v3
	v_lshlrev_b32_e32 v5, 2, v3
	v_lshrrev_b32_e32 v38, 5, v3
	v_bfe_u32 v3, v3, 11, 3
	v_and_b32_e32 v4, 0x3c00, v4
	v_and_b32_e32 v5, 0x3c0, v5
	v_and_or_b32 v3, v38, 56, v3
	v_or3_b32 v3, v3, v5, v4
	v_add_u32_e32 v4, 5, v209
	v_lshlrev_b32_e32 v38, 10, v4
	v_lshlrev_b32_e32 v102, 2, v4
	v_lshrrev_b32_e32 v103, 5, v4
	v_ashrrev_i32_e32 v4, 11, v4
	v_sub_u32_e32 v5, -5, v209
	v_and_b32_e32 v38, 0x3c00, v38
	v_and_b32_e32 v103, 56, v103
	v_and_or_b32 v4, v102, s9, v4
	v_or3_b32 v4, v4, v38, v103
	v_lshlrev_b32_e32 v38, 10, v5
	v_lshlrev_b32_e32 v102, 2, v5
	v_lshrrev_b32_e32 v103, 5, v5
	v_bfe_u32 v5, v5, 11, 3
	v_and_b32_e32 v38, 0x3c00, v38
	v_and_b32_e32 v102, 0x3c0, v102
	v_and_or_b32 v5, v103, 56, v5
	v_mul_i32_i24_e32 v2, 9, v2
	v_or3_b32 v5, v5, v102, v38
	v_and_b32_e32 v2, -8, v2
	v_mul_u32_u24_e32 v3, 9, v3
	v_mul_i32_i24_e32 v4, 9, v4
	v_mul_u32_u24_e32 v5, 9, v5
	v_add_u32_e32 v2, 0, v2
	v_and_b32_e32 v3, 0x3fff8, v3
	v_and_b32_e32 v4, -8, v4
	v_and_b32_e32 v5, 0x3fff8, v5
	v_add_u32_e32 v3, 0, v3
	v_add_u32_e32 v4, 0, v4
	v_add_u32_e32 v5, 0, v5
	ds_read_b64 v[142:143], v2
	ds_read_b64 v[144:145], v3
	ds_read_b64 v[138:139], v4
	ds_read_b64 v[140:141], v5
	v_add_u32_e32 v2, 6, v209
	v_lshlrev_b32_e32 v4, 10, v2
	v_lshlrev_b32_e32 v5, 2, v2
	v_lshrrev_b32_e32 v38, 5, v2
	v_ashrrev_i32_e32 v2, 11, v2
	v_sub_u32_e32 v3, -6, v209
	v_and_b32_e32 v4, 0x3c00, v4
	v_and_b32_e32 v38, 56, v38
	v_and_or_b32 v2, v5, s9, v2
	v_or3_b32 v2, v2, v4, v38
	v_lshlrev_b32_e32 v4, 10, v3
	v_lshlrev_b32_e32 v5, 2, v3
	v_lshrrev_b32_e32 v38, 5, v3
	v_bfe_u32 v3, v3, 11, 3
	v_and_b32_e32 v4, 0x3c00, v4
	v_and_b32_e32 v5, 0x3c0, v5
	v_and_or_b32 v3, v38, 56, v3
	v_or3_b32 v3, v3, v5, v4
	v_add_u32_e32 v4, 7, v209
	v_lshlrev_b32_e32 v38, 10, v4
	v_lshlrev_b32_e32 v102, 2, v4
	v_lshrrev_b32_e32 v103, 5, v4
	v_ashrrev_i32_e32 v4, 11, v4
	v_sub_u32_e32 v5, -7, v209
	v_and_b32_e32 v38, 0x3c00, v38
	v_and_b32_e32 v103, 56, v103
	v_and_or_b32 v4, v102, s9, v4
	v_or3_b32 v4, v4, v38, v103
	v_lshlrev_b32_e32 v38, 10, v5
	v_lshlrev_b32_e32 v102, 2, v5
	v_lshrrev_b32_e32 v103, 5, v5
	v_bfe_u32 v5, v5, 11, 3
	v_and_b32_e32 v38, 0x3c00, v38
	v_and_b32_e32 v102, 0x3c0, v102
	v_and_or_b32 v5, v103, 56, v5
	v_mul_i32_i24_e32 v2, 9, v2
	v_or3_b32 v5, v5, v102, v38
	v_and_b32_e32 v2, -8, v2
	v_mul_u32_u24_e32 v3, 9, v3
	v_mul_i32_i24_e32 v4, 9, v4
	v_mul_u32_u24_e32 v5, 9, v5
	v_add_u32_e32 v2, 0, v2
	v_and_b32_e32 v3, 0x3fff8, v3
	v_and_b32_e32 v4, -8, v4
	v_and_b32_e32 v5, 0x3fff8, v5
	v_add_u32_e32 v3, 0, v3
	v_add_u32_e32 v4, 0, v4
	v_add_u32_e32 v5, 0, v5
	ds_read_b64 v[134:135], v2
	ds_read_b64 v[136:137], v3
	ds_read_b64 v[130:131], v4
	ds_read_b64 v[132:133], v5
	v_add_u32_e32 v2, 8, v209
	v_lshlrev_b32_e32 v4, 10, v2
	v_lshlrev_b32_e32 v5, 2, v2
	v_lshrrev_b32_e32 v38, 5, v2
	v_ashrrev_i32_e32 v2, 11, v2
	v_sub_u32_e32 v3, -8, v209
	v_and_b32_e32 v4, 0x3c00, v4
	v_and_b32_e32 v38, 56, v38
	v_and_or_b32 v2, v5, s9, v2
	v_or3_b32 v2, v2, v4, v38
	v_lshlrev_b32_e32 v4, 10, v3
	v_lshlrev_b32_e32 v5, 2, v3
	v_lshrrev_b32_e32 v38, 5, v3
	v_bfe_u32 v3, v3, 11, 3
	v_and_b32_e32 v4, 0x3c00, v4
	v_and_b32_e32 v5, 0x3c0, v5
	v_and_or_b32 v3, v38, 56, v3
	v_or3_b32 v3, v3, v5, v4
	v_add_u32_e32 v4, 9, v209
	v_lshlrev_b32_e32 v38, 10, v4
	v_lshlrev_b32_e32 v102, 2, v4
	v_lshrrev_b32_e32 v103, 5, v4
	v_ashrrev_i32_e32 v4, 11, v4
	v_sub_u32_e32 v5, -9, v209
	v_and_b32_e32 v38, 0x3c00, v38
	v_and_b32_e32 v103, 56, v103
	v_and_or_b32 v4, v102, s9, v4
	v_or3_b32 v4, v4, v38, v103
	v_lshlrev_b32_e32 v38, 10, v5
	v_lshlrev_b32_e32 v102, 2, v5
	v_lshrrev_b32_e32 v103, 5, v5
	v_bfe_u32 v5, v5, 11, 3
	v_and_b32_e32 v38, 0x3c00, v38
	v_and_b32_e32 v102, 0x3c0, v102
	v_and_or_b32 v5, v103, 56, v5
	v_mul_i32_i24_e32 v2, 9, v2
	v_or3_b32 v5, v5, v102, v38
	v_and_b32_e32 v2, -8, v2
	v_mul_u32_u24_e32 v3, 9, v3
	v_mul_i32_i24_e32 v4, 9, v4
	v_mul_u32_u24_e32 v5, 9, v5
	v_add_u32_e32 v2, 0, v2
	v_and_b32_e32 v3, 0x3fff8, v3
	v_and_b32_e32 v4, -8, v4
	v_and_b32_e32 v5, 0x3fff8, v5
	v_add_u32_e32 v3, 0, v3
	v_add_u32_e32 v4, 0, v4
	v_add_u32_e32 v5, 0, v5
	ds_read_b64 v[126:127], v2
	ds_read_b64 v[128:129], v3
	ds_read_b64 v[122:123], v4
	ds_read_b64 v[124:125], v5
	v_add_u32_e32 v2, 10, v209
	v_lshlrev_b32_e32 v4, 10, v2
	v_lshlrev_b32_e32 v5, 2, v2
	v_lshrrev_b32_e32 v38, 5, v2
	v_ashrrev_i32_e32 v2, 11, v2
	v_sub_u32_e32 v3, -10, v209
	v_and_b32_e32 v4, 0x3c00, v4
	v_and_b32_e32 v38, 56, v38
	v_and_or_b32 v2, v5, s9, v2
	v_or3_b32 v2, v2, v4, v38
	v_lshlrev_b32_e32 v4, 10, v3
	v_lshlrev_b32_e32 v5, 2, v3
	v_lshrrev_b32_e32 v38, 5, v3
	v_bfe_u32 v3, v3, 11, 3
	v_and_b32_e32 v4, 0x3c00, v4
	v_and_b32_e32 v5, 0x3c0, v5
	v_and_or_b32 v3, v38, 56, v3
	v_or3_b32 v3, v3, v5, v4
	v_add_u32_e32 v4, 11, v209
	v_lshlrev_b32_e32 v38, 10, v4
	v_lshlrev_b32_e32 v102, 2, v4
	v_lshrrev_b32_e32 v103, 5, v4
	v_ashrrev_i32_e32 v4, 11, v4
	v_sub_u32_e32 v5, -11, v209
	v_and_b32_e32 v38, 0x3c00, v38
	v_and_b32_e32 v103, 56, v103
	v_and_or_b32 v4, v102, s9, v4
	v_or3_b32 v4, v4, v38, v103
	v_lshlrev_b32_e32 v38, 10, v5
	v_lshlrev_b32_e32 v102, 2, v5
	v_lshrrev_b32_e32 v103, 5, v5
	v_bfe_u32 v5, v5, 11, 3
	v_and_b32_e32 v38, 0x3c00, v38
	v_and_b32_e32 v102, 0x3c0, v102
	v_and_or_b32 v5, v103, 56, v5
	v_mul_i32_i24_e32 v2, 9, v2
	v_or3_b32 v5, v5, v102, v38
	v_and_b32_e32 v2, -8, v2
	v_mul_u32_u24_e32 v3, 9, v3
	v_mul_i32_i24_e32 v4, 9, v4
	v_mul_u32_u24_e32 v5, 9, v5
	v_add_u32_e32 v2, 0, v2
	v_and_b32_e32 v3, 0x3fff8, v3
	v_and_b32_e32 v4, -8, v4
	v_and_b32_e32 v5, 0x3fff8, v5
	v_add_u32_e32 v3, 0, v3
	v_add_u32_e32 v4, 0, v4
	v_add_u32_e32 v5, 0, v5
	ds_read_b64 v[118:119], v2
	ds_read_b64 v[120:121], v3
	ds_read_b64 v[114:115], v4
	ds_read_b64 v[116:117], v5
	v_add_u32_e32 v2, 12, v209
	v_lshlrev_b32_e32 v4, 10, v2
	v_lshlrev_b32_e32 v5, 2, v2
	v_lshrrev_b32_e32 v38, 5, v2
	v_ashrrev_i32_e32 v2, 11, v2
	v_sub_u32_e32 v3, -12, v209
	v_and_b32_e32 v4, 0x3c00, v4
	v_and_b32_e32 v38, 56, v38
	v_and_or_b32 v2, v5, s9, v2
	v_or3_b32 v2, v2, v4, v38
	v_lshlrev_b32_e32 v4, 10, v3
	v_lshlrev_b32_e32 v5, 2, v3
	v_lshrrev_b32_e32 v38, 5, v3
	v_bfe_u32 v3, v3, 11, 3
	v_and_b32_e32 v4, 0x3c00, v4
	v_and_b32_e32 v5, 0x3c0, v5
	v_and_or_b32 v3, v38, 56, v3
	v_or3_b32 v3, v3, v5, v4
	v_add_u32_e32 v4, 13, v209
	v_lshlrev_b32_e32 v38, 10, v4
	v_lshlrev_b32_e32 v102, 2, v4
	v_lshrrev_b32_e32 v103, 5, v4
	v_ashrrev_i32_e32 v4, 11, v4
	v_sub_u32_e32 v5, -13, v209
	v_and_b32_e32 v38, 0x3c00, v38
	v_and_b32_e32 v103, 56, v103
	v_and_or_b32 v4, v102, s9, v4
	v_or3_b32 v4, v4, v38, v103
	v_lshlrev_b32_e32 v38, 10, v5
	v_lshlrev_b32_e32 v102, 2, v5
	v_lshrrev_b32_e32 v103, 5, v5
	v_bfe_u32 v5, v5, 11, 3
	v_and_b32_e32 v38, 0x3c00, v38
	v_and_b32_e32 v102, 0x3c0, v102
	v_and_or_b32 v5, v103, 56, v5
	v_mul_i32_i24_e32 v2, 9, v2
	v_or3_b32 v5, v5, v102, v38
	v_and_b32_e32 v2, -8, v2
	v_mul_u32_u24_e32 v3, 9, v3
	v_mul_i32_i24_e32 v4, 9, v4
	v_mul_u32_u24_e32 v5, 9, v5
	v_add_u32_e32 v2, 0, v2
	v_and_b32_e32 v3, 0x3fff8, v3
	v_and_b32_e32 v4, -8, v4
	v_and_b32_e32 v5, 0x3fff8, v5
	v_add_u32_e32 v3, 0, v3
	v_add_u32_e32 v4, 0, v4
	v_add_u32_e32 v5, 0, v5
	ds_read_b64 v[110:111], v2
	ds_read_b64 v[112:113], v3
	ds_read_b64 v[106:107], v4
	ds_read_b64 v[108:109], v5
	v_add_u32_e32 v2, 14, v209
	v_lshlrev_b32_e32 v4, 10, v2
	v_lshlrev_b32_e32 v5, 2, v2
	v_lshrrev_b32_e32 v38, 5, v2
	v_ashrrev_i32_e32 v2, 11, v2
	v_sub_u32_e32 v3, -14, v209
	v_and_b32_e32 v4, 0x3c00, v4
	v_and_b32_e32 v38, 56, v38
	v_and_or_b32 v2, v5, s9, v2
	v_or3_b32 v2, v2, v4, v38
	v_lshlrev_b32_e32 v4, 10, v3
	v_lshlrev_b32_e32 v5, 2, v3
	v_lshrrev_b32_e32 v38, 5, v3
	v_bfe_u32 v3, v3, 11, 3
	v_and_b32_e32 v4, 0x3c00, v4
	v_and_b32_e32 v5, 0x3c0, v5
	v_and_or_b32 v3, v38, 56, v3
	v_or3_b32 v3, v3, v5, v4
	v_add_u32_e32 v4, 15, v209
	v_lshlrev_b32_e32 v38, 10, v4
	v_lshlrev_b32_e32 v102, 2, v4
	v_lshrrev_b32_e32 v103, 5, v4
	v_ashrrev_i32_e32 v4, 11, v4
	v_sub_u32_e32 v5, -15, v209
	v_and_b32_e32 v38, 0x3c00, v38
	v_and_b32_e32 v103, 56, v103
	v_and_or_b32 v4, v102, s9, v4
	v_or3_b32 v4, v4, v38, v103
	v_lshlrev_b32_e32 v38, 10, v5
	v_lshlrev_b32_e32 v102, 2, v5
	v_lshrrev_b32_e32 v103, 5, v5
	v_bfe_u32 v5, v5, 11, 3
	v_and_b32_e32 v38, 0x3c00, v38
	v_and_b32_e32 v102, 0x3c0, v102
	v_and_or_b32 v5, v103, 56, v5
	v_or3_b32 v5, v5, v102, v38
	v_mul_i32_i24_e32 v2, 9, v2
	v_mul_u32_u24_e32 v3, 9, v3
	v_mul_i32_i24_e32 v4, 9, v4
	v_mul_u32_u24_e32 v5, 9, v5
	v_and_b32_e32 v2, -8, v2
	v_and_b32_e32 v3, 0x3fff8, v3
	v_and_b32_e32 v4, -8, v4
	v_and_b32_e32 v5, 0x3fff8, v5
	v_add_u32_e32 v2, 0, v2
	v_add_u32_e32 v3, 0, v3
	v_add_u32_e32 v4, 0, v4
	v_add_u32_e32 v5, 0, v5
	ds_read_b64 v[102:103], v2
	ds_read_b64 v[104:105], v3
	ds_read_b64 v[2:3], v4
	ds_read_b64 v[4:5], v5
	s_and_saveexec_b64 s[84:85], s[0:1]
	s_cbranch_execz .LBB0_763
	ds_read_b64 v[162:163], v203 offset:32
	v_mov_b32_e32 v38, s94
	s_waitcnt lgkmcnt(0)
	ds_write_b64 v38, v[162:163]
.LBB0_763:
	s_or_b64 exec, exec, s[84:85]
	v_mov_b64_e32 v[166:167], s[4:5]
	s_waitcnt vmcnt(29)
	v_pk_mul_f32 v[162:163], v[74:75], v[166:167] op_sel_hi:[1,0]
	v_mov_b64_e32 v[168:169], s[10:11]
	v_pk_fma_f32 v[180:181], v[74:75], v[166:167], v[162:163] op_sel:[1,1,0] op_sel_hi:[0,1,1] neg_hi:[1,0,0]
	v_mov_b64_e32 v[162:163], s[6:7]
	s_waitcnt vmcnt(27)
	v_pk_mul_f32 v[164:165], v[78:79], v[162:163] op_sel_hi:[1,0]
	v_mov_b32_e32 v38, v204
	v_pk_fma_f32 v[184:185], v[78:79], v[162:163], v[164:165] op_sel:[1,1,0] op_sel_hi:[0,1,1] neg_hi:[1,0,0]
	s_waitcnt vmcnt(25)
	v_pk_mul_f32 v[164:165], v[82:83], v[168:169] op_sel_hi:[1,0]
	v_mov_b64_e32 v[170:171], s[12:13]
	v_pk_fma_f32 v[188:189], v[82:83], v[168:169], v[164:165] op_sel:[1,1,0] op_sel_hi:[0,1,1] neg_hi:[1,0,0]
	s_waitcnt vmcnt(2)
	v_pk_mul_f32 v[164:165], v[90:91], v[170:171] op_sel_hi:[1,0]
	s_waitcnt lgkmcnt(0)
	s_barrier
	v_pk_add_f32 v[176:177], v[70:71], 0 op_sel_hi:[1,0]
	v_pk_add_f32 v[178:179], v[74:75], 0 op_sel_hi:[1,0]
	v_pk_add_f32 v[190:191], v[86:87], 0 op_sel_hi:[1,0]
	v_pk_add_f32 v[194:195], v[90:91], 0 op_sel_hi:[1,0]
	v_pk_fma_f32 v[210:211], v[90:91], v[170:171], v[164:165] op_sel:[1,1,0] op_sel_hi:[0,1,1] neg_hi:[1,0,0]
	v_mov_b64_e32 v[164:165], s[14:15]
	s_waitcnt vmcnt(0)
	v_pk_mul_f32 v[174:175], v[94:95], v[164:165] op_sel_hi:[1,0]
	v_cvt_f32_i32_e32 v224, v38
	v_pk_add_f32 v[182:183], v[78:79], 0 op_sel_hi:[1,0]
	v_pk_add_f32 v[186:187], v[82:83], 0 op_sel_hi:[1,0]
	v_pk_add_f32 v[212:213], v[94:95], 0 op_sel_hi:[1,0]
	v_pk_fma_f32 v[214:215], v[94:95], v[164:165], v[174:175] op_sel:[1,1,0] op_sel_hi:[0,1,1] neg_hi:[1,0,0]
	v_pk_add_f32 v[216:217], v[98:99], 0 op_sel_hi:[1,0]
	v_mov_b64_e32 v[174:175], s[16:17]
	v_pk_mul_f32 v[218:219], v[98:99], v[174:175] op_sel_hi:[1,0]
	v_pk_add_f32 v[220:221], v[190:191], v[176:177]
	v_pk_add_f32 v[176:177], v[176:177], v[190:191] neg_lo:[0,1] neg_hi:[0,1]
	v_pk_add_f32 v[190:191], v[194:195], v[178:179]
	v_pk_add_f32 v[178:179], v[178:179], v[194:195] neg_lo:[0,1] neg_hi:[0,1]
	v_mov_b64_e32 v[172:173], s[18:19]
	v_pk_mul_f32 v[194:195], v[178:179], v[162:163] op_sel_hi:[1,0]
	v_pk_add_f32 v[192:193], v[86:87], v[172:173] op_sel:[1,1] op_sel_hi:[0,0] neg_lo:[0,1] neg_hi:[1,0]
	v_pk_fma_f32 v[218:219], v[98:99], v[174:175], v[218:219] op_sel:[1,1,0] op_sel_hi:[0,1,1] neg_hi:[1,0,0]
	v_pk_add_f32 v[222:223], v[180:181], v[210:211]
	v_pk_fma_f32 v[178:179], v[178:179], v[162:163], v[194:195] op_sel:[1,1,0] op_sel_hi:[0,1,1] neg_hi:[1,0,0]
	v_pk_add_f32 v[194:195], v[212:213], v[182:183]
	v_pk_add_f32 v[182:183], v[182:183], v[212:213] op_sel:[1,1] op_sel_hi:[0,0] neg_lo:[0,1] neg_hi:[1,0]
	v_pk_add_f32 v[212:213], v[216:217], v[186:187]
	v_pk_add_f32 v[186:187], v[186:187], v[216:217] neg_lo:[0,1] neg_hi:[0,1]
	v_pk_add_f32 v[180:181], v[180:181], v[210:211] neg_lo:[0,1] neg_hi:[0,1]
	v_pk_mul_f32 v[216:217], v[186:187], v[164:165] op_sel_hi:[1,0]
	v_mul_f32_e32 v225, 0x38800000, v224
	v_pk_mul_f32 v[210:211], v[180:181], v[162:163] op_sel_hi:[1,0]
	v_pk_fma_f32 v[186:187], v[186:187], v[164:165], v[216:217] op_sel:[1,1,0] op_sel_hi:[0,1,1] neg_hi:[1,0,0]
	v_pk_add_f32 v[216:217], v[70:71], v[192:193]
	v_pk_add_f32 v[192:193], v[70:71], v[192:193] neg_lo:[0,1] neg_hi:[0,1]
	v_pk_fma_f32 v[180:181], v[180:181], v[162:163], v[210:211] op_sel:[1,1,0] op_sel_hi:[0,1,1] neg_hi:[1,0,0]
	v_pk_add_f32 v[210:211], v[184:185], v[214:215]
	v_pk_add_f32 v[184:185], v[184:185], v[214:215] op_sel:[1,1] op_sel_hi:[0,0] neg_lo:[0,1] neg_hi:[1,0]
	v_pk_add_f32 v[214:215], v[188:189], v[218:219]
	v_pk_add_f32 v[188:189], v[188:189], v[218:219] neg_lo:[0,1] neg_hi:[0,1]
	v_cos_f32_e32 v224, v225
	v_pk_mul_f32 v[218:219], v[188:189], v[164:165] op_sel_hi:[1,0]
	v_sin_f32_e32 v225, v225
	v_pk_fma_f32 v[188:189], v[188:189], v[164:165], v[218:219] op_sel:[1,1,0] op_sel_hi:[0,1,1] neg_hi:[1,0,0]
	v_pk_add_f32 v[218:219], v[194:195], v[220:221]
	v_pk_add_f32 v[194:195], v[220:221], v[194:195] neg_lo:[0,1] neg_hi:[0,1]
	v_pk_add_f32 v[220:221], v[212:213], v[190:191]
	v_pk_add_f32 v[190:191], v[190:191], v[212:213] op_sel:[1,1] op_sel_hi:[0,0] neg_lo:[0,1] neg_hi:[1,0]
	v_pk_add_f32 v[212:213], v[176:177], v[182:183]
	v_pk_add_f32 v[176:177], v[176:177], v[182:183] neg_lo:[0,1] neg_hi:[0,1]
	v_pk_add_f32 v[182:183], v[178:179], v[186:187]
	v_pk_add_f32 v[178:179], v[178:179], v[186:187] op_sel:[1,1] op_sel_hi:[0,0] neg_lo:[0,1] neg_hi:[1,0]
	v_pk_add_f32 v[186:187], v[216:217], v[210:211]
	v_pk_add_f32 v[210:211], v[216:217], v[210:211] neg_lo:[0,1] neg_hi:[0,1]
	v_pk_add_f32 v[216:217], v[222:223], v[214:215]
	v_pk_add_f32 v[214:215], v[222:223], v[214:215] op_sel:[1,1] op_sel_hi:[0,0] neg_lo:[0,1] neg_hi:[1,0]
	v_pk_add_f32 v[222:223], v[192:193], v[184:185]
	v_pk_add_f32 v[184:185], v[192:193], v[184:185] neg_lo:[0,1] neg_hi:[0,1]
	v_pk_add_f32 v[192:193], v[180:181], v[188:189]
	v_pk_add_f32 v[180:181], v[180:181], v[188:189] op_sel:[1,1] op_sel_hi:[0,0] neg_lo:[0,1] neg_hi:[1,0]
	v_pk_add_f32 v[188:189], v[220:221], v[218:219]
	v_pk_add_f32 v[218:219], v[218:219], v[220:221] neg_lo:[0,1] neg_hi:[0,1]
	v_pk_add_f32 v[220:221], v[194:195], v[190:191]
	v_pk_add_f32 v[190:191], v[194:195], v[190:191] neg_lo:[0,1] neg_hi:[0,1]
	v_pk_add_f32 v[194:195], v[212:213], v[182:183]
	v_pk_add_f32 v[182:183], v[212:213], v[182:183] neg_lo:[0,1] neg_hi:[0,1]
	v_pk_add_f32 v[212:213], v[176:177], v[178:179]
	v_pk_add_f32 v[176:177], v[176:177], v[178:179] neg_lo:[0,1] neg_hi:[0,1]
	v_pk_add_f32 v[178:179], v[186:187], v[216:217]
	v_pk_add_f32 v[186:187], v[186:187], v[216:217] neg_lo:[0,1] neg_hi:[0,1]
	v_pk_add_f32 v[216:217], v[210:211], v[214:215]
	v_pk_add_f32 v[210:211], v[210:211], v[214:215] neg_lo:[0,1] neg_hi:[0,1]
	v_pk_add_f32 v[214:215], v[222:223], v[192:193]
	v_pk_add_f32 v[192:193], v[222:223], v[192:193] neg_lo:[0,1] neg_hi:[0,1]
	v_pk_add_f32 v[222:223], v[184:185], v[180:181]
	v_pk_add_f32 v[180:181], v[184:185], v[180:181] neg_lo:[0,1] neg_hi:[0,1]
	v_pk_mul_f32 v[184:185], v[178:179], v[224:225] op_sel_hi:[1,0]
	v_and_b32_e32 v228, -8, v38
	v_pk_fma_f32 v[178:179], v[178:179], v[224:225], v[184:185] op_sel:[1,1,0] op_sel_hi:[0,1,1] neg_hi:[1,0,0]
	v_pk_mul_f32 v[184:185], v[224:225], v[224:225] op_sel_hi:[1,0]
	v_pk_add_f32 v[172:173], v[88:89], v[172:173] op_sel:[1,1] op_sel_hi:[0,0] neg_lo:[0,1] neg_hi:[1,0]
	s_mov_b32 s86, 0
	v_pk_fma_f32 v[184:185], v[224:225], v[224:225], v[184:185] op_sel:[1,1,0] op_sel_hi:[0,1,1] neg_lo:[1,0,0]
	s_mov_b64 s[84:85], -1
	v_pk_mul_f32 v[226:227], v[194:195], v[184:185] op_sel_hi:[1,0]
	v_pk_fma_f32 v[194:195], v[194:195], v[184:185], v[226:227] op_sel:[1,1,0] op_sel_hi:[0,1,1] neg_hi:[1,0,0]
	v_pk_mul_f32 v[226:227], v[184:185], v[224:225] op_sel_hi:[1,0]
	v_pk_fma_f32 v[184:185], v[184:185], v[224:225], v[226:227] op_sel:[1,1,0] op_sel_hi:[0,1,1] neg_lo:[1,0,0]
	v_pk_mul_f32 v[226:227], v[214:215], v[184:185] op_sel_hi:[1,0]
	v_pk_fma_f32 v[214:215], v[214:215], v[184:185], v[226:227] op_sel:[1,1,0] op_sel_hi:[0,1,1] neg_hi:[1,0,0]
	v_pk_mul_f32 v[226:227], v[184:185], v[224:225] op_sel_hi:[1,0]
	v_pk_fma_f32 v[184:185], v[184:185], v[224:225], v[226:227] op_sel:[1,1,0] op_sel_hi:[0,1,1] neg_lo:[1,0,0]
	v_pk_mul_f32 v[226:227], v[220:221], v[184:185] op_sel_hi:[1,0]
	v_pk_fma_f32 v[220:221], v[220:221], v[184:185], v[226:227] op_sel:[1,1,0] op_sel_hi:[0,1,1] neg_hi:[1,0,0]
	v_pk_mul_f32 v[226:227], v[184:185], v[224:225] op_sel_hi:[1,0]
	v_pk_fma_f32 v[184:185], v[184:185], v[224:225], v[226:227] op_sel:[1,1,0] op_sel_hi:[0,1,1] neg_lo:[1,0,0]
	v_pk_mul_f32 v[226:227], v[216:217], v[184:185] op_sel_hi:[1,0]
	v_pk_fma_f32 v[216:217], v[216:217], v[184:185], v[226:227] op_sel:[1,1,0] op_sel_hi:[0,1,1] neg_hi:[1,0,0]
	v_pk_mul_f32 v[226:227], v[184:185], v[224:225] op_sel_hi:[1,0]
	v_pk_fma_f32 v[184:185], v[184:185], v[224:225], v[226:227] op_sel:[1,1,0] op_sel_hi:[0,1,1] neg_lo:[1,0,0]
	v_pk_mul_f32 v[226:227], v[212:213], v[184:185] op_sel_hi:[1,0]
	v_pk_fma_f32 v[212:213], v[212:213], v[184:185], v[226:227] op_sel:[1,1,0] op_sel_hi:[0,1,1] neg_hi:[1,0,0]
	v_pk_mul_f32 v[226:227], v[184:185], v[224:225] op_sel_hi:[1,0]
	v_pk_fma_f32 v[184:185], v[184:185], v[224:225], v[226:227] op_sel:[1,1,0] op_sel_hi:[0,1,1] neg_lo:[1,0,0]
	v_pk_mul_f32 v[226:227], v[222:223], v[184:185] op_sel_hi:[1,0]
	v_pk_fma_f32 v[222:223], v[222:223], v[184:185], v[226:227] op_sel:[1,1,0] op_sel_hi:[0,1,1] neg_hi:[1,0,0]
	v_pk_mul_f32 v[226:227], v[184:185], v[224:225] op_sel_hi:[1,0]
	v_pk_fma_f32 v[184:185], v[184:185], v[224:225], v[226:227] op_sel:[1,1,0] op_sel_hi:[0,1,1] neg_lo:[1,0,0]
	v_pk_mul_f32 v[226:227], v[218:219], v[184:185] op_sel_hi:[1,0]
	v_pk_fma_f32 v[218:219], v[218:219], v[184:185], v[226:227] op_sel:[1,1,0] op_sel_hi:[0,1,1] neg_hi:[1,0,0]
	v_pk_mul_f32 v[226:227], v[184:185], v[224:225] op_sel_hi:[1,0]
	v_pk_fma_f32 v[184:185], v[184:185], v[224:225], v[226:227] op_sel:[1,1,0] op_sel_hi:[0,1,1] neg_lo:[1,0,0]
	v_pk_mul_f32 v[226:227], v[186:187], v[184:185] op_sel_hi:[1,0]
	v_pk_fma_f32 v[186:187], v[186:187], v[184:185], v[226:227] op_sel:[1,1,0] op_sel_hi:[0,1,1] neg_hi:[1,0,0]
	v_pk_mul_f32 v[226:227], v[184:185], v[224:225] op_sel_hi:[1,0]
	v_pk_fma_f32 v[184:185], v[184:185], v[224:225], v[226:227] op_sel:[1,1,0] op_sel_hi:[0,1,1] neg_lo:[1,0,0]
	v_pk_mul_f32 v[226:227], v[182:183], v[184:185] op_sel_hi:[1,0]
	v_pk_fma_f32 v[182:183], v[182:183], v[184:185], v[226:227] op_sel:[1,1,0] op_sel_hi:[0,1,1] neg_hi:[1,0,0]
	v_pk_mul_f32 v[226:227], v[184:185], v[224:225] op_sel_hi:[1,0]
	v_pk_fma_f32 v[184:185], v[184:185], v[224:225], v[226:227] op_sel:[1,1,0] op_sel_hi:[0,1,1] neg_lo:[1,0,0]
	v_pk_mul_f32 v[226:227], v[192:193], v[184:185] op_sel_hi:[1,0]
	v_pk_fma_f32 v[192:193], v[192:193], v[184:185], v[226:227] op_sel:[1,1,0] op_sel_hi:[0,1,1] neg_hi:[1,0,0]
	v_pk_mul_f32 v[226:227], v[184:185], v[224:225] op_sel_hi:[1,0]
	v_pk_fma_f32 v[184:185], v[184:185], v[224:225], v[226:227] op_sel:[1,1,0] op_sel_hi:[0,1,1] neg_lo:[1,0,0]
	v_pk_mul_f32 v[226:227], v[190:191], v[184:185] op_sel_hi:[1,0]
	v_pk_fma_f32 v[190:191], v[190:191], v[184:185], v[226:227] op_sel:[1,1,0] op_sel_hi:[0,1,1] neg_hi:[1,0,0]
	v_pk_mul_f32 v[226:227], v[184:185], v[224:225] op_sel_hi:[1,0]
	v_pk_fma_f32 v[184:185], v[184:185], v[224:225], v[226:227] op_sel:[1,1,0] op_sel_hi:[0,1,1] neg_lo:[1,0,0]
	v_pk_mul_f32 v[226:227], v[210:211], v[184:185] op_sel_hi:[1,0]
	v_pk_fma_f32 v[210:211], v[210:211], v[184:185], v[226:227] op_sel:[1,1,0] op_sel_hi:[0,1,1] neg_hi:[1,0,0]
	v_pk_mul_f32 v[226:227], v[184:185], v[224:225] op_sel_hi:[1,0]
	v_pk_fma_f32 v[184:185], v[184:185], v[224:225], v[226:227] op_sel:[1,1,0] op_sel_hi:[0,1,1] neg_lo:[1,0,0]
	v_pk_mul_f32 v[226:227], v[176:177], v[184:185] op_sel_hi:[1,0]
	v_pk_fma_f32 v[176:177], v[176:177], v[184:185], v[226:227] op_sel:[1,1,0] op_sel_hi:[0,1,1] neg_hi:[1,0,0]
	v_pk_mul_f32 v[226:227], v[184:185], v[224:225] op_sel_hi:[1,0]
	v_pk_fma_f32 v[184:185], v[184:185], v[224:225], v[226:227] op_sel:[1,1,0] op_sel_hi:[0,1,1] neg_lo:[1,0,0]
	v_pk_mul_f32 v[224:225], v[180:181], v[184:185] op_sel_hi:[1,0]
	v_pk_fma_f32 v[180:181], v[180:181], v[184:185], v[224:225] op_sel:[1,1,0] op_sel_hi:[0,1,1] neg_hi:[1,0,0]
	v_lshlrev_b32_e32 v224, 3, v38
	v_add3_u32 v184, 0, v228, v224
	ds_write2st64_b64 v184, v[188:189], v[178:179] offset1:18
	ds_write2st64_b64 v184, v[194:195], v[214:215] offset0:36 offset1:54
	ds_write2st64_b64 v184, v[220:221], v[216:217] offset0:72 offset1:90
	ds_write2st64_b64 v184, v[212:213], v[222:223] offset0:108 offset1:126
	v_add_u32_e32 v178, 0x12000, v184
	ds_write_b64 v178, v[218:219]
	v_add_u32_e32 v178, 0x14400, v184
	ds_write_b64 v178, v[186:187]
	v_add_u32_e32 v178, 0x16800, v184
	ds_write_b64 v178, v[182:183]
	v_add_u32_e32 v178, 0x18c00, v184
	ds_write_b64 v178, v[192:193]
	v_add_u32_e32 v178, 0x1b000, v184
	ds_write_b64 v178, v[190:191]
	v_add_u32_e32 v178, 0x1d400, v184
	ds_write_b64 v178, v[210:211]
	v_add_u32_e32 v178, 0x1f800, v184
	ds_write_b64 v178, v[176:177]
	v_add_u32_e32 v176, 0x21c00, v184
	v_add_u32_e32 v38, 0x200, v38
	v_pk_mul_f32 v[186:187], v[84:85], v[168:169] op_sel_hi:[1,0]
	ds_write_b64 v176, v[180:181]
	v_and_b32_e32 v214, -8, v38
	v_pk_add_f32 v[176:177], v[72:73], 0 op_sel_hi:[1,0]
	v_pk_add_f32 v[178:179], v[76:77], 0 op_sel_hi:[1,0]
	v_pk_mul_f32 v[180:181], v[76:77], v[166:167] op_sel_hi:[1,0]
	v_pk_fma_f32 v[168:169], v[84:85], v[168:169], v[186:187] op_sel:[1,1,0] op_sel_hi:[0,1,1] neg_hi:[1,0,0]
	v_pk_add_f32 v[186:187], v[88:89], 0 op_sel_hi:[1,0]
	v_pk_add_f32 v[188:189], v[92:93], 0 op_sel_hi:[1,0]
	v_pk_mul_f32 v[190:191], v[92:93], v[170:171] op_sel_hi:[1,0]
	v_pk_mul_f32 v[210:211], v[100:101], v[174:175] op_sel_hi:[1,0]
	v_cvt_f32_i32_e32 v38, v38
	v_pk_fma_f32 v[166:167], v[76:77], v[166:167], v[180:181] op_sel:[1,1,0] op_sel_hi:[0,1,1] neg_hi:[1,0,0]
	v_pk_add_f32 v[180:181], v[80:81], 0 op_sel_hi:[1,0]
	v_pk_mul_f32 v[182:183], v[80:81], v[162:163] op_sel_hi:[1,0]
	v_pk_add_f32 v[184:185], v[84:85], 0 op_sel_hi:[1,0]
	v_pk_fma_f32 v[170:171], v[92:93], v[170:171], v[190:191] op_sel:[1,1,0] op_sel_hi:[0,1,1] neg_hi:[1,0,0]
	v_pk_add_f32 v[190:191], v[96:97], 0 op_sel_hi:[1,0]
	v_pk_add_f32 v[194:195], v[100:101], 0 op_sel_hi:[1,0]
	v_pk_fma_f32 v[174:175], v[100:101], v[174:175], v[210:211] op_sel:[1,1,0] op_sel_hi:[0,1,1] neg_hi:[1,0,0]
	v_pk_add_f32 v[210:211], v[186:187], v[176:177]
	v_pk_add_f32 v[176:177], v[176:177], v[186:187] neg_lo:[0,1] neg_hi:[0,1]
	v_pk_add_f32 v[186:187], v[188:189], v[178:179]
	v_pk_add_f32 v[178:179], v[178:179], v[188:189] neg_lo:[0,1] neg_hi:[0,1]
	v_pk_fma_f32 v[182:183], v[80:81], v[162:163], v[182:183] op_sel:[1,1,0] op_sel_hi:[0,1,1] neg_hi:[1,0,0]
	v_pk_mul_f32 v[192:193], v[96:97], v[164:165] op_sel_hi:[1,0]
	v_pk_add_f32 v[212:213], v[166:167], v[170:171]
	v_pk_mul_f32 v[188:189], v[178:179], v[162:163] op_sel_hi:[1,0]
	v_pk_add_f32 v[166:167], v[166:167], v[170:171] neg_lo:[0,1] neg_hi:[0,1]
	v_pk_fma_f32 v[178:179], v[178:179], v[162:163], v[188:189] op_sel:[1,1,0] op_sel_hi:[0,1,1] neg_hi:[1,0,0]
	v_pk_add_f32 v[188:189], v[190:191], v[180:181]
	v_pk_add_f32 v[180:181], v[180:181], v[190:191] op_sel:[1,1] op_sel_hi:[0,0] neg_lo:[0,1] neg_hi:[1,0]
	v_pk_add_f32 v[190:191], v[194:195], v[184:185]
	v_pk_add_f32 v[184:185], v[184:185], v[194:195] neg_lo:[0,1] neg_hi:[0,1]
	v_pk_mul_f32 v[170:171], v[166:167], v[162:163] op_sel_hi:[1,0]
	v_pk_fma_f32 v[192:193], v[96:97], v[164:165], v[192:193] op_sel:[1,1,0] op_sel_hi:[0,1,1] neg_hi:[1,0,0]
	v_mul_f32_e32 v38, 0x38800000, v38
	v_pk_mul_f32 v[194:195], v[184:185], v[164:165] op_sel_hi:[1,0]
	v_pk_fma_f32 v[162:163], v[166:167], v[162:163], v[170:171] op_sel:[1,1,0] op_sel_hi:[0,1,1] neg_hi:[1,0,0]
	v_pk_add_f32 v[166:167], v[182:183], v[192:193]
	v_pk_fma_f32 v[184:185], v[184:185], v[164:165], v[194:195] op_sel:[1,1,0] op_sel_hi:[0,1,1] neg_hi:[1,0,0]
	v_pk_add_f32 v[194:195], v[72:73], v[172:173]
	v_pk_add_f32 v[172:173], v[72:73], v[172:173] neg_lo:[0,1] neg_hi:[0,1]
	v_pk_add_f32 v[170:171], v[182:183], v[192:193] op_sel:[1,1] op_sel_hi:[0,0] neg_lo:[0,1] neg_hi:[1,0]
	v_pk_add_f32 v[182:183], v[168:169], v[174:175]
	v_pk_add_f32 v[168:169], v[168:169], v[174:175] neg_lo:[0,1] neg_hi:[0,1]
	v_pk_add_f32 v[192:193], v[212:213], v[182:183]
	v_pk_mul_f32 v[174:175], v[168:169], v[164:165] op_sel_hi:[1,0]
	v_pk_add_f32 v[182:183], v[212:213], v[182:183] op_sel:[1,1] op_sel_hi:[0,0] neg_lo:[0,1] neg_hi:[1,0]
	v_pk_fma_f32 v[164:165], v[168:169], v[164:165], v[174:175] op_sel:[1,1,0] op_sel_hi:[0,1,1] neg_hi:[1,0,0]
	v_pk_add_f32 v[168:169], v[188:189], v[210:211]
	v_pk_add_f32 v[174:175], v[210:211], v[188:189] neg_lo:[0,1] neg_hi:[0,1]
	v_pk_add_f32 v[188:189], v[190:191], v[186:187]
	v_pk_add_f32 v[186:187], v[186:187], v[190:191] op_sel:[1,1] op_sel_hi:[0,0] neg_lo:[0,1] neg_hi:[1,0]
	v_pk_add_f32 v[190:191], v[176:177], v[180:181]
	v_pk_add_f32 v[176:177], v[176:177], v[180:181] neg_lo:[0,1] neg_hi:[0,1]
	v_pk_add_f32 v[180:181], v[178:179], v[184:185]
	v_pk_add_f32 v[178:179], v[178:179], v[184:185] op_sel:[1,1] op_sel_hi:[0,0] neg_lo:[0,1] neg_hi:[1,0]
	v_pk_add_f32 v[184:185], v[194:195], v[166:167]
	v_pk_add_f32 v[166:167], v[194:195], v[166:167] neg_lo:[0,1] neg_hi:[0,1]
	v_pk_add_f32 v[194:195], v[172:173], v[170:171]
	v_pk_add_f32 v[170:171], v[172:173], v[170:171] neg_lo:[0,1] neg_hi:[0,1]
	v_pk_add_f32 v[172:173], v[162:163], v[164:165]
	v_pk_add_f32 v[162:163], v[162:163], v[164:165] op_sel:[1,1] op_sel_hi:[0,0] neg_lo:[0,1] neg_hi:[1,0]
	v_pk_add_f32 v[164:165], v[188:189], v[168:169]
	v_pk_add_f32 v[168:169], v[168:169], v[188:189] neg_lo:[0,1] neg_hi:[0,1]
	v_pk_add_f32 v[188:189], v[174:175], v[186:187]
	v_pk_add_f32 v[174:175], v[174:175], v[186:187] neg_lo:[0,1] neg_hi:[0,1]
	v_pk_add_f32 v[186:187], v[190:191], v[180:181]
	v_pk_add_f32 v[180:181], v[190:191], v[180:181] neg_lo:[0,1] neg_hi:[0,1]
	v_pk_add_f32 v[190:191], v[176:177], v[178:179]
	v_pk_add_f32 v[176:177], v[176:177], v[178:179] neg_lo:[0,1] neg_hi:[0,1]
	v_pk_add_f32 v[178:179], v[184:185], v[192:193]
	v_pk_add_f32 v[184:185], v[184:185], v[192:193] neg_lo:[0,1] neg_hi:[0,1]
	v_pk_add_f32 v[192:193], v[166:167], v[182:183]
	v_pk_add_f32 v[166:167], v[166:167], v[182:183] neg_lo:[0,1] neg_hi:[0,1]
	v_pk_add_f32 v[182:183], v[194:195], v[172:173]
	v_cos_f32_e32 v210, v38
	v_sin_f32_e32 v211, v38
	v_pk_add_f32 v[172:173], v[194:195], v[172:173] neg_lo:[0,1] neg_hi:[0,1]
	v_pk_add_f32 v[194:195], v[170:171], v[162:163]
	v_pk_add_f32 v[162:163], v[170:171], v[162:163] neg_lo:[0,1] neg_hi:[0,1]
	v_pk_mul_f32 v[170:171], v[178:179], v[210:211] op_sel_hi:[1,0]
	v_add3_u32 v38, 0, v214, v224
	v_pk_fma_f32 v[170:171], v[178:179], v[210:211], v[170:171] op_sel:[1,1,0] op_sel_hi:[0,1,1] neg_hi:[1,0,0]
	v_pk_mul_f32 v[178:179], v[210:211], v[210:211] op_sel_hi:[1,0]
	v_pk_fma_f32 v[178:179], v[210:211], v[210:211], v[178:179] op_sel:[1,1,0] op_sel_hi:[0,1,1] neg_lo:[1,0,0]
	v_pk_mul_f32 v[212:213], v[186:187], v[178:179] op_sel_hi:[1,0]
	v_pk_fma_f32 v[186:187], v[186:187], v[178:179], v[212:213] op_sel:[1,1,0] op_sel_hi:[0,1,1] neg_hi:[1,0,0]
	v_pk_mul_f32 v[212:213], v[178:179], v[210:211] op_sel_hi:[1,0]
	v_pk_fma_f32 v[178:179], v[178:179], v[210:211], v[212:213] op_sel:[1,1,0] op_sel_hi:[0,1,1] neg_lo:[1,0,0]
	v_pk_mul_f32 v[212:213], v[182:183], v[178:179] op_sel_hi:[1,0]
	v_pk_fma_f32 v[182:183], v[182:183], v[178:179], v[212:213] op_sel:[1,1,0] op_sel_hi:[0,1,1] neg_hi:[1,0,0]
	v_pk_mul_f32 v[212:213], v[178:179], v[210:211] op_sel_hi:[1,0]
	v_pk_fma_f32 v[178:179], v[178:179], v[210:211], v[212:213] op_sel:[1,1,0] op_sel_hi:[0,1,1] neg_lo:[1,0,0]
	v_pk_mul_f32 v[212:213], v[188:189], v[178:179] op_sel_hi:[1,0]
	v_pk_fma_f32 v[188:189], v[188:189], v[178:179], v[212:213] op_sel:[1,1,0] op_sel_hi:[0,1,1] neg_hi:[1,0,0]
	v_pk_mul_f32 v[212:213], v[178:179], v[210:211] op_sel_hi:[1,0]
	v_pk_fma_f32 v[178:179], v[178:179], v[210:211], v[212:213] op_sel:[1,1,0] op_sel_hi:[0,1,1] neg_lo:[1,0,0]
	v_pk_mul_f32 v[212:213], v[192:193], v[178:179] op_sel_hi:[1,0]
	v_pk_fma_f32 v[192:193], v[192:193], v[178:179], v[212:213] op_sel:[1,1,0] op_sel_hi:[0,1,1] neg_hi:[1,0,0]
	v_pk_mul_f32 v[212:213], v[178:179], v[210:211] op_sel_hi:[1,0]
	v_pk_fma_f32 v[178:179], v[178:179], v[210:211], v[212:213] op_sel:[1,1,0] op_sel_hi:[0,1,1] neg_lo:[1,0,0]
	v_pk_mul_f32 v[212:213], v[190:191], v[178:179] op_sel_hi:[1,0]
	v_pk_fma_f32 v[190:191], v[190:191], v[178:179], v[212:213] op_sel:[1,1,0] op_sel_hi:[0,1,1] neg_hi:[1,0,0]
	v_pk_mul_f32 v[212:213], v[178:179], v[210:211] op_sel_hi:[1,0]
	v_pk_fma_f32 v[178:179], v[178:179], v[210:211], v[212:213] op_sel:[1,1,0] op_sel_hi:[0,1,1] neg_lo:[1,0,0]
	v_pk_mul_f32 v[212:213], v[194:195], v[178:179] op_sel_hi:[1,0]
	v_pk_fma_f32 v[194:195], v[194:195], v[178:179], v[212:213] op_sel:[1,1,0] op_sel_hi:[0,1,1] neg_hi:[1,0,0]
	v_pk_mul_f32 v[212:213], v[178:179], v[210:211] op_sel_hi:[1,0]
	v_pk_fma_f32 v[178:179], v[178:179], v[210:211], v[212:213] op_sel:[1,1,0] op_sel_hi:[0,1,1] neg_lo:[1,0,0]
	v_pk_mul_f32 v[212:213], v[168:169], v[178:179] op_sel_hi:[1,0]
	v_pk_fma_f32 v[168:169], v[168:169], v[178:179], v[212:213] op_sel:[1,1,0] op_sel_hi:[0,1,1] neg_hi:[1,0,0]
	v_pk_mul_f32 v[212:213], v[178:179], v[210:211] op_sel_hi:[1,0]
	v_pk_fma_f32 v[178:179], v[178:179], v[210:211], v[212:213] op_sel:[1,1,0] op_sel_hi:[0,1,1] neg_lo:[1,0,0]
	v_pk_mul_f32 v[212:213], v[184:185], v[178:179] op_sel_hi:[1,0]
	v_pk_fma_f32 v[184:185], v[184:185], v[178:179], v[212:213] op_sel:[1,1,0] op_sel_hi:[0,1,1] neg_hi:[1,0,0]
	v_pk_mul_f32 v[212:213], v[178:179], v[210:211] op_sel_hi:[1,0]
	v_pk_fma_f32 v[178:179], v[178:179], v[210:211], v[212:213] op_sel:[1,1,0] op_sel_hi:[0,1,1] neg_lo:[1,0,0]
	v_pk_mul_f32 v[212:213], v[180:181], v[178:179] op_sel_hi:[1,0]
	v_pk_fma_f32 v[180:181], v[180:181], v[178:179], v[212:213] op_sel:[1,1,0] op_sel_hi:[0,1,1] neg_hi:[1,0,0]
	v_pk_mul_f32 v[212:213], v[178:179], v[210:211] op_sel_hi:[1,0]
	v_pk_fma_f32 v[178:179], v[178:179], v[210:211], v[212:213] op_sel:[1,1,0] op_sel_hi:[0,1,1] neg_lo:[1,0,0]
	v_pk_mul_f32 v[212:213], v[172:173], v[178:179] op_sel_hi:[1,0]
	v_pk_fma_f32 v[172:173], v[172:173], v[178:179], v[212:213] op_sel:[1,1,0] op_sel_hi:[0,1,1] neg_hi:[1,0,0]
	v_pk_mul_f32 v[212:213], v[178:179], v[210:211] op_sel_hi:[1,0]
	v_pk_fma_f32 v[178:179], v[178:179], v[210:211], v[212:213] op_sel:[1,1,0] op_sel_hi:[0,1,1] neg_lo:[1,0,0]
	v_pk_mul_f32 v[212:213], v[174:175], v[178:179] op_sel_hi:[1,0]
	v_pk_fma_f32 v[174:175], v[174:175], v[178:179], v[212:213] op_sel:[1,1,0] op_sel_hi:[0,1,1] neg_hi:[1,0,0]
	v_pk_mul_f32 v[212:213], v[178:179], v[210:211] op_sel_hi:[1,0]
	v_pk_fma_f32 v[178:179], v[178:179], v[210:211], v[212:213] op_sel:[1,1,0] op_sel_hi:[0,1,1] neg_lo:[1,0,0]
	v_pk_mul_f32 v[212:213], v[166:167], v[178:179] op_sel_hi:[1,0]
	v_pk_fma_f32 v[166:167], v[166:167], v[178:179], v[212:213] op_sel:[1,1,0] op_sel_hi:[0,1,1] neg_hi:[1,0,0]
	v_pk_mul_f32 v[212:213], v[178:179], v[210:211] op_sel_hi:[1,0]
	v_pk_fma_f32 v[178:179], v[178:179], v[210:211], v[212:213] op_sel:[1,1,0] op_sel_hi:[0,1,1] neg_lo:[1,0,0]
	v_pk_mul_f32 v[212:213], v[176:177], v[178:179] op_sel_hi:[1,0]
	v_pk_fma_f32 v[176:177], v[176:177], v[178:179], v[212:213] op_sel:[1,1,0] op_sel_hi:[0,1,1] neg_hi:[1,0,0]
	v_pk_mul_f32 v[212:213], v[178:179], v[210:211] op_sel_hi:[1,0]
	v_pk_fma_f32 v[178:179], v[178:179], v[210:211], v[212:213] op_sel:[1,1,0] op_sel_hi:[0,1,1] neg_lo:[1,0,0]
	v_pk_mul_f32 v[210:211], v[162:163], v[178:179] op_sel_hi:[1,0]
	v_pk_fma_f32 v[162:163], v[162:163], v[178:179], v[210:211] op_sel:[1,1,0] op_sel_hi:[0,1,1] neg_hi:[1,0,0]
	v_add_u32_e32 v178, 0x1000, v38
	ds_write2st64_b64 v38, v[164:165], v[170:171] offset0:8 offset1:26
	ds_write2st64_b64 v38, v[186:187], v[182:183] offset0:44 offset1:62
	ds_write2st64_b64 v38, v[188:189], v[192:193] offset0:80 offset1:98
	ds_write_b64 v38, v[190:191] offset:59392
	ds_write_b64 v178, v[194:195] offset:64512
	v_add_u32_e32 v164, 0x13000, v38
	ds_write_b64 v164, v[168:169]
	v_add_u32_e32 v164, 0x15400, v38
	ds_write_b64 v164, v[184:185]
	v_add_u32_e32 v164, 0x17800, v38
	ds_write_b64 v164, v[180:181]
	v_add_u32_e32 v164, 0x19c00, v38
	ds_write_b64 v164, v[172:173]
	v_add_u32_e32 v164, 0x1c000, v38
	ds_write_b64 v164, v[174:175]
	v_add_u32_e32 v164, 0x1e400, v38
	ds_write_b64 v164, v[166:167]
	v_add_u32_e32 v164, 0x20800, v38
	v_add_u32_e32 v38, 0x22c00, v38
	ds_write_b64 v164, v[176:177]
	ds_write_b64 v38, v[162:163]
	v_mov_b32_e32 v164, v204
	s_waitcnt lgkmcnt(0)
	s_barrier
	s_nop 0
	v_and_b32_e32 v38, 63, v164
	v_cvt_f32_ubyte0_e32 v162, v38
	v_mul_f32_e32 v163, 0x3a800000, v162
	v_cos_f32_e32 v162, v163
	v_sin_f32_e32 v163, v163
	v_lshlrev_b32_e32 v210, 4, v164
.LBB0_764:
	v_add_u32_e32 v164, s86, v210
	v_and_b32_e32 v164, 0xfffffc00, v164
	v_or_b32_e32 v165, v164, v38
	v_bitop3_b32 v164, v164, s97, v38 bitop3:0xc8
	v_lshlrev_b32_e32 v165, 3, v165
	v_add3_u32 v211, 0, v164, v165
	v_add_u32_e32 v212, 0x800, v211
	v_add_u32_e32 v213, 0x1000, v211
	ds_read2_b64 v[164:167], v211 offset1:72
	ds_read2_b64 v[168:171], v211 offset0:144 offset1:216
	ds_read2_b64 v[172:175], v212 offset0:32 offset1:104
	ds_read2_b64 v[176:179], v212 offset0:176 offset1:248
	ds_read2_b64 v[180:183], v213 offset0:64 offset1:136
	v_add_u32_e32 v214, 0x1400, v211
	ds_read2_b64 v[184:187], v214 offset0:80 offset1:152
	v_add_u32_e32 v215, 0x1800, v211
	ds_read2_b64 v[188:191], v215 offset0:96 offset1:168
	v_add_u32_e32 v216, 0x1c00, v211
	ds_read2_b64 v[192:195], v216 offset0:112 offset1:184
	s_waitcnt lgkmcnt(3)
	v_pk_add_f32 v[218:219], v[164:165], v[180:181]
	v_pk_add_f32 v[164:165], v[164:165], v[180:181] neg_lo:[0,1] neg_hi:[0,1]
	v_pk_add_f32 v[180:181], v[166:167], v[182:183]
	v_pk_add_f32 v[166:167], v[166:167], v[182:183] neg_lo:[0,1] neg_hi:[0,1]
	v_mov_b64_e32 v[182:183], s[4:5]
	v_pk_mul_f32 v[220:221], v[166:167], v[182:183] op_sel_hi:[1,0]
	s_movk_i32 s86, 0x2000
	v_pk_fma_f32 v[166:167], v[166:167], v[182:183], v[220:221] op_sel:[1,1,0] op_sel_hi:[0,1,1] neg_hi:[1,0,0]
	s_waitcnt lgkmcnt(2)
	v_pk_add_f32 v[182:183], v[168:169], v[184:185]
	v_pk_add_f32 v[168:169], v[168:169], v[184:185] neg_lo:[0,1] neg_hi:[0,1]
	v_mov_b64_e32 v[184:185], s[6:7]
	v_pk_mul_f32 v[220:221], v[168:169], v[184:185] op_sel_hi:[1,0]
	s_and_b64 vcc, exec, s[84:85]
	v_pk_fma_f32 v[168:169], v[168:169], v[184:185], v[220:221] op_sel:[1,1,0] op_sel_hi:[0,1,1] neg_hi:[1,0,0]
	v_pk_add_f32 v[220:221], v[170:171], v[186:187]
	v_pk_add_f32 v[170:171], v[170:171], v[186:187] neg_lo:[0,1] neg_hi:[0,1]
	v_mov_b64_e32 v[186:187], s[10:11]
	v_pk_mul_f32 v[222:223], v[170:171], v[186:187] op_sel_hi:[1,0]
	s_mov_b64 s[84:85], 0
	v_pk_fma_f32 v[170:171], v[170:171], v[186:187], v[222:223] op_sel:[1,1,0] op_sel_hi:[0,1,1] neg_hi:[1,0,0]
	s_waitcnt lgkmcnt(1)
	v_pk_add_f32 v[186:187], v[172:173], v[188:189]
	v_pk_add_f32 v[172:173], v[172:173], v[188:189] op_sel:[1,1] op_sel_hi:[0,0] neg_lo:[0,1] neg_hi:[1,0]
	v_pk_add_f32 v[188:189], v[174:175], v[190:191]
	v_pk_add_f32 v[174:175], v[174:175], v[190:191] neg_lo:[0,1] neg_hi:[0,1]
	v_mov_b64_e32 v[190:191], s[12:13]
	v_pk_mul_f32 v[222:223], v[174:175], v[190:191] op_sel_hi:[1,0]
	v_pk_fma_f32 v[174:175], v[174:175], v[190:191], v[222:223] op_sel:[1,1,0] op_sel_hi:[0,1,1] neg_hi:[1,0,0]
	s_waitcnt lgkmcnt(0)
	v_pk_add_f32 v[190:191], v[176:177], v[192:193]
	v_pk_add_f32 v[176:177], v[176:177], v[192:193] neg_lo:[0,1] neg_hi:[0,1]
	v_mov_b64_e32 v[192:193], s[14:15]
	v_pk_mul_f32 v[222:223], v[176:177], v[192:193] op_sel_hi:[1,0]
	v_pk_fma_f32 v[176:177], v[176:177], v[192:193], v[222:223] op_sel:[1,1,0] op_sel_hi:[0,1,1] neg_hi:[1,0,0]
	v_pk_add_f32 v[222:223], v[178:179], v[194:195]
	v_pk_add_f32 v[178:179], v[178:179], v[194:195] neg_lo:[0,1] neg_hi:[0,1]
	v_mov_b64_e32 v[194:195], s[16:17]
	v_pk_mul_f32 v[224:225], v[178:179], v[194:195] op_sel_hi:[1,0]
	v_pk_fma_f32 v[178:179], v[178:179], v[194:195], v[224:225] op_sel:[1,1,0] op_sel_hi:[0,1,1] neg_hi:[1,0,0]
	v_pk_add_f32 v[194:195], v[218:219], v[186:187]
	v_pk_add_f32 v[186:187], v[218:219], v[186:187] neg_lo:[0,1] neg_hi:[0,1]
	v_pk_add_f32 v[218:219], v[180:181], v[188:189]
	v_pk_add_f32 v[180:181], v[180:181], v[188:189] neg_lo:[0,1] neg_hi:[0,1]
	s_nop 0
	v_pk_mul_f32 v[188:189], v[180:181], v[184:185] op_sel_hi:[1,0]
	v_pk_fma_f32 v[180:181], v[180:181], v[184:185], v[188:189] op_sel:[1,1,0] op_sel_hi:[0,1,1] neg_hi:[1,0,0]
	v_pk_add_f32 v[188:189], v[182:183], v[190:191]
	v_pk_add_f32 v[182:183], v[182:183], v[190:191] op_sel:[1,1] op_sel_hi:[0,0] neg_lo:[0,1] neg_hi:[1,0]
	v_pk_add_f32 v[190:191], v[220:221], v[222:223]
	v_pk_add_f32 v[220:221], v[220:221], v[222:223] neg_lo:[0,1] neg_hi:[0,1]
	s_nop 0
	v_pk_mul_f32 v[222:223], v[220:221], v[192:193] op_sel_hi:[1,0]
	v_pk_fma_f32 v[220:221], v[220:221], v[192:193], v[222:223] op_sel:[1,1,0] op_sel_hi:[0,1,1] neg_hi:[1,0,0]
	v_pk_add_f32 v[222:223], v[164:165], v[172:173]
	v_pk_add_f32 v[164:165], v[164:165], v[172:173] neg_lo:[0,1] neg_hi:[0,1]
	v_pk_add_f32 v[172:173], v[166:167], v[174:175]
	v_pk_add_f32 v[166:167], v[166:167], v[174:175] neg_lo:[0,1] neg_hi:[0,1]
	s_nop 0
	v_pk_mul_f32 v[174:175], v[166:167], v[184:185] op_sel_hi:[1,0]
	v_pk_fma_f32 v[166:167], v[166:167], v[184:185], v[174:175] op_sel:[1,1,0] op_sel_hi:[0,1,1] neg_hi:[1,0,0]
	v_pk_add_f32 v[174:175], v[168:169], v[176:177]
	v_pk_add_f32 v[168:169], v[168:169], v[176:177] op_sel:[1,1] op_sel_hi:[0,0] neg_lo:[0,1] neg_hi:[1,0]
	v_pk_add_f32 v[176:177], v[170:171], v[178:179]
	v_pk_add_f32 v[170:171], v[170:171], v[178:179] neg_lo:[0,1] neg_hi:[0,1]
	v_pk_add_f32 v[184:185], v[194:195], v[188:189] neg_lo:[0,1] neg_hi:[0,1]
	v_pk_mul_f32 v[178:179], v[170:171], v[192:193] op_sel_hi:[1,0]
	v_pk_add_f32 v[224:225], v[164:165], v[168:169]
	v_pk_fma_f32 v[170:171], v[170:171], v[192:193], v[178:179] op_sel:[1,1,0] op_sel_hi:[0,1,1] neg_hi:[1,0,0]
	v_pk_add_f32 v[178:179], v[194:195], v[188:189]
	v_pk_add_f32 v[188:189], v[218:219], v[190:191]
	v_pk_add_f32 v[190:191], v[218:219], v[190:191] op_sel:[1,1] op_sel_hi:[0,0] neg_lo:[0,1] neg_hi:[1,0]
	v_pk_add_f32 v[194:195], v[186:187], v[182:183]
	v_pk_add_f32 v[218:219], v[180:181], v[220:221]
	v_pk_add_f32 v[180:181], v[180:181], v[220:221] op_sel:[1,1] op_sel_hi:[0,0] neg_lo:[0,1] neg_hi:[1,0]
	v_pk_add_f32 v[220:221], v[222:223], v[174:175]
	v_pk_add_f32 v[174:175], v[222:223], v[174:175] neg_lo:[0,1] neg_hi:[0,1]
	v_pk_add_f32 v[222:223], v[172:173], v[176:177]
	v_pk_add_f32 v[172:173], v[172:173], v[176:177] op_sel:[1,1] op_sel_hi:[0,0] neg_lo:[0,1] neg_hi:[1,0]
	v_pk_add_f32 v[182:183], v[186:187], v[182:183] neg_lo:[0,1] neg_hi:[0,1]
	v_pk_add_f32 v[226:227], v[164:165], v[168:169] neg_lo:[0,1] neg_hi:[0,1]
	v_pk_add_f32 v[186:187], v[184:185], v[190:191]
	v_pk_add_f32 v[168:169], v[184:185], v[190:191] neg_lo:[0,1] neg_hi:[0,1]
	v_pk_add_f32 v[192:193], v[194:195], v[218:219]
	v_pk_add_f32 v[176:177], v[194:195], v[218:219] neg_lo:[0,1] neg_hi:[0,1]
	v_pk_add_f32 v[218:219], v[220:221], v[222:223]
	v_pk_add_f32 v[190:191], v[174:175], v[172:173]
	v_pk_add_f32 v[174:175], v[174:175], v[172:173] neg_lo:[0,1] neg_hi:[0,1]
	v_pk_mul_f32 v[172:173], v[218:219], v[162:163] op_sel_hi:[1,0]
	v_pk_add_f32 v[228:229], v[166:167], v[170:171]
	v_pk_fma_f32 v[172:173], v[218:219], v[162:163], v[172:173] op_sel:[1,1,0] op_sel_hi:[0,1,1] neg_hi:[1,0,0]
	v_pk_mul_f32 v[218:219], v[162:163], v[162:163] op_sel_hi:[1,0]
	v_pk_add_f32 v[170:171], v[166:167], v[170:171] op_sel:[1,1] op_sel_hi:[0,0] neg_lo:[0,1] neg_hi:[1,0]
	v_pk_add_f32 v[184:185], v[182:183], v[180:181]
	v_pk_add_f32 v[166:167], v[182:183], v[180:181] neg_lo:[0,1] neg_hi:[0,1]
	v_pk_add_f32 v[182:183], v[220:221], v[222:223] neg_lo:[0,1] neg_hi:[0,1]
	v_pk_fma_f32 v[218:219], v[162:163], v[162:163], v[218:219] op_sel:[1,1,0] op_sel_hi:[0,1,1] neg_lo:[1,0,0]
	v_pk_add_f32 v[194:195], v[224:225], v[228:229]
	v_pk_mul_f32 v[220:221], v[192:193], v[218:219] op_sel_hi:[1,0]
	v_pk_add_f32 v[164:165], v[178:179], v[188:189]
	v_pk_fma_f32 v[192:193], v[192:193], v[218:219], v[220:221] op_sel:[1,1,0] op_sel_hi:[0,1,1] neg_hi:[1,0,0]
	v_pk_mul_f32 v[220:221], v[218:219], v[162:163] op_sel_hi:[1,0]
	v_pk_add_f32 v[178:179], v[178:179], v[188:189] neg_lo:[0,1] neg_hi:[0,1]
	v_pk_fma_f32 v[218:219], v[218:219], v[162:163], v[220:221] op_sel:[1,1,0] op_sel_hi:[0,1,1] neg_lo:[1,0,0]
	v_pk_add_f32 v[188:189], v[226:227], v[170:171]
	v_pk_mul_f32 v[220:221], v[194:195], v[218:219] op_sel_hi:[1,0]
	v_pk_add_f32 v[180:181], v[224:225], v[228:229] neg_lo:[0,1] neg_hi:[0,1]
	v_pk_fma_f32 v[194:195], v[194:195], v[218:219], v[220:221] op_sel:[1,1,0] op_sel_hi:[0,1,1] neg_hi:[1,0,0]
	v_pk_mul_f32 v[220:221], v[218:219], v[162:163] op_sel_hi:[1,0]
	v_pk_add_f32 v[170:171], v[226:227], v[170:171] neg_lo:[0,1] neg_hi:[0,1]
	v_pk_fma_f32 v[218:219], v[218:219], v[162:163], v[220:221] op_sel:[1,1,0] op_sel_hi:[0,1,1] neg_lo:[1,0,0]
	v_pk_mul_f32 v[220:221], v[186:187], v[218:219] op_sel_hi:[1,0]
	v_pk_fma_f32 v[186:187], v[186:187], v[218:219], v[220:221] op_sel:[1,1,0] op_sel_hi:[0,1,1] neg_hi:[1,0,0]
	v_pk_mul_f32 v[220:221], v[218:219], v[162:163] op_sel_hi:[1,0]
	v_pk_fma_f32 v[218:219], v[218:219], v[162:163], v[220:221] op_sel:[1,1,0] op_sel_hi:[0,1,1] neg_lo:[1,0,0]
	v_pk_mul_f32 v[220:221], v[190:191], v[218:219] op_sel_hi:[1,0]
	v_pk_fma_f32 v[190:191], v[190:191], v[218:219], v[220:221] op_sel:[1,1,0] op_sel_hi:[0,1,1] neg_hi:[1,0,0]
	v_pk_mul_f32 v[220:221], v[218:219], v[162:163] op_sel_hi:[1,0]
	v_pk_fma_f32 v[218:219], v[218:219], v[162:163], v[220:221] op_sel:[1,1,0] op_sel_hi:[0,1,1] neg_lo:[1,0,0]
	v_pk_mul_f32 v[220:221], v[184:185], v[218:219] op_sel_hi:[1,0]
	v_pk_fma_f32 v[184:185], v[184:185], v[218:219], v[220:221] op_sel:[1,1,0] op_sel_hi:[0,1,1] neg_hi:[1,0,0]
	v_pk_mul_f32 v[220:221], v[218:219], v[162:163] op_sel_hi:[1,0]
	v_pk_fma_f32 v[218:219], v[218:219], v[162:163], v[220:221] op_sel:[1,1,0] op_sel_hi:[0,1,1] neg_lo:[1,0,0]
	v_pk_mul_f32 v[220:221], v[188:189], v[218:219] op_sel_hi:[1,0]
	v_pk_fma_f32 v[188:189], v[188:189], v[218:219], v[220:221] op_sel:[1,1,0] op_sel_hi:[0,1,1] neg_hi:[1,0,0]
	v_pk_mul_f32 v[220:221], v[218:219], v[162:163] op_sel_hi:[1,0]
	v_pk_fma_f32 v[218:219], v[218:219], v[162:163], v[220:221] op_sel:[1,1,0] op_sel_hi:[0,1,1] neg_lo:[1,0,0]
	v_pk_mul_f32 v[220:221], v[178:179], v[218:219] op_sel_hi:[1,0]
	v_pk_fma_f32 v[178:179], v[178:179], v[218:219], v[220:221] op_sel:[1,1,0] op_sel_hi:[0,1,1] neg_hi:[1,0,0]
	v_pk_mul_f32 v[220:221], v[218:219], v[162:163] op_sel_hi:[1,0]
	v_pk_fma_f32 v[218:219], v[218:219], v[162:163], v[220:221] op_sel:[1,1,0] op_sel_hi:[0,1,1] neg_lo:[1,0,0]
	v_pk_mul_f32 v[220:221], v[182:183], v[218:219] op_sel_hi:[1,0]
	v_pk_fma_f32 v[182:183], v[182:183], v[218:219], v[220:221] op_sel:[1,1,0] op_sel_hi:[0,1,1] neg_hi:[1,0,0]
	v_pk_mul_f32 v[220:221], v[218:219], v[162:163] op_sel_hi:[1,0]
	v_pk_fma_f32 v[218:219], v[218:219], v[162:163], v[220:221] op_sel:[1,1,0] op_sel_hi:[0,1,1] neg_lo:[1,0,0]
	v_pk_mul_f32 v[220:221], v[176:177], v[218:219] op_sel_hi:[1,0]
	v_pk_fma_f32 v[176:177], v[176:177], v[218:219], v[220:221] op_sel:[1,1,0] op_sel_hi:[0,1,1] neg_hi:[1,0,0]
	v_pk_mul_f32 v[220:221], v[218:219], v[162:163] op_sel_hi:[1,0]
	v_pk_fma_f32 v[218:219], v[218:219], v[162:163], v[220:221] op_sel:[1,1,0] op_sel_hi:[0,1,1] neg_lo:[1,0,0]
	v_pk_mul_f32 v[220:221], v[180:181], v[218:219] op_sel_hi:[1,0]
	v_pk_fma_f32 v[180:181], v[180:181], v[218:219], v[220:221] op_sel:[1,1,0] op_sel_hi:[0,1,1] neg_hi:[1,0,0]
	v_pk_mul_f32 v[220:221], v[218:219], v[162:163] op_sel_hi:[1,0]
	v_pk_fma_f32 v[218:219], v[218:219], v[162:163], v[220:221] op_sel:[1,1,0] op_sel_hi:[0,1,1] neg_lo:[1,0,0]
	v_pk_mul_f32 v[220:221], v[168:169], v[218:219] op_sel_hi:[1,0]
	v_pk_fma_f32 v[168:169], v[168:169], v[218:219], v[220:221] op_sel:[1,1,0] op_sel_hi:[0,1,1] neg_hi:[1,0,0]
	v_pk_mul_f32 v[220:221], v[218:219], v[162:163] op_sel_hi:[1,0]
	v_pk_fma_f32 v[218:219], v[218:219], v[162:163], v[220:221] op_sel:[1,1,0] op_sel_hi:[0,1,1] neg_lo:[1,0,0]
	v_pk_mul_f32 v[220:221], v[174:175], v[218:219] op_sel_hi:[1,0]
	v_pk_fma_f32 v[174:175], v[174:175], v[218:219], v[220:221] op_sel:[1,1,0] op_sel_hi:[0,1,1] neg_hi:[1,0,0]
	v_pk_mul_f32 v[220:221], v[218:219], v[162:163] op_sel_hi:[1,0]
	v_pk_fma_f32 v[218:219], v[218:219], v[162:163], v[220:221] op_sel:[1,1,0] op_sel_hi:[0,1,1] neg_lo:[1,0,0]
	v_pk_mul_f32 v[220:221], v[166:167], v[218:219] op_sel_hi:[1,0]
	v_pk_fma_f32 v[166:167], v[166:167], v[218:219], v[220:221] op_sel:[1,1,0] op_sel_hi:[0,1,1] neg_hi:[1,0,0]
	v_pk_mul_f32 v[220:221], v[218:219], v[162:163] op_sel_hi:[1,0]
	v_pk_fma_f32 v[218:219], v[218:219], v[162:163], v[220:221] op_sel:[1,1,0] op_sel_hi:[0,1,1] neg_lo:[1,0,0]
	v_pk_mul_f32 v[220:221], v[170:171], v[218:219] op_sel_hi:[1,0]
	v_pk_fma_f32 v[170:171], v[170:171], v[218:219], v[220:221] op_sel:[1,1,0] op_sel_hi:[0,1,1] neg_hi:[1,0,0]
	ds_write2_b64 v211, v[164:165], v[172:173] offset1:72
	ds_write2_b64 v211, v[192:193], v[194:195] offset0:144 offset1:216
	ds_write2_b64 v212, v[186:187], v[190:191] offset0:32 offset1:104
	ds_write2_b64 v212, v[184:185], v[188:189] offset0:176 offset1:248
	ds_write2_b64 v213, v[178:179], v[182:183] offset0:64 offset1:136
	ds_write2_b64 v214, v[176:177], v[180:181] offset0:80 offset1:152
	ds_write2_b64 v215, v[168:169], v[174:175] offset0:96 offset1:168
	ds_write2_b64 v216, v[166:167], v[170:171] offset0:112 offset1:184
	s_cbranch_vccnz .LBB0_764
	v_mov_b32_e32 v38, v204
	s_waitcnt lgkmcnt(0)
	s_barrier
	s_mov_b32 s84, 0
	v_and_b32_e32 v164, 7, v38
	v_cvt_f32_ubyte0_e32 v162, v164
	v_mul_f32_e32 v163, 0x3c800000, v162
	v_cos_f32_e32 v162, v163
	v_sin_f32_e32 v163, v163
	v_lshlrev_b32_e32 v38, 3, v38
	v_lshl_add_u32 v164, v164, 3, 0
.LBB0_766:
	v_add_u32_e32 v165, s84, v38
	v_and_b32_e32 v165, 0xffffffc0, v165
	v_lshlrev_b32_e32 v166, 3, v165
	v_add3_u32 v165, v164, v165, v166
	ds_read2_b64 v[166:169], v165 offset1:9
	ds_read2_b64 v[170:173], v165 offset0:18 offset1:27
	ds_read2_b64 v[174:177], v165 offset0:36 offset1:45
	ds_read2_b64 v[178:181], v165 offset0:54 offset1:63
	s_addk_i32 s84, 0x1000
	s_cmpk_lg_i32 s84, 0x4000
	s_waitcnt lgkmcnt(1)
	v_pk_add_f32 v[182:183], v[166:167], v[174:175]
	v_pk_add_f32 v[166:167], v[166:167], v[174:175] neg_lo:[0,1] neg_hi:[0,1]
	v_pk_add_f32 v[174:175], v[168:169], v[176:177]
	v_pk_add_f32 v[168:169], v[168:169], v[176:177] neg_lo:[0,1] neg_hi:[0,1]
	v_mov_b64_e32 v[176:177], s[6:7]
	v_pk_mul_f32 v[184:185], v[168:169], v[176:177] op_sel_hi:[1,0]
	v_pk_fma_f32 v[168:169], v[168:169], v[176:177], v[184:185] op_sel:[1,1,0] op_sel_hi:[0,1,1] neg_hi:[1,0,0]
	s_waitcnt lgkmcnt(0)
	v_pk_add_f32 v[176:177], v[170:171], v[178:179]
	v_pk_add_f32 v[170:171], v[170:171], v[178:179] op_sel:[1,1] op_sel_hi:[0,0] neg_lo:[0,1] neg_hi:[1,0]
	v_pk_add_f32 v[178:179], v[172:173], v[180:181]
	v_pk_add_f32 v[172:173], v[172:173], v[180:181] neg_lo:[0,1] neg_hi:[0,1]
	v_mov_b64_e32 v[180:181], s[14:15]
	v_pk_mul_f32 v[184:185], v[172:173], v[180:181] op_sel_hi:[1,0]
	v_pk_fma_f32 v[172:173], v[172:173], v[180:181], v[184:185] op_sel:[1,1,0] op_sel_hi:[0,1,1] neg_hi:[1,0,0]
	v_pk_add_f32 v[180:181], v[182:183], v[176:177]
	v_pk_add_f32 v[176:177], v[182:183], v[176:177] neg_lo:[0,1] neg_hi:[0,1]
	v_pk_add_f32 v[182:183], v[174:175], v[178:179]
	v_pk_add_f32 v[174:175], v[174:175], v[178:179] op_sel:[1,1] op_sel_hi:[0,0] neg_lo:[0,1] neg_hi:[1,0]
	v_pk_add_f32 v[178:179], v[166:167], v[170:171]
	v_pk_add_f32 v[166:167], v[166:167], v[170:171] neg_lo:[0,1] neg_hi:[0,1]
	v_pk_add_f32 v[170:171], v[168:169], v[172:173]
	v_pk_add_f32 v[168:169], v[168:169], v[172:173] op_sel:[1,1] op_sel_hi:[0,0] neg_lo:[0,1] neg_hi:[1,0]
	v_pk_add_f32 v[172:173], v[180:181], v[182:183]
	v_pk_add_f32 v[180:181], v[180:181], v[182:183] neg_lo:[0,1] neg_hi:[0,1]
	v_pk_add_f32 v[182:183], v[176:177], v[174:175]
	v_pk_add_f32 v[174:175], v[176:177], v[174:175] neg_lo:[0,1] neg_hi:[0,1]
	v_pk_add_f32 v[176:177], v[178:179], v[170:171]
	v_pk_add_f32 v[170:171], v[178:179], v[170:171] neg_lo:[0,1] neg_hi:[0,1]
	v_pk_add_f32 v[178:179], v[166:167], v[168:169]
	v_pk_add_f32 v[166:167], v[166:167], v[168:169] neg_lo:[0,1] neg_hi:[0,1]
	v_pk_mul_f32 v[168:169], v[176:177], v[162:163] op_sel_hi:[1,0]
	v_pk_fma_f32 v[168:169], v[176:177], v[162:163], v[168:169] op_sel:[1,1,0] op_sel_hi:[0,1,1] neg_hi:[1,0,0]
	v_pk_mul_f32 v[176:177], v[162:163], v[162:163] op_sel_hi:[1,0]
	v_pk_fma_f32 v[176:177], v[162:163], v[162:163], v[176:177] op_sel:[1,1,0] op_sel_hi:[0,1,1] neg_lo:[1,0,0]
	v_pk_mul_f32 v[184:185], v[182:183], v[176:177] op_sel_hi:[1,0]
	v_pk_fma_f32 v[182:183], v[182:183], v[176:177], v[184:185] op_sel:[1,1,0] op_sel_hi:[0,1,1] neg_hi:[1,0,0]
	v_pk_mul_f32 v[184:185], v[176:177], v[162:163] op_sel_hi:[1,0]
	v_pk_fma_f32 v[176:177], v[176:177], v[162:163], v[184:185] op_sel:[1,1,0] op_sel_hi:[0,1,1] neg_lo:[1,0,0]
	v_pk_mul_f32 v[184:185], v[178:179], v[176:177] op_sel_hi:[1,0]
	v_pk_fma_f32 v[178:179], v[178:179], v[176:177], v[184:185] op_sel:[1,1,0] op_sel_hi:[0,1,1] neg_hi:[1,0,0]
	v_pk_mul_f32 v[184:185], v[176:177], v[162:163] op_sel_hi:[1,0]
	v_pk_fma_f32 v[176:177], v[176:177], v[162:163], v[184:185] op_sel:[1,1,0] op_sel_hi:[0,1,1] neg_lo:[1,0,0]
	v_pk_mul_f32 v[184:185], v[180:181], v[176:177] op_sel_hi:[1,0]
	v_pk_fma_f32 v[180:181], v[180:181], v[176:177], v[184:185] op_sel:[1,1,0] op_sel_hi:[0,1,1] neg_hi:[1,0,0]
	v_pk_mul_f32 v[184:185], v[176:177], v[162:163] op_sel_hi:[1,0]
	v_pk_fma_f32 v[176:177], v[176:177], v[162:163], v[184:185] op_sel:[1,1,0] op_sel_hi:[0,1,1] neg_lo:[1,0,0]
	v_pk_mul_f32 v[184:185], v[170:171], v[176:177] op_sel_hi:[1,0]
	v_pk_fma_f32 v[170:171], v[170:171], v[176:177], v[184:185] op_sel:[1,1,0] op_sel_hi:[0,1,1] neg_hi:[1,0,0]
	v_pk_mul_f32 v[184:185], v[176:177], v[162:163] op_sel_hi:[1,0]
	v_pk_fma_f32 v[176:177], v[176:177], v[162:163], v[184:185] op_sel:[1,1,0] op_sel_hi:[0,1,1] neg_lo:[1,0,0]
	v_pk_mul_f32 v[184:185], v[174:175], v[176:177] op_sel_hi:[1,0]
	v_pk_fma_f32 v[174:175], v[174:175], v[176:177], v[184:185] op_sel:[1,1,0] op_sel_hi:[0,1,1] neg_hi:[1,0,0]
	v_pk_mul_f32 v[184:185], v[176:177], v[162:163] op_sel_hi:[1,0]
	v_pk_fma_f32 v[176:177], v[176:177], v[162:163], v[184:185] op_sel:[1,1,0] op_sel_hi:[0,1,1] neg_lo:[1,0,0]
	v_pk_mul_f32 v[184:185], v[166:167], v[176:177] op_sel_hi:[1,0]
	v_pk_fma_f32 v[166:167], v[166:167], v[176:177], v[184:185] op_sel:[1,1,0] op_sel_hi:[0,1,1] neg_hi:[1,0,0]
	ds_write2_b64 v165, v[172:173], v[168:169] offset1:9
	ds_write2_b64 v165, v[182:183], v[178:179] offset0:18 offset1:27
	ds_write2_b64 v165, v[180:181], v[170:171] offset0:36 offset1:45
	ds_write2_b64 v165, v[174:175], v[166:167] offset0:54 offset1:63
	s_cbranch_scc1 .LBB0_766
	v_mov_b32_e32 v38, v204
	s_waitcnt lgkmcnt(0)
	s_barrier
	s_mov_b32 s84, 0
	v_mul_lo_u32 v38, v38, s33
	v_add_u32_e32 v38, 0, v38
.LBB0_768:
	v_add_u32_e32 v182, s84, v38
	ds_read2_b64 v[162:165], v182 offset1:1
	ds_read2_b64 v[166:169], v182 offset0:2 offset1:3
	ds_read2_b64 v[170:173], v182 offset0:4 offset1:5
	ds_read2_b64 v[174:177], v182 offset0:6 offset1:7
	s_add_i32 s84, s84, 0x9000
	s_cmp_lg_u32 s84, 0x24000
	s_waitcnt lgkmcnt(1)
	v_pk_add_f32 v[178:179], v[162:163], v[170:171]
	v_pk_add_f32 v[162:163], v[162:163], v[170:171] neg_lo:[0,1] neg_hi:[0,1]
	v_pk_add_f32 v[170:171], v[164:165], v[172:173]
	v_pk_add_f32 v[164:165], v[164:165], v[172:173] neg_lo:[0,1] neg_hi:[0,1]
	v_mov_b64_e32 v[172:173], s[6:7]
	v_pk_mul_f32 v[180:181], v[164:165], v[172:173] op_sel_hi:[1,0]
	v_pk_fma_f32 v[164:165], v[164:165], v[172:173], v[180:181] op_sel:[1,1,0] op_sel_hi:[0,1,1] neg_hi:[1,0,0]
	s_waitcnt lgkmcnt(0)
	v_pk_add_f32 v[172:173], v[166:167], v[174:175]
	v_pk_add_f32 v[166:167], v[166:167], v[174:175] op_sel:[1,1] op_sel_hi:[0,0] neg_lo:[0,1] neg_hi:[1,0]
	v_pk_add_f32 v[174:175], v[168:169], v[176:177]
	v_pk_add_f32 v[168:169], v[168:169], v[176:177] neg_lo:[0,1] neg_hi:[0,1]
	v_mov_b64_e32 v[176:177], s[14:15]
	v_pk_mul_f32 v[180:181], v[168:169], v[176:177] op_sel_hi:[1,0]
	v_pk_fma_f32 v[168:169], v[168:169], v[176:177], v[180:181] op_sel:[1,1,0] op_sel_hi:[0,1,1] neg_hi:[1,0,0]
	v_pk_add_f32 v[176:177], v[178:179], v[172:173]
	v_pk_add_f32 v[172:173], v[178:179], v[172:173] neg_lo:[0,1] neg_hi:[0,1]
	v_pk_add_f32 v[178:179], v[170:171], v[174:175]
	v_pk_add_f32 v[170:171], v[170:171], v[174:175] op_sel:[1,1] op_sel_hi:[0,0] neg_lo:[0,1] neg_hi:[1,0]
	v_pk_add_f32 v[174:175], v[162:163], v[166:167]
	v_pk_add_f32 v[162:163], v[162:163], v[166:167] neg_lo:[0,1] neg_hi:[0,1]
	v_pk_add_f32 v[166:167], v[164:165], v[168:169]
	v_pk_add_f32 v[164:165], v[164:165], v[168:169] op_sel:[1,1] op_sel_hi:[0,0] neg_lo:[0,1] neg_hi:[1,0]
	v_pk_add_f32 v[168:169], v[176:177], v[178:179]
	v_pk_add_f32 v[176:177], v[176:177], v[178:179] neg_lo:[0,1] neg_hi:[0,1]
	v_pk_add_f32 v[178:179], v[172:173], v[170:171]
	v_pk_add_f32 v[170:171], v[172:173], v[170:171] neg_lo:[0,1] neg_hi:[0,1]
	v_pk_add_f32 v[172:173], v[174:175], v[166:167]
	v_pk_add_f32 v[166:167], v[174:175], v[166:167] neg_lo:[0,1] neg_hi:[0,1]
	v_pk_add_f32 v[174:175], v[162:163], v[164:165]
	v_pk_add_f32 v[162:163], v[162:163], v[164:165] neg_lo:[0,1] neg_hi:[0,1]
	ds_write2_b64 v182, v[168:169], v[172:173] offset1:1
	ds_write2_b64 v182, v[178:179], v[174:175] offset0:2 offset1:3
	ds_write2_b64 v182, v[176:177], v[166:167] offset0:4 offset1:5
	ds_write2_b64 v182, v[170:171], v[162:163] offset0:6 offset1:7
	s_cbranch_scc1 .LBB0_768
	s_waitcnt lgkmcnt(0)
	s_barrier
	s_nop 0
	v_cvt_f32_i32_e32 v38, v209
	v_lshlrev_b32_e32 v165, 2, v209
	v_lshrrev_b32_e32 v166, 5, v209
	v_ashrrev_i32_e32 v167, 11, v209
	v_mul_f32_e32 v38, 0x38800000, v38
	v_cos_f32_e32 v163, v38
	v_sin_f32_e32 v162, v38
	v_lshlrev_b32_e32 v38, 10, v209
	v_sub_u32_e32 v164, 0, v209
	v_and_b32_e32 v38, 0x3c00, v38
	v_and_b32_e32 v166, 56, v166
	v_and_or_b32 v165, v165, s9, v167
	v_or3_b32 v38, v165, v38, v166
	v_lshlrev_b32_e32 v165, 10, v164
	v_lshlrev_b32_e32 v166, 2, v164
	v_lshrrev_b32_e32 v167, 5, v164
	v_bfe_u32 v164, v164, 11, 3
	v_and_b32_e32 v165, 0x3c00, v165
	v_and_b32_e32 v166, 0x3c0, v166
	v_and_or_b32 v164, v167, 56, v164
	v_mul_i32_i24_e32 v38, 9, v38
	v_or3_b32 v164, v164, v166, v165
	v_and_b32_e32 v38, -8, v38
	v_mul_u32_u24_e32 v164, 9, v164
	v_add_u32_e32 v38, 0, v38
	v_and_b32_e32 v164, 0x3fff8, v164
	v_add_u32_e32 v176, 0, v164
	ds_read_b64 v[164:165], v38
	ds_read_b64 v[166:167], v176
	v_pk_fma_f32 v[168:169], v[162:163], 0, v[162:163] op_sel:[0,0,1] op_sel_hi:[1,0,0] neg_lo:[1,0,0] neg_hi:[1,0,0]
	v_pk_fma_f32 v[170:171], v[162:163], 0, v[162:163] op_sel:[0,0,1] op_sel_hi:[1,0,0]
	s_nop 0
	v_mov_b32_e32 v169, v171
	s_waitcnt lgkmcnt(0)
	v_pk_add_f32 v[170:171], v[164:165], v[166:167] neg_hi:[0,1]
	v_pk_add_f32 v[164:165], v[164:165], v[166:167] op_sel:[1,1] op_sel_hi:[0,0] neg_hi:[1,0]
	v_pk_add_f32 v[166:167], v[158:159], v[160:161] neg_hi:[0,1]
	v_pk_add_f32 v[158:159], v[158:159], v[160:161] op_sel:[1,1] op_sel_hi:[0,0] neg_hi:[1,0]
	v_pk_mul_f32 v[160:161], v[170:171], v[166:167] op_sel_hi:[1,0]
	v_pk_mul_f32 v[172:173], v[164:165], v[158:159] op_sel_hi:[1,0]
	v_pk_fma_f32 v[160:161], v[170:171], v[166:167], v[160:161] op_sel:[1,1,0] op_sel_hi:[0,1,1] neg_lo:[1,0,0]
	v_pk_fma_f32 v[172:173], v[164:165], v[158:159], v[172:173] op_sel:[1,1,0] op_sel_hi:[0,1,1] neg_lo:[1,0,0]
	v_pk_mul_f32 v[174:175], v[172:173], v[168:169] op_sel_hi:[1,0]
	v_pk_fma_f32 v[168:169], v[172:173], v[168:169], v[174:175] op_sel:[1,1,0] op_sel_hi:[0,1,1] neg_hi:[1,0,0]
	v_pk_add_f32 v[160:161], v[160:161], v[168:169]
	v_pk_mul_f32 v[168:169], v[170:171], v[158:159] op_sel_hi:[1,0]
	v_pk_fma_f32 v[158:159], v[170:171], v[158:159], v[168:169] op_sel:[1,1,0] op_sel_hi:[0,1,1] neg_lo:[1,0,0]
	v_pk_mul_f32 v[168:169], v[164:165], v[166:167] op_sel_hi:[1,0]
	v_pk_fma_f32 v[164:165], v[164:165], v[166:167], v[168:169] op_sel:[1,1,0] op_sel_hi:[0,1,1] neg_lo:[1,0,0]
	v_pk_add_f32 v[158:159], v[158:159], v[164:165]
	s_nop 0
	v_pk_add_f32 v[164:165], v[160:161], v[158:159] op_sel:[0,1] op_sel_hi:[1,0] neg_lo:[0,1]
	v_pk_add_f32 v[158:159], v[160:161], v[158:159] op_sel:[0,1] op_sel_hi:[1,0] neg_hi:[1,0]
	ds_write_b64 v38, v[164:165]
	ds_write_b64 v176, v[158:159]
	v_add_u32_e32 v158, 1, v209
	v_lshlrev_b32_e32 v164, 10, v158
	v_lshlrev_b32_e32 v165, 2, v158
	v_lshrrev_b32_e32 v166, 5, v158
	v_ashrrev_i32_e32 v158, 11, v158
	v_and_b32_e32 v164, 0x3c00, v164
	v_and_b32_e32 v166, 56, v166
	v_and_or_b32 v158, v165, s9, v158
	v_or3_b32 v158, v158, v164, v166
	v_mul_i32_i24_e32 v158, 9, v158
	v_not_b32_e32 v159, v209
	v_and_b32_e32 v158, -8, v158
	v_add_u32_e32 v174, 0, v158
	v_lshlrev_b32_e32 v158, 10, v159
	v_lshlrev_b32_e32 v164, 2, v159
	v_lshrrev_b32_e32 v165, 5, v159
	v_bfe_u32 v159, v159, 11, 3
	v_and_b32_e32 v158, 0x3c00, v158
	v_and_b32_e32 v164, 0x3c0, v164
	v_and_or_b32 v159, v165, 56, v159
	v_or3_b32 v158, v159, v164, v158
	v_mul_u32_u24_e32 v158, 9, v158
	v_and_b32_e32 v158, 0x3fff8, v158
	v_add_u32_e32 v159, 0, v158
	ds_read_b64 v[164:165], v159
	ds_read_b64 v[166:167], v174
	v_pk_mul_f32 v[160:161], v[162:163], s[20:21] op_sel_hi:[0,1]
	v_mov_b32_e32 v38, v163
	v_mov_b32_e32 v158, v163
	v_pk_fma_f32 v[168:169], v[38:39], s[22:23], v[160:161] neg_lo:[0,0,1] neg_hi:[0,0,1]
	v_pk_fma_f32 v[160:161], v[158:159], s[22:23], v[160:161] op_sel_hi:[0,1,1]
	v_mov_b32_e32 v169, v161
	s_waitcnt lgkmcnt(0)
	v_pk_add_f32 v[160:161], v[166:167], v[164:165] neg_hi:[0,1]
	v_pk_add_f32 v[164:165], v[166:167], v[164:165] op_sel:[1,1] op_sel_hi:[0,0] neg_hi:[1,0]
	v_pk_add_f32 v[166:167], v[154:155], v[156:157] neg_hi:[0,1]
	v_pk_add_f32 v[154:155], v[154:155], v[156:157] op_sel:[1,1] op_sel_hi:[0,0] neg_hi:[1,0]
	v_pk_mul_f32 v[156:157], v[160:161], v[166:167] op_sel_hi:[1,0]
	v_pk_mul_f32 v[170:171], v[164:165], v[154:155] op_sel_hi:[1,0]
	v_pk_fma_f32 v[156:157], v[160:161], v[166:167], v[156:157] op_sel:[1,1,0] op_sel_hi:[0,1,1] neg_lo:[1,0,0]
	v_pk_fma_f32 v[170:171], v[164:165], v[154:155], v[170:171] op_sel:[1,1,0] op_sel_hi:[0,1,1] neg_lo:[1,0,0]
	v_pk_mul_f32 v[172:173], v[170:171], v[168:169] op_sel_hi:[1,0]
	v_pk_fma_f32 v[168:169], v[170:171], v[168:169], v[172:173] op_sel:[1,1,0] op_sel_hi:[0,1,1] neg_hi:[1,0,0]
	v_pk_add_f32 v[156:157], v[156:157], v[168:169]
	v_pk_mul_f32 v[168:169], v[160:161], v[154:155] op_sel_hi:[1,0]
	v_pk_fma_f32 v[154:155], v[160:161], v[154:155], v[168:169] op_sel:[1,1,0] op_sel_hi:[0,1,1] neg_lo:[1,0,0]
	v_pk_mul_f32 v[160:161], v[164:165], v[166:167] op_sel_hi:[1,0]
	v_pk_fma_f32 v[160:161], v[164:165], v[166:167], v[160:161] op_sel:[1,1,0] op_sel_hi:[0,1,1] neg_lo:[1,0,0]
	v_pk_add_f32 v[154:155], v[154:155], v[160:161]
	s_nop 0
	v_pk_add_f32 v[160:161], v[156:157], v[154:155] op_sel:[0,1] op_sel_hi:[1,0] neg_lo:[0,1]
	v_pk_add_f32 v[154:155], v[156:157], v[154:155] op_sel:[0,1] op_sel_hi:[1,0] neg_hi:[1,0]
	ds_write_b64 v174, v[160:161]
	ds_write_b64 v159, v[154:155]
	v_add_u32_e32 v154, 2, v209
	v_lshlrev_b32_e32 v156, 10, v154
	v_lshlrev_b32_e32 v157, 2, v154
	v_lshrrev_b32_e32 v159, 5, v154
	v_ashrrev_i32_e32 v154, 11, v154
	v_and_b32_e32 v156, 0x3c00, v156
	v_and_b32_e32 v159, 56, v159
	v_and_or_b32 v154, v157, s9, v154
	v_or3_b32 v154, v154, v156, v159
	v_mul_i32_i24_e32 v154, 9, v154
	v_sub_u32_e32 v155, -2, v209
	v_and_b32_e32 v154, -8, v154
	v_add_u32_e32 v159, 0, v154
	v_lshlrev_b32_e32 v154, 10, v155
	v_lshlrev_b32_e32 v156, 2, v155
	v_lshrrev_b32_e32 v157, 5, v155
	v_bfe_u32 v155, v155, 11, 3
	v_and_b32_e32 v154, 0x3c00, v154
	v_and_b32_e32 v156, 0x3c0, v156
	v_and_or_b32 v155, v157, 56, v155
	v_or3_b32 v154, v155, v156, v154
	v_mul_u32_u24_e32 v154, 9, v154
	v_and_b32_e32 v154, 0x3fff8, v154
	v_add_u32_e32 v163, 0, v154
	ds_read_b64 v[154:155], v159
	ds_read_b64 v[156:157], v163
	v_pk_mul_f32 v[160:161], v[162:163], s[24:25] op_sel_hi:[0,1]
	v_pk_fma_f32 v[164:165], v[38:39], s[26:27], v[160:161] neg_lo:[0,0,1] neg_hi:[0,0,1]
	v_pk_fma_f32 v[160:161], v[158:159], s[26:27], v[160:161] op_sel_hi:[0,1,1]
	v_mov_b32_e32 v165, v161
	s_waitcnt lgkmcnt(0)
	v_pk_add_f32 v[160:161], v[154:155], v[156:157] neg_hi:[0,1]
	v_pk_add_f32 v[154:155], v[154:155], v[156:157] op_sel:[1,1] op_sel_hi:[0,0] neg_hi:[1,0]
	v_pk_add_f32 v[156:157], v[150:151], v[152:153] neg_hi:[0,1]
	v_pk_add_f32 v[150:151], v[150:151], v[152:153] op_sel:[1,1] op_sel_hi:[0,0] neg_hi:[1,0]
	v_pk_mul_f32 v[152:153], v[160:161], v[156:157] op_sel_hi:[1,0]
	v_pk_mul_f32 v[166:167], v[154:155], v[150:151] op_sel_hi:[1,0]
	v_pk_fma_f32 v[152:153], v[160:161], v[156:157], v[152:153] op_sel:[1,1,0] op_sel_hi:[0,1,1] neg_lo:[1,0,0]
	v_pk_fma_f32 v[166:167], v[154:155], v[150:151], v[166:167] op_sel:[1,1,0] op_sel_hi:[0,1,1] neg_lo:[1,0,0]
	v_pk_mul_f32 v[168:169], v[166:167], v[164:165] op_sel_hi:[1,0]
	v_pk_fma_f32 v[164:165], v[166:167], v[164:165], v[168:169] op_sel:[1,1,0] op_sel_hi:[0,1,1] neg_hi:[1,0,0]
	v_pk_add_f32 v[152:153], v[152:153], v[164:165]
	v_pk_mul_f32 v[164:165], v[160:161], v[150:151] op_sel_hi:[1,0]
	v_pk_fma_f32 v[150:151], v[160:161], v[150:151], v[164:165] op_sel:[1,1,0] op_sel_hi:[0,1,1] neg_lo:[1,0,0]
	v_pk_mul_f32 v[160:161], v[154:155], v[156:157] op_sel_hi:[1,0]
	v_pk_fma_f32 v[154:155], v[154:155], v[156:157], v[160:161] op_sel:[1,1,0] op_sel_hi:[0,1,1] neg_lo:[1,0,0]
	v_pk_add_f32 v[150:151], v[150:151], v[154:155]
	s_nop 0
	v_pk_add_f32 v[154:155], v[152:153], v[150:151] op_sel:[0,1] op_sel_hi:[1,0] neg_lo:[0,1]
	v_pk_add_f32 v[150:151], v[152:153], v[150:151] op_sel:[0,1] op_sel_hi:[1,0] neg_hi:[1,0]
	ds_write_b64 v159, v[154:155]
	ds_write_b64 v163, v[150:151]
	v_add_u32_e32 v150, 3, v209
	v_lshlrev_b32_e32 v152, 10, v150
	v_lshlrev_b32_e32 v153, 2, v150
	v_lshrrev_b32_e32 v154, 5, v150
	v_ashrrev_i32_e32 v150, 11, v150
	v_and_b32_e32 v152, 0x3c00, v152
	v_and_b32_e32 v154, 56, v154
	v_and_or_b32 v150, v153, s9, v150
	v_or3_b32 v150, v150, v152, v154
	v_mul_i32_i24_e32 v150, 9, v150
	v_sub_u32_e32 v151, -3, v209
	v_and_b32_e32 v150, -8, v150
	v_add_u32_e32 v159, 0, v150
	v_lshlrev_b32_e32 v150, 10, v151
	v_lshlrev_b32_e32 v152, 2, v151
	v_lshrrev_b32_e32 v153, 5, v151
	v_bfe_u32 v151, v151, 11, 3
	v_and_b32_e32 v150, 0x3c00, v150
	v_and_b32_e32 v152, 0x3c0, v152
	v_and_or_b32 v151, v153, 56, v151
	v_or3_b32 v150, v151, v152, v150
	v_mul_u32_u24_e32 v150, 9, v150
	v_and_b32_e32 v150, 0x3fff8, v150
	v_add_u32_e32 v163, 0, v150
	ds_read_b64 v[150:151], v159
	ds_read_b64 v[152:153], v163
	v_pk_mul_f32 v[154:155], v[162:163], s[28:29] op_sel_hi:[0,1]
	v_pk_fma_f32 v[156:157], v[38:39], s[30:31], v[154:155] neg_lo:[0,0,1] neg_hi:[0,0,1]
	v_pk_fma_f32 v[154:155], v[158:159], s[30:31], v[154:155] op_sel_hi:[0,1,1]
	v_mov_b32_e32 v157, v155
	s_waitcnt lgkmcnt(0)
	v_pk_add_f32 v[154:155], v[150:151], v[152:153] neg_hi:[0,1]
	v_pk_add_f32 v[150:151], v[150:151], v[152:153] op_sel:[1,1] op_sel_hi:[0,0] neg_hi:[1,0]
	v_pk_add_f32 v[152:153], v[146:147], v[148:149] neg_hi:[0,1]
	v_pk_add_f32 v[146:147], v[146:147], v[148:149] op_sel:[1,1] op_sel_hi:[0,0] neg_hi:[1,0]
	v_pk_mul_f32 v[148:149], v[154:155], v[152:153] op_sel_hi:[1,0]
	v_pk_mul_f32 v[160:161], v[150:151], v[146:147] op_sel_hi:[1,0]
	v_pk_fma_f32 v[148:149], v[154:155], v[152:153], v[148:149] op_sel:[1,1,0] op_sel_hi:[0,1,1] neg_lo:[1,0,0]
	v_pk_fma_f32 v[160:161], v[150:151], v[146:147], v[160:161] op_sel:[1,1,0] op_sel_hi:[0,1,1] neg_lo:[1,0,0]
	v_pk_mul_f32 v[164:165], v[160:161], v[156:157] op_sel_hi:[1,0]
	v_pk_fma_f32 v[156:157], v[160:161], v[156:157], v[164:165] op_sel:[1,1,0] op_sel_hi:[0,1,1] neg_hi:[1,0,0]
	v_pk_add_f32 v[148:149], v[148:149], v[156:157]
	v_pk_mul_f32 v[156:157], v[154:155], v[146:147] op_sel_hi:[1,0]
	v_pk_fma_f32 v[146:147], v[154:155], v[146:147], v[156:157] op_sel:[1,1,0] op_sel_hi:[0,1,1] neg_lo:[1,0,0]
	v_pk_mul_f32 v[154:155], v[150:151], v[152:153] op_sel_hi:[1,0]
	v_pk_fma_f32 v[150:151], v[150:151], v[152:153], v[154:155] op_sel:[1,1,0] op_sel_hi:[0,1,1] neg_lo:[1,0,0]
	v_pk_add_f32 v[146:147], v[146:147], v[150:151]
	s_nop 0
	v_pk_add_f32 v[150:151], v[148:149], v[146:147] op_sel:[0,1] op_sel_hi:[1,0] neg_lo:[0,1]
	v_pk_add_f32 v[146:147], v[148:149], v[146:147] op_sel:[0,1] op_sel_hi:[1,0] neg_hi:[1,0]
	ds_write_b64 v159, v[150:151]
	ds_write_b64 v163, v[146:147]
	v_add_u32_e32 v146, 4, v209
	v_lshlrev_b32_e32 v148, 10, v146
	v_lshlrev_b32_e32 v149, 2, v146
	v_lshrrev_b32_e32 v150, 5, v146
	v_ashrrev_i32_e32 v146, 11, v146
	v_and_b32_e32 v148, 0x3c00, v148
	v_and_b32_e32 v150, 56, v150
	v_and_or_b32 v146, v149, s9, v146
	v_or3_b32 v146, v146, v148, v150
	v_mul_i32_i24_e32 v146, 9, v146
	v_sub_u32_e32 v147, -4, v209
	v_and_b32_e32 v146, -8, v146
	v_add_u32_e32 v159, 0, v146
	v_lshlrev_b32_e32 v146, 10, v147
	v_lshlrev_b32_e32 v148, 2, v147
	v_lshrrev_b32_e32 v149, 5, v147
	v_bfe_u32 v147, v147, 11, 3
	v_and_b32_e32 v146, 0x3c00, v146
	v_and_b32_e32 v148, 0x3c0, v148
	v_and_or_b32 v147, v149, 56, v147
	v_or3_b32 v146, v147, v148, v146
	v_mul_u32_u24_e32 v146, 9, v146
	v_and_b32_e32 v146, 0x3fff8, v146
	v_add_u32_e32 v160, 0, v146
	ds_read_b64 v[146:147], v159
	ds_read_b64 v[148:149], v160
	v_pk_mul_f32 v[150:151], v[162:163], s[34:35] op_sel_hi:[0,1]
	v_pk_fma_f32 v[152:153], v[38:39], s[36:37], v[150:151] neg_lo:[0,0,1] neg_hi:[0,0,1]
	v_pk_fma_f32 v[150:151], v[158:159], s[36:37], v[150:151] op_sel_hi:[0,1,1]
	v_mov_b32_e32 v153, v151
	s_waitcnt lgkmcnt(0)
	v_pk_add_f32 v[150:151], v[146:147], v[148:149] neg_hi:[0,1]
	v_pk_add_f32 v[146:147], v[146:147], v[148:149] op_sel:[1,1] op_sel_hi:[0,0] neg_hi:[1,0]
	v_pk_add_f32 v[148:149], v[142:143], v[144:145] neg_hi:[0,1]
	v_pk_add_f32 v[142:143], v[142:143], v[144:145] op_sel:[1,1] op_sel_hi:[0,0] neg_hi:[1,0]
	v_pk_mul_f32 v[144:145], v[150:151], v[148:149] op_sel_hi:[1,0]
	v_pk_mul_f32 v[154:155], v[146:147], v[142:143] op_sel_hi:[1,0]
	v_pk_fma_f32 v[144:145], v[150:151], v[148:149], v[144:145] op_sel:[1,1,0] op_sel_hi:[0,1,1] neg_lo:[1,0,0]
	v_pk_fma_f32 v[154:155], v[146:147], v[142:143], v[154:155] op_sel:[1,1,0] op_sel_hi:[0,1,1] neg_lo:[1,0,0]
	v_pk_mul_f32 v[156:157], v[154:155], v[152:153] op_sel_hi:[1,0]
	v_pk_fma_f32 v[152:153], v[154:155], v[152:153], v[156:157] op_sel:[1,1,0] op_sel_hi:[0,1,1] neg_hi:[1,0,0]
	v_pk_add_f32 v[144:145], v[144:145], v[152:153]
	v_pk_mul_f32 v[152:153], v[150:151], v[142:143] op_sel_hi:[1,0]
	v_pk_fma_f32 v[142:143], v[150:151], v[142:143], v[152:153] op_sel:[1,1,0] op_sel_hi:[0,1,1] neg_lo:[1,0,0]
	v_pk_mul_f32 v[150:151], v[146:147], v[148:149] op_sel_hi:[1,0]
	v_pk_fma_f32 v[146:147], v[146:147], v[148:149], v[150:151] op_sel:[1,1,0] op_sel_hi:[0,1,1] neg_lo:[1,0,0]
	v_pk_add_f32 v[142:143], v[142:143], v[146:147]
	s_nop 0
	v_pk_add_f32 v[146:147], v[144:145], v[142:143] op_sel:[0,1] op_sel_hi:[1,0] neg_lo:[0,1]
	v_pk_add_f32 v[142:143], v[144:145], v[142:143] op_sel:[0,1] op_sel_hi:[1,0] neg_hi:[1,0]
	ds_write_b64 v159, v[146:147]
	ds_write_b64 v160, v[142:143]
	v_add_u32_e32 v142, 5, v209
	v_lshlrev_b32_e32 v144, 10, v142
	v_lshlrev_b32_e32 v145, 2, v142
	v_lshrrev_b32_e32 v146, 5, v142
	v_ashrrev_i32_e32 v142, 11, v142
	v_and_b32_e32 v144, 0x3c00, v144
	v_and_b32_e32 v146, 56, v146
	v_and_or_b32 v142, v145, s9, v142
	v_or3_b32 v142, v142, v144, v146
	v_mul_i32_i24_e32 v142, 9, v142
	v_sub_u32_e32 v143, -5, v209
	v_and_b32_e32 v142, -8, v142
	v_add_u32_e32 v154, 0, v142
	v_lshlrev_b32_e32 v142, 10, v143
	v_lshlrev_b32_e32 v144, 2, v143
	v_lshrrev_b32_e32 v145, 5, v143
	v_bfe_u32 v143, v143, 11, 3
	v_and_b32_e32 v142, 0x3c00, v142
	v_and_b32_e32 v144, 0x3c0, v144
	v_and_or_b32 v143, v145, 56, v143
	v_or3_b32 v142, v143, v144, v142
	v_mul_u32_u24_e32 v142, 9, v142
	v_and_b32_e32 v142, 0x3fff8, v142
	v_add_u32_e32 v155, 0, v142
	ds_read_b64 v[142:143], v154
	ds_read_b64 v[144:145], v155
	v_pk_mul_f32 v[146:147], v[162:163], s[38:39] op_sel_hi:[0,1]
	v_pk_fma_f32 v[148:149], v[38:39], s[40:41], v[146:147] neg_lo:[0,0,1] neg_hi:[0,0,1]
	v_pk_fma_f32 v[146:147], v[158:159], s[40:41], v[146:147] op_sel_hi:[0,1,1]
	v_mov_b32_e32 v149, v147
	s_waitcnt lgkmcnt(0)
	v_pk_add_f32 v[146:147], v[142:143], v[144:145] neg_hi:[0,1]
	v_pk_add_f32 v[142:143], v[142:143], v[144:145] op_sel:[1,1] op_sel_hi:[0,0] neg_hi:[1,0]
	v_pk_add_f32 v[144:145], v[138:139], v[140:141] neg_hi:[0,1]
	v_pk_add_f32 v[138:139], v[138:139], v[140:141] op_sel:[1,1] op_sel_hi:[0,0] neg_hi:[1,0]
	v_pk_mul_f32 v[140:141], v[146:147], v[144:145] op_sel_hi:[1,0]
	v_pk_mul_f32 v[150:151], v[142:143], v[138:139] op_sel_hi:[1,0]
	v_pk_fma_f32 v[140:141], v[146:147], v[144:145], v[140:141] op_sel:[1,1,0] op_sel_hi:[0,1,1] neg_lo:[1,0,0]
	v_pk_fma_f32 v[150:151], v[142:143], v[138:139], v[150:151] op_sel:[1,1,0] op_sel_hi:[0,1,1] neg_lo:[1,0,0]
	v_pk_mul_f32 v[152:153], v[150:151], v[148:149] op_sel_hi:[1,0]
	v_pk_fma_f32 v[148:149], v[150:151], v[148:149], v[152:153] op_sel:[1,1,0] op_sel_hi:[0,1,1] neg_hi:[1,0,0]
	v_pk_add_f32 v[140:141], v[140:141], v[148:149]
	v_pk_mul_f32 v[148:149], v[146:147], v[138:139] op_sel_hi:[1,0]
	v_pk_fma_f32 v[138:139], v[146:147], v[138:139], v[148:149] op_sel:[1,1,0] op_sel_hi:[0,1,1] neg_lo:[1,0,0]
	v_pk_mul_f32 v[146:147], v[142:143], v[144:145] op_sel_hi:[1,0]
	v_pk_fma_f32 v[142:143], v[142:143], v[144:145], v[146:147] op_sel:[1,1,0] op_sel_hi:[0,1,1] neg_lo:[1,0,0]
	v_pk_add_f32 v[138:139], v[138:139], v[142:143]
	s_nop 0
	v_pk_add_f32 v[142:143], v[140:141], v[138:139] op_sel:[0,1] op_sel_hi:[1,0] neg_lo:[0,1]
	v_pk_add_f32 v[138:139], v[140:141], v[138:139] op_sel:[0,1] op_sel_hi:[1,0] neg_hi:[1,0]
	ds_write_b64 v154, v[142:143]
	ds_write_b64 v155, v[138:139]
	v_add_u32_e32 v138, 6, v209
	v_lshlrev_b32_e32 v140, 10, v138
	v_lshlrev_b32_e32 v141, 2, v138
	v_lshrrev_b32_e32 v142, 5, v138
	v_ashrrev_i32_e32 v138, 11, v138
	v_and_b32_e32 v140, 0x3c00, v140
	v_and_b32_e32 v142, 56, v142
	v_and_or_b32 v138, v141, s9, v138
	v_or3_b32 v138, v138, v140, v142
	v_mul_i32_i24_e32 v138, 9, v138
	v_sub_u32_e32 v139, -6, v209
	v_and_b32_e32 v138, -8, v138
	v_add_u32_e32 v150, 0, v138
	v_lshlrev_b32_e32 v138, 10, v139
	v_lshlrev_b32_e32 v140, 2, v139
	v_lshrrev_b32_e32 v141, 5, v139
	v_bfe_u32 v139, v139, 11, 3
	v_and_b32_e32 v138, 0x3c00, v138
	v_and_b32_e32 v140, 0x3c0, v140
	v_and_or_b32 v139, v141, 56, v139
	v_or3_b32 v138, v139, v140, v138
	v_mul_u32_u24_e32 v138, 9, v138
	v_and_b32_e32 v138, 0x3fff8, v138
	v_add_u32_e32 v151, 0, v138
	ds_read_b64 v[138:139], v150
	ds_read_b64 v[140:141], v151
	v_pk_mul_f32 v[142:143], v[162:163], s[42:43] op_sel_hi:[0,1]
	v_pk_fma_f32 v[144:145], v[38:39], s[44:45], v[142:143] neg_lo:[0,0,1] neg_hi:[0,0,1]
	v_pk_fma_f32 v[142:143], v[158:159], s[44:45], v[142:143] op_sel_hi:[0,1,1]
	v_mov_b32_e32 v145, v143
	s_waitcnt lgkmcnt(0)
	v_pk_add_f32 v[142:143], v[138:139], v[140:141] neg_hi:[0,1]
	v_pk_add_f32 v[138:139], v[138:139], v[140:141] op_sel:[1,1] op_sel_hi:[0,0] neg_hi:[1,0]
	v_pk_add_f32 v[140:141], v[134:135], v[136:137] neg_hi:[0,1]
	v_pk_add_f32 v[134:135], v[134:135], v[136:137] op_sel:[1,1] op_sel_hi:[0,0] neg_hi:[1,0]
	v_pk_mul_f32 v[136:137], v[142:143], v[140:141] op_sel_hi:[1,0]
	v_pk_mul_f32 v[146:147], v[138:139], v[134:135] op_sel_hi:[1,0]
	v_pk_fma_f32 v[136:137], v[142:143], v[140:141], v[136:137] op_sel:[1,1,0] op_sel_hi:[0,1,1] neg_lo:[1,0,0]
	v_pk_fma_f32 v[146:147], v[138:139], v[134:135], v[146:147] op_sel:[1,1,0] op_sel_hi:[0,1,1] neg_lo:[1,0,0]
	v_pk_mul_f32 v[148:149], v[146:147], v[144:145] op_sel_hi:[1,0]
	v_pk_fma_f32 v[144:145], v[146:147], v[144:145], v[148:149] op_sel:[1,1,0] op_sel_hi:[0,1,1] neg_hi:[1,0,0]
	v_pk_add_f32 v[136:137], v[136:137], v[144:145]
	v_pk_mul_f32 v[144:145], v[142:143], v[134:135] op_sel_hi:[1,0]
	v_pk_fma_f32 v[134:135], v[142:143], v[134:135], v[144:145] op_sel:[1,1,0] op_sel_hi:[0,1,1] neg_lo:[1,0,0]
	v_pk_mul_f32 v[142:143], v[138:139], v[140:141] op_sel_hi:[1,0]
	v_pk_fma_f32 v[138:139], v[138:139], v[140:141], v[142:143] op_sel:[1,1,0] op_sel_hi:[0,1,1] neg_lo:[1,0,0]
	v_pk_add_f32 v[134:135], v[134:135], v[138:139]
	s_nop 0
	v_pk_add_f32 v[138:139], v[136:137], v[134:135] op_sel:[0,1] op_sel_hi:[1,0] neg_lo:[0,1]
	v_pk_add_f32 v[134:135], v[136:137], v[134:135] op_sel:[0,1] op_sel_hi:[1,0] neg_hi:[1,0]
	ds_write_b64 v150, v[138:139]
	ds_write_b64 v151, v[134:135]
	v_add_u32_e32 v134, 7, v209
	v_lshlrev_b32_e32 v136, 10, v134
	v_lshlrev_b32_e32 v137, 2, v134
	v_lshrrev_b32_e32 v138, 5, v134
	v_ashrrev_i32_e32 v134, 11, v134
	v_and_b32_e32 v136, 0x3c00, v136
	v_and_b32_e32 v138, 56, v138
	v_and_or_b32 v134, v137, s9, v134
	v_or3_b32 v134, v134, v136, v138
	v_mul_i32_i24_e32 v134, 9, v134
	v_sub_u32_e32 v135, -7, v209
	v_and_b32_e32 v134, -8, v134
	v_add_u32_e32 v146, 0, v134
	v_lshlrev_b32_e32 v134, 10, v135
	v_lshlrev_b32_e32 v136, 2, v135
	v_lshrrev_b32_e32 v137, 5, v135
	v_bfe_u32 v135, v135, 11, 3
	v_and_b32_e32 v134, 0x3c00, v134
	v_and_b32_e32 v136, 0x3c0, v136
	v_and_or_b32 v135, v137, 56, v135
	v_or3_b32 v134, v135, v136, v134
	v_mul_u32_u24_e32 v134, 9, v134
	v_and_b32_e32 v134, 0x3fff8, v134
	v_add_u32_e32 v147, 0, v134
	ds_read_b64 v[134:135], v146
	ds_read_b64 v[136:137], v147
	v_pk_mul_f32 v[138:139], v[162:163], s[46:47] op_sel_hi:[0,1]
	v_pk_fma_f32 v[140:141], v[38:39], s[48:49], v[138:139] neg_lo:[0,0,1] neg_hi:[0,0,1]
	v_pk_fma_f32 v[138:139], v[158:159], s[48:49], v[138:139] op_sel_hi:[0,1,1]
	v_mov_b32_e32 v141, v139
	s_waitcnt lgkmcnt(0)
	v_pk_add_f32 v[138:139], v[134:135], v[136:137] neg_hi:[0,1]
	v_pk_add_f32 v[134:135], v[134:135], v[136:137] op_sel:[1,1] op_sel_hi:[0,0] neg_hi:[1,0]
	v_pk_add_f32 v[136:137], v[130:131], v[132:133] neg_hi:[0,1]
	v_pk_add_f32 v[130:131], v[130:131], v[132:133] op_sel:[1,1] op_sel_hi:[0,0] neg_hi:[1,0]
	v_pk_mul_f32 v[132:133], v[138:139], v[136:137] op_sel_hi:[1,0]
	v_pk_mul_f32 v[142:143], v[134:135], v[130:131] op_sel_hi:[1,0]
	v_pk_fma_f32 v[132:133], v[138:139], v[136:137], v[132:133] op_sel:[1,1,0] op_sel_hi:[0,1,1] neg_lo:[1,0,0]
	v_pk_fma_f32 v[142:143], v[134:135], v[130:131], v[142:143] op_sel:[1,1,0] op_sel_hi:[0,1,1] neg_lo:[1,0,0]
	v_pk_mul_f32 v[144:145], v[142:143], v[140:141] op_sel_hi:[1,0]
	v_pk_fma_f32 v[140:141], v[142:143], v[140:141], v[144:145] op_sel:[1,1,0] op_sel_hi:[0,1,1] neg_hi:[1,0,0]
	v_pk_add_f32 v[132:133], v[132:133], v[140:141]
	v_pk_mul_f32 v[140:141], v[138:139], v[130:131] op_sel_hi:[1,0]
	v_pk_fma_f32 v[130:131], v[138:139], v[130:131], v[140:141] op_sel:[1,1,0] op_sel_hi:[0,1,1] neg_lo:[1,0,0]
	v_pk_mul_f32 v[138:139], v[134:135], v[136:137] op_sel_hi:[1,0]
	v_pk_fma_f32 v[134:135], v[134:135], v[136:137], v[138:139] op_sel:[1,1,0] op_sel_hi:[0,1,1] neg_lo:[1,0,0]
	v_pk_add_f32 v[130:131], v[130:131], v[134:135]
	s_nop 0
	v_pk_add_f32 v[134:135], v[132:133], v[130:131] op_sel:[0,1] op_sel_hi:[1,0] neg_lo:[0,1]
	v_pk_add_f32 v[130:131], v[132:133], v[130:131] op_sel:[0,1] op_sel_hi:[1,0] neg_hi:[1,0]
	ds_write_b64 v146, v[134:135]
	ds_write_b64 v147, v[130:131]
	v_add_u32_e32 v130, 8, v209
	v_lshlrev_b32_e32 v132, 10, v130
	v_lshlrev_b32_e32 v133, 2, v130
	v_lshrrev_b32_e32 v134, 5, v130
	v_ashrrev_i32_e32 v130, 11, v130
	v_and_b32_e32 v132, 0x3c00, v132
	v_and_b32_e32 v134, 56, v134
	v_and_or_b32 v130, v133, s9, v130
	v_or3_b32 v130, v130, v132, v134
	v_mul_i32_i24_e32 v130, 9, v130
	v_sub_u32_e32 v131, -8, v209
	v_and_b32_e32 v130, -8, v130
	v_add_u32_e32 v142, 0, v130
	v_lshlrev_b32_e32 v130, 10, v131
	v_lshlrev_b32_e32 v132, 2, v131
	v_lshrrev_b32_e32 v133, 5, v131
	v_bfe_u32 v131, v131, 11, 3
	v_and_b32_e32 v130, 0x3c00, v130
	v_and_b32_e32 v132, 0x3c0, v132
	v_and_or_b32 v131, v133, 56, v131
	v_or3_b32 v130, v131, v132, v130
	v_mul_u32_u24_e32 v130, 9, v130
	v_and_b32_e32 v130, 0x3fff8, v130
	v_add_u32_e32 v143, 0, v130
	ds_read_b64 v[130:131], v142
	ds_read_b64 v[132:133], v143
	v_pk_mul_f32 v[134:135], v[162:163], s[50:51] op_sel_hi:[0,1]
	v_pk_fma_f32 v[136:137], v[38:39], s[52:53], v[134:135] neg_lo:[0,0,1] neg_hi:[0,0,1]
	v_pk_fma_f32 v[134:135], v[158:159], s[52:53], v[134:135] op_sel_hi:[0,1,1]
	v_mov_b32_e32 v137, v135
	s_waitcnt lgkmcnt(0)
	v_pk_add_f32 v[134:135], v[130:131], v[132:133] neg_hi:[0,1]
	v_pk_add_f32 v[130:131], v[130:131], v[132:133] op_sel:[1,1] op_sel_hi:[0,0] neg_hi:[1,0]
	v_pk_add_f32 v[132:133], v[126:127], v[128:129] neg_hi:[0,1]
	v_pk_add_f32 v[126:127], v[126:127], v[128:129] op_sel:[1,1] op_sel_hi:[0,0] neg_hi:[1,0]
	v_pk_mul_f32 v[128:129], v[134:135], v[132:133] op_sel_hi:[1,0]
	v_pk_mul_f32 v[138:139], v[130:131], v[126:127] op_sel_hi:[1,0]
	v_pk_fma_f32 v[128:129], v[134:135], v[132:133], v[128:129] op_sel:[1,1,0] op_sel_hi:[0,1,1] neg_lo:[1,0,0]
	v_pk_fma_f32 v[138:139], v[130:131], v[126:127], v[138:139] op_sel:[1,1,0] op_sel_hi:[0,1,1] neg_lo:[1,0,0]
	v_pk_mul_f32 v[140:141], v[138:139], v[136:137] op_sel_hi:[1,0]
	v_pk_fma_f32 v[136:137], v[138:139], v[136:137], v[140:141] op_sel:[1,1,0] op_sel_hi:[0,1,1] neg_hi:[1,0,0]
	v_pk_add_f32 v[128:129], v[128:129], v[136:137]
	v_pk_mul_f32 v[136:137], v[134:135], v[126:127] op_sel_hi:[1,0]
	v_pk_fma_f32 v[126:127], v[134:135], v[126:127], v[136:137] op_sel:[1,1,0] op_sel_hi:[0,1,1] neg_lo:[1,0,0]
	v_pk_mul_f32 v[134:135], v[130:131], v[132:133] op_sel_hi:[1,0]
	v_pk_fma_f32 v[130:131], v[130:131], v[132:133], v[134:135] op_sel:[1,1,0] op_sel_hi:[0,1,1] neg_lo:[1,0,0]
	v_pk_add_f32 v[126:127], v[126:127], v[130:131]
	s_nop 0
	v_pk_add_f32 v[130:131], v[128:129], v[126:127] op_sel:[0,1] op_sel_hi:[1,0] neg_lo:[0,1]
	v_pk_add_f32 v[126:127], v[128:129], v[126:127] op_sel:[0,1] op_sel_hi:[1,0] neg_hi:[1,0]
	ds_write_b64 v142, v[130:131]
	ds_write_b64 v143, v[126:127]
	v_add_u32_e32 v126, 9, v209
	v_lshlrev_b32_e32 v128, 10, v126
	v_lshlrev_b32_e32 v129, 2, v126
	v_lshrrev_b32_e32 v130, 5, v126
	v_ashrrev_i32_e32 v126, 11, v126
	v_and_b32_e32 v128, 0x3c00, v128
	v_and_b32_e32 v130, 56, v130
	v_and_or_b32 v126, v129, s9, v126
	v_or3_b32 v126, v126, v128, v130
	v_mul_i32_i24_e32 v126, 9, v126
	v_sub_u32_e32 v127, -9, v209
	v_and_b32_e32 v126, -8, v126
	v_add_u32_e32 v138, 0, v126
	v_lshlrev_b32_e32 v126, 10, v127
	v_lshlrev_b32_e32 v128, 2, v127
	v_lshrrev_b32_e32 v129, 5, v127
	v_bfe_u32 v127, v127, 11, 3
	v_and_b32_e32 v126, 0x3c00, v126
	v_and_b32_e32 v128, 0x3c0, v128
	v_and_or_b32 v127, v129, 56, v127
	v_or3_b32 v126, v127, v128, v126
	v_mul_u32_u24_e32 v126, 9, v126
	v_and_b32_e32 v126, 0x3fff8, v126
	v_add_u32_e32 v139, 0, v126
	ds_read_b64 v[126:127], v138
	ds_read_b64 v[128:129], v139
	v_pk_mul_f32 v[130:131], v[162:163], s[54:55] op_sel_hi:[0,1]
	v_pk_fma_f32 v[132:133], v[38:39], s[56:57], v[130:131] neg_lo:[0,0,1] neg_hi:[0,0,1]
	v_pk_fma_f32 v[130:131], v[158:159], s[56:57], v[130:131] op_sel_hi:[0,1,1]
	v_mov_b32_e32 v133, v131
	s_waitcnt lgkmcnt(0)
	v_pk_add_f32 v[130:131], v[126:127], v[128:129] neg_hi:[0,1]
	v_pk_add_f32 v[126:127], v[126:127], v[128:129] op_sel:[1,1] op_sel_hi:[0,0] neg_hi:[1,0]
	v_pk_add_f32 v[128:129], v[122:123], v[124:125] neg_hi:[0,1]
	v_pk_add_f32 v[122:123], v[122:123], v[124:125] op_sel:[1,1] op_sel_hi:[0,0] neg_hi:[1,0]
	v_pk_mul_f32 v[124:125], v[130:131], v[128:129] op_sel_hi:[1,0]
	v_pk_mul_f32 v[134:135], v[126:127], v[122:123] op_sel_hi:[1,0]
	v_pk_fma_f32 v[124:125], v[130:131], v[128:129], v[124:125] op_sel:[1,1,0] op_sel_hi:[0,1,1] neg_lo:[1,0,0]
	v_pk_fma_f32 v[134:135], v[126:127], v[122:123], v[134:135] op_sel:[1,1,0] op_sel_hi:[0,1,1] neg_lo:[1,0,0]
	v_pk_mul_f32 v[136:137], v[134:135], v[132:133] op_sel_hi:[1,0]
	v_pk_fma_f32 v[132:133], v[134:135], v[132:133], v[136:137] op_sel:[1,1,0] op_sel_hi:[0,1,1] neg_hi:[1,0,0]
	v_pk_add_f32 v[124:125], v[124:125], v[132:133]
	v_pk_mul_f32 v[132:133], v[130:131], v[122:123] op_sel_hi:[1,0]
	v_pk_fma_f32 v[122:123], v[130:131], v[122:123], v[132:133] op_sel:[1,1,0] op_sel_hi:[0,1,1] neg_lo:[1,0,0]
	v_pk_mul_f32 v[130:131], v[126:127], v[128:129] op_sel_hi:[1,0]
	v_pk_fma_f32 v[126:127], v[126:127], v[128:129], v[130:131] op_sel:[1,1,0] op_sel_hi:[0,1,1] neg_lo:[1,0,0]
	v_pk_add_f32 v[122:123], v[122:123], v[126:127]
	s_nop 0
	v_pk_add_f32 v[126:127], v[124:125], v[122:123] op_sel:[0,1] op_sel_hi:[1,0] neg_lo:[0,1]
	v_pk_add_f32 v[122:123], v[124:125], v[122:123] op_sel:[0,1] op_sel_hi:[1,0] neg_hi:[1,0]
	ds_write_b64 v138, v[126:127]
	ds_write_b64 v139, v[122:123]
	v_add_u32_e32 v122, 10, v209
	v_lshlrev_b32_e32 v124, 10, v122
	v_lshlrev_b32_e32 v125, 2, v122
	v_lshrrev_b32_e32 v126, 5, v122
	v_ashrrev_i32_e32 v122, 11, v122
	v_and_b32_e32 v124, 0x3c00, v124
	v_and_b32_e32 v126, 56, v126
	v_and_or_b32 v122, v125, s9, v122
	v_or3_b32 v122, v122, v124, v126
	v_mul_i32_i24_e32 v122, 9, v122
	v_sub_u32_e32 v123, -10, v209
	v_and_b32_e32 v122, -8, v122
	v_add_u32_e32 v134, 0, v122
	v_lshlrev_b32_e32 v122, 10, v123
	v_lshlrev_b32_e32 v124, 2, v123
	v_lshrrev_b32_e32 v125, 5, v123
	v_bfe_u32 v123, v123, 11, 3
	v_and_b32_e32 v122, 0x3c00, v122
	v_and_b32_e32 v124, 0x3c0, v124
	v_and_or_b32 v123, v125, 56, v123
	v_or3_b32 v122, v123, v124, v122
	v_mul_u32_u24_e32 v122, 9, v122
	v_and_b32_e32 v122, 0x3fff8, v122
	v_add_u32_e32 v135, 0, v122
	ds_read_b64 v[122:123], v134
	ds_read_b64 v[124:125], v135
	v_pk_mul_f32 v[126:127], v[162:163], s[58:59] op_sel_hi:[0,1]
	v_pk_fma_f32 v[128:129], v[38:39], s[60:61], v[126:127] neg_lo:[0,0,1] neg_hi:[0,0,1]
	v_pk_fma_f32 v[126:127], v[158:159], s[60:61], v[126:127] op_sel_hi:[0,1,1]
	v_mov_b32_e32 v129, v127
	s_waitcnt lgkmcnt(0)
	v_pk_add_f32 v[126:127], v[122:123], v[124:125] neg_hi:[0,1]
	v_pk_add_f32 v[122:123], v[122:123], v[124:125] op_sel:[1,1] op_sel_hi:[0,0] neg_hi:[1,0]
	v_pk_add_f32 v[124:125], v[118:119], v[120:121] neg_hi:[0,1]
	v_pk_add_f32 v[118:119], v[118:119], v[120:121] op_sel:[1,1] op_sel_hi:[0,0] neg_hi:[1,0]
	v_pk_mul_f32 v[120:121], v[126:127], v[124:125] op_sel_hi:[1,0]
	v_pk_mul_f32 v[130:131], v[122:123], v[118:119] op_sel_hi:[1,0]
	v_pk_fma_f32 v[120:121], v[126:127], v[124:125], v[120:121] op_sel:[1,1,0] op_sel_hi:[0,1,1] neg_lo:[1,0,0]
	v_pk_fma_f32 v[130:131], v[122:123], v[118:119], v[130:131] op_sel:[1,1,0] op_sel_hi:[0,1,1] neg_lo:[1,0,0]
	v_pk_mul_f32 v[132:133], v[130:131], v[128:129] op_sel_hi:[1,0]
	v_pk_fma_f32 v[128:129], v[130:131], v[128:129], v[132:133] op_sel:[1,1,0] op_sel_hi:[0,1,1] neg_hi:[1,0,0]
	v_pk_add_f32 v[120:121], v[120:121], v[128:129]
	v_pk_mul_f32 v[128:129], v[126:127], v[118:119] op_sel_hi:[1,0]
	v_pk_fma_f32 v[118:119], v[126:127], v[118:119], v[128:129] op_sel:[1,1,0] op_sel_hi:[0,1,1] neg_lo:[1,0,0]
	v_pk_mul_f32 v[126:127], v[122:123], v[124:125] op_sel_hi:[1,0]
	v_pk_fma_f32 v[122:123], v[122:123], v[124:125], v[126:127] op_sel:[1,1,0] op_sel_hi:[0,1,1] neg_lo:[1,0,0]
	v_pk_add_f32 v[118:119], v[118:119], v[122:123]
	s_nop 0
	v_pk_add_f32 v[122:123], v[120:121], v[118:119] op_sel:[0,1] op_sel_hi:[1,0] neg_lo:[0,1]
	v_pk_add_f32 v[118:119], v[120:121], v[118:119] op_sel:[0,1] op_sel_hi:[1,0] neg_hi:[1,0]
	ds_write_b64 v134, v[122:123]
	ds_write_b64 v135, v[118:119]
	v_add_u32_e32 v118, 11, v209
	v_lshlrev_b32_e32 v120, 10, v118
	v_lshlrev_b32_e32 v121, 2, v118
	v_lshrrev_b32_e32 v122, 5, v118
	v_ashrrev_i32_e32 v118, 11, v118
	v_and_b32_e32 v120, 0x3c00, v120
	v_and_b32_e32 v122, 56, v122
	v_and_or_b32 v118, v121, s9, v118
	v_or3_b32 v118, v118, v120, v122
	v_mul_i32_i24_e32 v118, 9, v118
	v_sub_u32_e32 v119, -11, v209
	v_and_b32_e32 v118, -8, v118
	v_add_u32_e32 v130, 0, v118
	v_lshlrev_b32_e32 v118, 10, v119
	v_lshlrev_b32_e32 v120, 2, v119
	v_lshrrev_b32_e32 v121, 5, v119
	v_bfe_u32 v119, v119, 11, 3
	v_and_b32_e32 v118, 0x3c00, v118
	v_and_b32_e32 v120, 0x3c0, v120
	v_and_or_b32 v119, v121, 56, v119
	v_or3_b32 v118, v119, v120, v118
	v_mul_u32_u24_e32 v118, 9, v118
	v_and_b32_e32 v118, 0x3fff8, v118
	v_add_u32_e32 v131, 0, v118
	ds_read_b64 v[118:119], v130
	ds_read_b64 v[120:121], v131
	v_pk_mul_f32 v[122:123], v[162:163], s[62:63] op_sel_hi:[0,1]
	v_pk_fma_f32 v[124:125], v[38:39], s[64:65], v[122:123] neg_lo:[0,0,1] neg_hi:[0,0,1]
	v_pk_fma_f32 v[122:123], v[158:159], s[64:65], v[122:123] op_sel_hi:[0,1,1]
	v_mov_b32_e32 v125, v123
	s_waitcnt lgkmcnt(0)
	v_pk_add_f32 v[122:123], v[118:119], v[120:121] neg_hi:[0,1]
	v_pk_add_f32 v[118:119], v[118:119], v[120:121] op_sel:[1,1] op_sel_hi:[0,0] neg_hi:[1,0]
	v_pk_add_f32 v[120:121], v[114:115], v[116:117] neg_hi:[0,1]
	v_pk_add_f32 v[114:115], v[114:115], v[116:117] op_sel:[1,1] op_sel_hi:[0,0] neg_hi:[1,0]
	v_pk_mul_f32 v[116:117], v[122:123], v[120:121] op_sel_hi:[1,0]
	v_pk_mul_f32 v[126:127], v[118:119], v[114:115] op_sel_hi:[1,0]
	v_pk_fma_f32 v[116:117], v[122:123], v[120:121], v[116:117] op_sel:[1,1,0] op_sel_hi:[0,1,1] neg_lo:[1,0,0]
	v_pk_fma_f32 v[126:127], v[118:119], v[114:115], v[126:127] op_sel:[1,1,0] op_sel_hi:[0,1,1] neg_lo:[1,0,0]
	v_pk_mul_f32 v[128:129], v[126:127], v[124:125] op_sel_hi:[1,0]
	v_pk_fma_f32 v[124:125], v[126:127], v[124:125], v[128:129] op_sel:[1,1,0] op_sel_hi:[0,1,1] neg_hi:[1,0,0]
	v_pk_add_f32 v[116:117], v[116:117], v[124:125]
	v_pk_mul_f32 v[124:125], v[122:123], v[114:115] op_sel_hi:[1,0]
	v_pk_fma_f32 v[114:115], v[122:123], v[114:115], v[124:125] op_sel:[1,1,0] op_sel_hi:[0,1,1] neg_lo:[1,0,0]
	v_pk_mul_f32 v[122:123], v[118:119], v[120:121] op_sel_hi:[1,0]
	v_pk_fma_f32 v[118:119], v[118:119], v[120:121], v[122:123] op_sel:[1,1,0] op_sel_hi:[0,1,1] neg_lo:[1,0,0]
	v_pk_add_f32 v[114:115], v[114:115], v[118:119]
	s_nop 0
	v_pk_add_f32 v[118:119], v[116:117], v[114:115] op_sel:[0,1] op_sel_hi:[1,0] neg_lo:[0,1]
	v_pk_add_f32 v[114:115], v[116:117], v[114:115] op_sel:[0,1] op_sel_hi:[1,0] neg_hi:[1,0]
	ds_write_b64 v130, v[118:119]
	ds_write_b64 v131, v[114:115]
	v_add_u32_e32 v114, 12, v209
	v_lshlrev_b32_e32 v116, 10, v114
	v_lshlrev_b32_e32 v117, 2, v114
	v_lshrrev_b32_e32 v118, 5, v114
	v_ashrrev_i32_e32 v114, 11, v114
	v_and_b32_e32 v116, 0x3c00, v116
	v_and_b32_e32 v118, 56, v118
	v_and_or_b32 v114, v117, s9, v114
	v_or3_b32 v114, v114, v116, v118
	v_mul_i32_i24_e32 v114, 9, v114
	v_sub_u32_e32 v115, -12, v209
	v_and_b32_e32 v114, -8, v114
	v_add_u32_e32 v126, 0, v114
	v_lshlrev_b32_e32 v114, 10, v115
	v_lshlrev_b32_e32 v116, 2, v115
	v_lshrrev_b32_e32 v117, 5, v115
	v_bfe_u32 v115, v115, 11, 3
	v_and_b32_e32 v114, 0x3c00, v114
	v_and_b32_e32 v116, 0x3c0, v116
	v_and_or_b32 v115, v117, 56, v115
	v_or3_b32 v114, v115, v116, v114
	v_mul_u32_u24_e32 v114, 9, v114
	v_and_b32_e32 v114, 0x3fff8, v114
	v_add_u32_e32 v127, 0, v114
	ds_read_b64 v[114:115], v126
	ds_read_b64 v[116:117], v127
	v_pk_mul_f32 v[118:119], v[162:163], s[66:67] op_sel_hi:[0,1]
	v_pk_fma_f32 v[120:121], v[38:39], s[68:69], v[118:119] neg_lo:[0,0,1] neg_hi:[0,0,1]
	v_pk_fma_f32 v[118:119], v[158:159], s[68:69], v[118:119] op_sel_hi:[0,1,1]
	v_mov_b32_e32 v121, v119
	s_waitcnt lgkmcnt(0)
	v_pk_add_f32 v[118:119], v[114:115], v[116:117] neg_hi:[0,1]
	v_pk_add_f32 v[114:115], v[114:115], v[116:117] op_sel:[1,1] op_sel_hi:[0,0] neg_hi:[1,0]
	v_pk_add_f32 v[116:117], v[110:111], v[112:113] neg_hi:[0,1]
	v_pk_add_f32 v[110:111], v[110:111], v[112:113] op_sel:[1,1] op_sel_hi:[0,0] neg_hi:[1,0]
	v_pk_mul_f32 v[112:113], v[118:119], v[116:117] op_sel_hi:[1,0]
	v_pk_mul_f32 v[122:123], v[114:115], v[110:111] op_sel_hi:[1,0]
	v_pk_fma_f32 v[112:113], v[118:119], v[116:117], v[112:113] op_sel:[1,1,0] op_sel_hi:[0,1,1] neg_lo:[1,0,0]
	v_pk_fma_f32 v[122:123], v[114:115], v[110:111], v[122:123] op_sel:[1,1,0] op_sel_hi:[0,1,1] neg_lo:[1,0,0]
	v_pk_mul_f32 v[124:125], v[122:123], v[120:121] op_sel_hi:[1,0]
	v_pk_fma_f32 v[120:121], v[122:123], v[120:121], v[124:125] op_sel:[1,1,0] op_sel_hi:[0,1,1] neg_hi:[1,0,0]
	v_pk_add_f32 v[112:113], v[112:113], v[120:121]
	v_pk_mul_f32 v[120:121], v[118:119], v[110:111] op_sel_hi:[1,0]
	v_pk_fma_f32 v[110:111], v[118:119], v[110:111], v[120:121] op_sel:[1,1,0] op_sel_hi:[0,1,1] neg_lo:[1,0,0]
	v_pk_mul_f32 v[118:119], v[114:115], v[116:117] op_sel_hi:[1,0]
	v_pk_fma_f32 v[114:115], v[114:115], v[116:117], v[118:119] op_sel:[1,1,0] op_sel_hi:[0,1,1] neg_lo:[1,0,0]
	v_pk_add_f32 v[110:111], v[110:111], v[114:115]
	s_nop 0
	v_pk_add_f32 v[114:115], v[112:113], v[110:111] op_sel:[0,1] op_sel_hi:[1,0] neg_lo:[0,1]
	v_pk_add_f32 v[110:111], v[112:113], v[110:111] op_sel:[0,1] op_sel_hi:[1,0] neg_hi:[1,0]
	ds_write_b64 v126, v[114:115]
	ds_write_b64 v127, v[110:111]
	v_add_u32_e32 v110, 13, v209
	v_lshlrev_b32_e32 v112, 10, v110
	v_lshlrev_b32_e32 v113, 2, v110
	v_lshrrev_b32_e32 v114, 5, v110
	v_ashrrev_i32_e32 v110, 11, v110
	v_and_b32_e32 v112, 0x3c00, v112
	v_and_b32_e32 v114, 56, v114
	v_and_or_b32 v110, v113, s9, v110
	v_or3_b32 v110, v110, v112, v114
	v_mul_i32_i24_e32 v110, 9, v110
	v_sub_u32_e32 v111, -13, v209
	v_and_b32_e32 v110, -8, v110
	v_add_u32_e32 v122, 0, v110
	v_lshlrev_b32_e32 v110, 10, v111
	v_lshlrev_b32_e32 v112, 2, v111
	v_lshrrev_b32_e32 v113, 5, v111
	v_bfe_u32 v111, v111, 11, 3
	v_and_b32_e32 v110, 0x3c00, v110
	v_and_b32_e32 v112, 0x3c0, v112
	v_and_or_b32 v111, v113, 56, v111
	v_or3_b32 v110, v111, v112, v110
	v_mul_u32_u24_e32 v110, 9, v110
	v_and_b32_e32 v110, 0x3fff8, v110
	v_add_u32_e32 v123, 0, v110
	ds_read_b64 v[110:111], v122
	ds_read_b64 v[112:113], v123
	v_pk_mul_f32 v[114:115], v[162:163], s[70:71] op_sel_hi:[0,1]
	v_pk_fma_f32 v[116:117], v[38:39], s[72:73], v[114:115] neg_lo:[0,0,1] neg_hi:[0,0,1]
	v_pk_fma_f32 v[114:115], v[158:159], s[72:73], v[114:115] op_sel_hi:[0,1,1]
	v_mov_b32_e32 v117, v115
	s_waitcnt lgkmcnt(0)
	v_pk_add_f32 v[114:115], v[110:111], v[112:113] neg_hi:[0,1]
	v_pk_add_f32 v[110:111], v[110:111], v[112:113] op_sel:[1,1] op_sel_hi:[0,0] neg_hi:[1,0]
	v_pk_add_f32 v[112:113], v[106:107], v[108:109] neg_hi:[0,1]
	v_pk_add_f32 v[106:107], v[106:107], v[108:109] op_sel:[1,1] op_sel_hi:[0,0] neg_hi:[1,0]
	v_pk_mul_f32 v[108:109], v[114:115], v[112:113] op_sel_hi:[1,0]
	v_pk_mul_f32 v[118:119], v[110:111], v[106:107] op_sel_hi:[1,0]
	v_pk_fma_f32 v[108:109], v[114:115], v[112:113], v[108:109] op_sel:[1,1,0] op_sel_hi:[0,1,1] neg_lo:[1,0,0]
	v_pk_fma_f32 v[118:119], v[110:111], v[106:107], v[118:119] op_sel:[1,1,0] op_sel_hi:[0,1,1] neg_lo:[1,0,0]
	v_pk_mul_f32 v[120:121], v[118:119], v[116:117] op_sel_hi:[1,0]
	v_pk_fma_f32 v[116:117], v[118:119], v[116:117], v[120:121] op_sel:[1,1,0] op_sel_hi:[0,1,1] neg_hi:[1,0,0]
	v_pk_add_f32 v[108:109], v[108:109], v[116:117]
	v_pk_mul_f32 v[116:117], v[114:115], v[106:107] op_sel_hi:[1,0]
	v_pk_fma_f32 v[106:107], v[114:115], v[106:107], v[116:117] op_sel:[1,1,0] op_sel_hi:[0,1,1] neg_lo:[1,0,0]
	v_pk_mul_f32 v[114:115], v[110:111], v[112:113] op_sel_hi:[1,0]
	v_pk_fma_f32 v[110:111], v[110:111], v[112:113], v[114:115] op_sel:[1,1,0] op_sel_hi:[0,1,1] neg_lo:[1,0,0]
	v_pk_add_f32 v[106:107], v[106:107], v[110:111]
	s_nop 0
	v_pk_add_f32 v[110:111], v[108:109], v[106:107] op_sel:[0,1] op_sel_hi:[1,0] neg_lo:[0,1]
	v_pk_add_f32 v[106:107], v[108:109], v[106:107] op_sel:[0,1] op_sel_hi:[1,0] neg_hi:[1,0]
	ds_write_b64 v122, v[110:111]
	ds_write_b64 v123, v[106:107]
	v_add_u32_e32 v106, 14, v209
	v_lshlrev_b32_e32 v108, 10, v106
	v_lshlrev_b32_e32 v109, 2, v106
	v_lshrrev_b32_e32 v110, 5, v106
	v_ashrrev_i32_e32 v106, 11, v106
	v_and_b32_e32 v108, 0x3c00, v108
	v_and_b32_e32 v110, 56, v110
	v_and_or_b32 v106, v109, s9, v106
	v_or3_b32 v106, v106, v108, v110
	v_mul_i32_i24_e32 v106, 9, v106
	v_sub_u32_e32 v107, -14, v209
	v_and_b32_e32 v106, -8, v106
	v_add_u32_e32 v118, 0, v106
	v_lshlrev_b32_e32 v106, 10, v107
	v_lshlrev_b32_e32 v108, 2, v107
	v_lshrrev_b32_e32 v109, 5, v107
	v_bfe_u32 v107, v107, 11, 3
	v_and_b32_e32 v106, 0x3c00, v106
	v_and_b32_e32 v108, 0x3c0, v108
	v_and_or_b32 v107, v109, 56, v107
	v_or3_b32 v106, v107, v108, v106
	v_mul_u32_u24_e32 v106, 9, v106
	v_and_b32_e32 v106, 0x3fff8, v106
	v_add_u32_e32 v119, 0, v106
	ds_read_b64 v[106:107], v118
	ds_read_b64 v[108:109], v119
	v_pk_mul_f32 v[110:111], v[162:163], s[74:75] op_sel_hi:[0,1]
	v_pk_fma_f32 v[112:113], v[38:39], s[76:77], v[110:111] neg_lo:[0,0,1] neg_hi:[0,0,1]
	v_pk_fma_f32 v[110:111], v[158:159], s[76:77], v[110:111] op_sel_hi:[0,1,1]
	v_mov_b32_e32 v113, v111
	s_waitcnt lgkmcnt(0)
	v_pk_add_f32 v[110:111], v[106:107], v[108:109] neg_hi:[0,1]
	v_pk_add_f32 v[106:107], v[106:107], v[108:109] op_sel:[1,1] op_sel_hi:[0,0] neg_hi:[1,0]
	v_pk_add_f32 v[108:109], v[102:103], v[104:105] neg_hi:[0,1]
	v_pk_add_f32 v[102:103], v[102:103], v[104:105] op_sel:[1,1] op_sel_hi:[0,0] neg_hi:[1,0]
	v_pk_mul_f32 v[104:105], v[110:111], v[108:109] op_sel_hi:[1,0]
	v_pk_mul_f32 v[114:115], v[106:107], v[102:103] op_sel_hi:[1,0]
	v_pk_fma_f32 v[104:105], v[110:111], v[108:109], v[104:105] op_sel:[1,1,0] op_sel_hi:[0,1,1] neg_lo:[1,0,0]
	v_pk_fma_f32 v[114:115], v[106:107], v[102:103], v[114:115] op_sel:[1,1,0] op_sel_hi:[0,1,1] neg_lo:[1,0,0]
	v_pk_mul_f32 v[116:117], v[114:115], v[112:113] op_sel_hi:[1,0]
	v_pk_fma_f32 v[112:113], v[114:115], v[112:113], v[116:117] op_sel:[1,1,0] op_sel_hi:[0,1,1] neg_hi:[1,0,0]
	v_pk_add_f32 v[104:105], v[104:105], v[112:113]
	v_pk_mul_f32 v[112:113], v[110:111], v[102:103] op_sel_hi:[1,0]
	v_pk_fma_f32 v[102:103], v[110:111], v[102:103], v[112:113] op_sel:[1,1,0] op_sel_hi:[0,1,1] neg_lo:[1,0,0]
	v_pk_mul_f32 v[110:111], v[106:107], v[108:109] op_sel_hi:[1,0]
	v_pk_fma_f32 v[106:107], v[106:107], v[108:109], v[110:111] op_sel:[1,1,0] op_sel_hi:[0,1,1] neg_lo:[1,0,0]
	v_pk_add_f32 v[102:103], v[102:103], v[106:107]
	s_nop 0
	v_pk_add_f32 v[106:107], v[104:105], v[102:103] op_sel:[0,1] op_sel_hi:[1,0] neg_lo:[0,1]
	v_pk_add_f32 v[102:103], v[104:105], v[102:103] op_sel:[0,1] op_sel_hi:[1,0] neg_hi:[1,0]
	ds_write_b64 v118, v[106:107]
	ds_write_b64 v119, v[102:103]
	v_add_u32_e32 v102, 15, v209
	v_lshlrev_b32_e32 v104, 10, v102
	v_lshlrev_b32_e32 v105, 2, v102
	v_lshrrev_b32_e32 v106, 5, v102
	v_ashrrev_i32_e32 v102, 11, v102
	v_and_b32_e32 v104, 0x3c00, v104
	v_and_b32_e32 v106, 56, v106
	v_and_or_b32 v102, v105, s9, v102
	v_or3_b32 v102, v102, v104, v106
	v_mul_i32_i24_e32 v102, 9, v102
	v_sub_u32_e32 v103, -15, v209
	v_and_b32_e32 v102, -8, v102
	v_add_u32_e32 v114, 0, v102
	v_lshlrev_b32_e32 v102, 10, v103
	v_lshlrev_b32_e32 v104, 2, v103
	v_lshrrev_b32_e32 v105, 5, v103
	v_bfe_u32 v103, v103, 11, 3
	v_and_b32_e32 v102, 0x3c00, v102
	v_and_b32_e32 v104, 0x3c0, v104
	v_and_or_b32 v103, v105, 56, v103
	v_or3_b32 v102, v103, v104, v102
	v_mul_u32_u24_e32 v102, 9, v102
	v_and_b32_e32 v102, 0x3fff8, v102
	v_add_u32_e32 v115, 0, v102
	ds_read_b64 v[102:103], v114
	ds_read_b64 v[104:105], v115
	v_pk_mul_f32 v[106:107], v[162:163], s[78:79] op_sel_hi:[0,1]
	v_pk_fma_f32 v[108:109], v[38:39], s[80:81], v[106:107] neg_lo:[0,0,1] neg_hi:[0,0,1]
	v_pk_fma_f32 v[106:107], v[158:159], s[80:81], v[106:107] op_sel_hi:[0,1,1]
	v_mov_b32_e32 v109, v107
	s_waitcnt lgkmcnt(0)
	v_pk_add_f32 v[106:107], v[102:103], v[104:105] neg_hi:[0,1]
	v_pk_add_f32 v[102:103], v[102:103], v[104:105] op_sel:[1,1] op_sel_hi:[0,0] neg_hi:[1,0]
	v_pk_add_f32 v[104:105], v[2:3], v[4:5] neg_hi:[0,1]
	v_pk_add_f32 v[2:3], v[2:3], v[4:5] op_sel:[1,1] op_sel_hi:[0,0] neg_hi:[1,0]
	v_pk_mul_f32 v[4:5], v[106:107], v[104:105] op_sel_hi:[1,0]
	v_pk_mul_f32 v[110:111], v[102:103], v[2:3] op_sel_hi:[1,0]
	v_pk_fma_f32 v[4:5], v[106:107], v[104:105], v[4:5] op_sel:[1,1,0] op_sel_hi:[0,1,1] neg_lo:[1,0,0]
	v_pk_fma_f32 v[110:111], v[102:103], v[2:3], v[110:111] op_sel:[1,1,0] op_sel_hi:[0,1,1] neg_lo:[1,0,0]
	v_pk_mul_f32 v[112:113], v[110:111], v[108:109] op_sel_hi:[1,0]
	v_pk_fma_f32 v[108:109], v[110:111], v[108:109], v[112:113] op_sel:[1,1,0] op_sel_hi:[0,1,1] neg_hi:[1,0,0]
	v_pk_add_f32 v[4:5], v[4:5], v[108:109]
	v_pk_mul_f32 v[108:109], v[106:107], v[2:3] op_sel_hi:[1,0]
	v_pk_fma_f32 v[2:3], v[106:107], v[2:3], v[108:109] op_sel:[1,1,0] op_sel_hi:[0,1,1] neg_lo:[1,0,0]
	v_pk_mul_f32 v[106:107], v[102:103], v[104:105] op_sel_hi:[1,0]
	v_pk_fma_f32 v[102:103], v[102:103], v[104:105], v[106:107] op_sel:[1,1,0] op_sel_hi:[0,1,1] neg_lo:[1,0,0]
	v_pk_add_f32 v[2:3], v[2:3], v[102:103]
	s_nop 0
	v_pk_add_f32 v[102:103], v[4:5], v[2:3] op_sel:[0,1] op_sel_hi:[1,0] neg_lo:[0,1]
	ds_write_b64 v114, v[102:103]
	v_pk_add_f32 v[2:3], v[4:5], v[2:3] op_sel:[0,1] op_sel_hi:[1,0] neg_hi:[1,0]
	ds_write_b64 v115, v[2:3]
	s_and_saveexec_b64 s[84:85], s[0:1]
	s_cbranch_execz .LBB0_771
	v_mov_b32_e32 v4, s94
	ds_read_b64 v[2:3], v203 offset:32
	ds_read_b64 v[4:5], v4
	s_waitcnt lgkmcnt(1)
	v_pk_add_f32 v[102:103], v[2:3], v[2:3] neg_hi:[0,1]
	v_pk_add_f32 v[2:3], v[2:3], v[2:3] op_sel:[1,1] op_sel_hi:[0,0] neg_hi:[1,0]
	s_waitcnt lgkmcnt(0)
	v_pk_add_f32 v[104:105], v[4:5], v[4:5] neg_hi:[0,1]
	v_pk_add_f32 v[4:5], v[4:5], v[4:5] op_sel:[1,1] op_sel_hi:[0,0] neg_hi:[1,0]
	v_mov_b64_e32 v[110:111], s[2:3]
	v_pk_mul_f32 v[108:109], v[2:3], v[4:5] op_sel_hi:[1,0]
	v_pk_mul_f32 v[106:107], v[102:103], v[104:105] op_sel_hi:[1,0]
	v_pk_fma_f32 v[108:109], v[2:3], v[4:5], v[108:109] op_sel:[1,1,0] op_sel_hi:[0,1,1] neg_lo:[1,0,0]
	v_pk_fma_f32 v[106:107], v[102:103], v[104:105], v[106:107] op_sel:[1,1,0] op_sel_hi:[0,1,1] neg_lo:[1,0,0]
	v_pk_mul_f32 v[112:113], v[108:109], v[110:111] op_sel_hi:[1,0]
	v_pk_fma_f32 v[108:109], v[108:109], v[110:111], v[112:113] op_sel:[1,1,0] op_sel_hi:[0,1,1] neg_hi:[1,0,0]
	v_pk_add_f32 v[106:107], v[106:107], v[108:109]
	v_pk_mul_f32 v[108:109], v[102:103], v[4:5] op_sel_hi:[1,0]
	v_pk_fma_f32 v[4:5], v[102:103], v[4:5], v[108:109] op_sel:[1,1,0] op_sel_hi:[0,1,1] neg_lo:[1,0,0]
	v_pk_mul_f32 v[102:103], v[2:3], v[104:105] op_sel_hi:[1,0]
	v_pk_fma_f32 v[2:3], v[2:3], v[104:105], v[102:103] op_sel:[1,1,0] op_sel_hi:[0,1,1] neg_lo:[1,0,0]
	v_pk_add_f32 v[2:3], v[4:5], v[2:3]
	s_nop 0
	v_pk_add_f32 v[2:3], v[106:107], v[2:3] op_sel:[0,1] op_sel_hi:[1,0] neg_hi:[1,0]
	ds_write_b64 v203, v[2:3] offset:32

.LBB0_774:
	v_add_u32_e32 v3, s85, v2
	ds_read2_b64 v[102:105], v3 offset1:1
	ds_read2_b64 v[106:109], v3 offset0:2 offset1:3
	ds_read2_b64 v[110:113], v3 offset0:4 offset1:5
	ds_read2_b64 v[114:117], v3 offset0:6 offset1:7
	s_add_i32 s85, s85, 0x9000
	s_cmp_lg_u32 s85, 0x24000
	s_waitcnt lgkmcnt(1)
	v_pk_add_f32 v[4:5], v[102:103], v[110:111]
	v_pk_add_f32 v[102:103], v[102:103], v[110:111] neg_lo:[0,1] neg_hi:[0,1]
	v_pk_add_f32 v[110:111], v[104:105], v[112:113]
	v_pk_add_f32 v[104:105], v[104:105], v[112:113] neg_lo:[0,1] neg_hi:[0,1]
	v_mov_b64_e32 v[112:113], s[6:7]
	v_pk_mul_f32 v[118:119], v[104:105], v[112:113] op_sel_hi:[1,0]
	v_pk_fma_f32 v[104:105], v[104:105], v[112:113], v[118:119] op_sel:[1,1,0] op_sel_hi:[0,1,1] neg_lo:[1,0,0]
	s_waitcnt lgkmcnt(0)
	v_pk_add_f32 v[112:113], v[106:107], v[114:115]
	v_pk_add_f32 v[106:107], v[106:107], v[114:115] op_sel:[1,1] op_sel_hi:[0,0] neg_lo:[1,0] neg_hi:[0,1]
	v_pk_add_f32 v[114:115], v[108:109], v[116:117]
	v_pk_add_f32 v[108:109], v[108:109], v[116:117] neg_lo:[0,1] neg_hi:[0,1]
	v_mov_b64_e32 v[116:117], s[14:15]
	v_pk_mul_f32 v[118:119], v[108:109], v[116:117] op_sel_hi:[1,0]
	v_pk_fma_f32 v[108:109], v[108:109], v[116:117], v[118:119] op_sel:[1,1,0] op_sel_hi:[0,1,1] neg_lo:[1,0,0]
	v_pk_add_f32 v[116:117], v[4:5], v[112:113]
	v_pk_add_f32 v[4:5], v[4:5], v[112:113] neg_lo:[0,1] neg_hi:[0,1]
	v_pk_add_f32 v[112:113], v[110:111], v[114:115]
	v_pk_add_f32 v[110:111], v[110:111], v[114:115] op_sel:[1,1] op_sel_hi:[0,0] neg_lo:[1,0] neg_hi:[0,1]
	v_pk_add_f32 v[114:115], v[102:103], v[106:107]
	v_pk_add_f32 v[102:103], v[102:103], v[106:107] neg_lo:[0,1] neg_hi:[0,1]
	v_pk_add_f32 v[106:107], v[104:105], v[108:109]
	v_pk_add_f32 v[104:105], v[104:105], v[108:109] op_sel:[1,1] op_sel_hi:[0,0] neg_lo:[1,0] neg_hi:[0,1]
	v_pk_add_f32 v[108:109], v[116:117], v[112:113]
	v_pk_add_f32 v[112:113], v[116:117], v[112:113] neg_lo:[0,1] neg_hi:[0,1]
	v_pk_add_f32 v[116:117], v[4:5], v[110:111]
	v_pk_add_f32 v[4:5], v[4:5], v[110:111] neg_lo:[0,1] neg_hi:[0,1]
	v_pk_add_f32 v[110:111], v[114:115], v[106:107]
	v_pk_add_f32 v[106:107], v[114:115], v[106:107] neg_lo:[0,1] neg_hi:[0,1]
	v_pk_add_f32 v[114:115], v[102:103], v[104:105]
	v_pk_add_f32 v[102:103], v[102:103], v[104:105] neg_lo:[0,1] neg_hi:[0,1]
	ds_write2_b64 v3, v[108:109], v[110:111] offset1:1
	ds_write2_b64 v3, v[116:117], v[114:115] offset0:2 offset1:3
	ds_write2_b64 v3, v[112:113], v[106:107] offset0:4 offset1:5
	ds_write2_b64 v3, v[4:5], v[102:103] offset0:6 offset1:7
	s_cbranch_scc1 .LBB0_774
	v_mov_b32_e32 v4, v204
	s_waitcnt lgkmcnt(0)
	s_barrier
	s_mov_b32 s85, 0
	v_and_b32_e32 v5, 7, v4
	v_cvt_f32_ubyte0_e32 v2, v5
	v_mul_f32_e32 v3, 0x3c800000, v2
	v_cos_f32_e32 v2, v3
	v_sin_f32_e32 v3, v3
	v_lshlrev_b32_e32 v4, 3, v4
	v_lshl_add_u32 v5, v5, 3, 0
.LBB0_776:
	v_add_u32_e32 v38, s85, v4
	v_and_b32_e32 v38, 0xffffffc0, v38
	v_lshlrev_b32_e32 v102, 3, v38
	v_add3_u32 v38, v5, v38, v102
	ds_read2_b64 v[102:105], v38 offset1:9
	s_waitcnt lgkmcnt(0)
	v_pk_mul_f32 v[106:107], v[104:105], v[2:3] op_sel_hi:[1,0]
	s_addk_i32 s85, 0x1000
	v_pk_fma_f32 v[108:109], v[104:105], v[2:3], v[106:107] op_sel:[1,1,0] op_sel_hi:[0,1,1] neg_lo:[1,0,0]
	v_pk_mul_f32 v[104:105], v[2:3], v[2:3] op_sel_hi:[1,0]
	s_cmpk_lg_i32 s85, 0x4000
	v_pk_fma_f32 v[110:111], v[2:3], v[2:3], v[104:105] op_sel:[1,1,0] op_sel_hi:[0,1,1] neg_lo:[1,0,0]
	ds_read2_b64 v[104:107], v38 offset0:18 offset1:27
	s_waitcnt lgkmcnt(0)
	v_pk_mul_f32 v[112:113], v[104:105], v[110:111] op_sel_hi:[1,0]
	v_pk_fma_f32 v[112:113], v[104:105], v[110:111], v[112:113] op_sel:[1,1,0] op_sel_hi:[0,1,1] neg_lo:[1,0,0]
	v_pk_mul_f32 v[104:105], v[110:111], v[2:3] op_sel_hi:[1,0]
	v_pk_fma_f32 v[104:105], v[110:111], v[2:3], v[104:105] op_sel:[1,1,0] op_sel_hi:[0,1,1] neg_lo:[1,0,0]
	v_pk_mul_f32 v[110:111], v[106:107], v[104:105] op_sel_hi:[1,0]
	v_pk_fma_f32 v[110:111], v[106:107], v[104:105], v[110:111] op_sel:[1,1,0] op_sel_hi:[0,1,1] neg_lo:[1,0,0]
	v_pk_mul_f32 v[106:107], v[104:105], v[2:3] op_sel_hi:[1,0]
	v_pk_fma_f32 v[114:115], v[104:105], v[2:3], v[106:107] op_sel:[1,1,0] op_sel_hi:[0,1,1] neg_lo:[1,0,0]
	ds_read2_b64 v[104:107], v38 offset0:36 offset1:45
	s_waitcnt lgkmcnt(0)
	v_pk_mul_f32 v[116:117], v[104:105], v[114:115] op_sel_hi:[1,0]
	v_pk_fma_f32 v[116:117], v[104:105], v[114:115], v[116:117] op_sel:[1,1,0] op_sel_hi:[0,1,1] neg_lo:[1,0,0]
	v_pk_mul_f32 v[104:105], v[114:115], v[2:3] op_sel_hi:[1,0]
	v_pk_fma_f32 v[104:105], v[114:115], v[2:3], v[104:105] op_sel:[1,1,0] op_sel_hi:[0,1,1] neg_lo:[1,0,0]
	v_pk_mul_f32 v[114:115], v[106:107], v[104:105] op_sel_hi:[1,0]
	v_pk_fma_f32 v[114:115], v[106:107], v[104:105], v[114:115] op_sel:[1,1,0] op_sel_hi:[0,1,1] neg_lo:[1,0,0]
	v_pk_mul_f32 v[106:107], v[104:105], v[2:3] op_sel_hi:[1,0]
	v_pk_fma_f32 v[118:119], v[104:105], v[2:3], v[106:107] op_sel:[1,1,0] op_sel_hi:[0,1,1] neg_lo:[1,0,0]
	ds_read2_b64 v[104:107], v38 offset0:54 offset1:63
	s_waitcnt lgkmcnt(0)
	v_pk_mul_f32 v[120:121], v[104:105], v[118:119] op_sel_hi:[1,0]
	v_pk_fma_f32 v[104:105], v[104:105], v[118:119], v[120:121] op_sel:[1,1,0] op_sel_hi:[0,1,1] neg_lo:[1,0,0]
	v_pk_mul_f32 v[120:121], v[118:119], v[2:3] op_sel_hi:[1,0]
	v_pk_fma_f32 v[118:119], v[118:119], v[2:3], v[120:121] op_sel:[1,1,0] op_sel_hi:[0,1,1] neg_lo:[1,0,0]
	v_pk_mul_f32 v[120:121], v[106:107], v[118:119] op_sel_hi:[1,0]
	v_pk_fma_f32 v[106:107], v[106:107], v[118:119], v[120:121] op_sel:[1,1,0] op_sel_hi:[0,1,1] neg_lo:[1,0,0]
	v_pk_add_f32 v[118:119], v[102:103], v[116:117]
	v_pk_add_f32 v[102:103], v[102:103], v[116:117] neg_lo:[0,1] neg_hi:[0,1]
	v_pk_add_f32 v[116:117], v[108:109], v[114:115]
	v_pk_add_f32 v[108:109], v[108:109], v[114:115] neg_lo:[0,1] neg_hi:[0,1]
	v_mov_b64_e32 v[114:115], s[6:7]
	v_pk_mul_f32 v[120:121], v[108:109], v[114:115] op_sel_hi:[1,0]
	v_pk_fma_f32 v[108:109], v[108:109], v[114:115], v[120:121] op_sel:[1,1,0] op_sel_hi:[0,1,1] neg_lo:[1,0,0]
	v_pk_add_f32 v[114:115], v[112:113], v[104:105]
	v_pk_add_f32 v[104:105], v[112:113], v[104:105] op_sel:[1,1] op_sel_hi:[0,0] neg_lo:[1,0] neg_hi:[0,1]
	v_pk_add_f32 v[112:113], v[110:111], v[106:107]
	v_pk_add_f32 v[106:107], v[110:111], v[106:107] neg_lo:[0,1] neg_hi:[0,1]
	v_mov_b64_e32 v[110:111], s[14:15]
	v_pk_mul_f32 v[120:121], v[106:107], v[110:111] op_sel_hi:[1,0]
	v_pk_fma_f32 v[106:107], v[106:107], v[110:111], v[120:121] op_sel:[1,1,0] op_sel_hi:[0,1,1] neg_lo:[1,0,0]
	v_pk_add_f32 v[110:111], v[118:119], v[114:115]
	v_pk_add_f32 v[114:115], v[118:119], v[114:115] neg_lo:[0,1] neg_hi:[0,1]
	v_pk_add_f32 v[118:119], v[116:117], v[112:113]
	v_pk_add_f32 v[112:113], v[116:117], v[112:113] op_sel:[1,1] op_sel_hi:[0,0] neg_lo:[1,0] neg_hi:[0,1]
	v_pk_add_f32 v[116:117], v[102:103], v[104:105]
	v_pk_add_f32 v[102:103], v[102:103], v[104:105] neg_lo:[0,1] neg_hi:[0,1]
	v_pk_add_f32 v[104:105], v[108:109], v[106:107]
	v_pk_add_f32 v[106:107], v[108:109], v[106:107] op_sel:[1,1] op_sel_hi:[0,0] neg_lo:[1,0] neg_hi:[0,1]
	v_pk_add_f32 v[108:109], v[110:111], v[118:119]
	v_pk_add_f32 v[110:111], v[110:111], v[118:119] neg_lo:[0,1] neg_hi:[0,1]
	v_pk_add_f32 v[118:119], v[114:115], v[112:113]
	v_pk_add_f32 v[112:113], v[114:115], v[112:113] neg_lo:[0,1] neg_hi:[0,1]
	v_pk_add_f32 v[114:115], v[116:117], v[104:105]
	v_pk_add_f32 v[104:105], v[116:117], v[104:105] neg_lo:[0,1] neg_hi:[0,1]
	v_pk_add_f32 v[116:117], v[102:103], v[106:107]
	v_pk_add_f32 v[102:103], v[102:103], v[106:107] neg_lo:[0,1] neg_hi:[0,1]
	ds_write2_b64 v38, v[108:109], v[114:115] offset1:9
	ds_write2_b64 v38, v[118:119], v[116:117] offset0:18 offset1:27
	ds_write2_b64 v38, v[110:111], v[104:105] offset0:36 offset1:45
	ds_write2_b64 v38, v[112:113], v[102:103] offset0:54 offset1:63
	s_cbranch_scc1 .LBB0_776
	v_mov_b32_e32 v4, v204
	s_waitcnt lgkmcnt(0)
	s_barrier
	s_mov_b32 s85, 0
	v_and_b32_e32 v38, 63, v4
	v_cvt_f32_ubyte0_e32 v2, v38
	v_mul_f32_e32 v3, 0x3a800000, v2
	v_cos_f32_e32 v2, v3
	v_sin_f32_e32 v3, v3
	v_lshlrev_b32_e32 v132, 4, v4
	s_mov_b64 s[86:87], -1
.LBB0_778:
	v_add_u32_e32 v4, s85, v132
	v_and_b32_e32 v4, 0xfffffc00, v4
	v_or_b32_e32 v5, v4, v38
	v_bitop3_b32 v4, v4, s97, v38 bitop3:0xc8
	v_lshlrev_b32_e32 v5, 3, v5
	v_add3_u32 v133, 0, v4, v5
	ds_read2_b64 v[102:105], v133 offset1:72
	s_waitcnt lgkmcnt(0)
	v_pk_mul_f32 v[4:5], v[104:105], v[2:3] op_sel_hi:[1,0]
	v_add_u32_e32 v134, 0x800, v133
	v_pk_fma_f32 v[130:131], v[104:105], v[2:3], v[4:5] op_sel:[1,1,0] op_sel_hi:[0,1,1] neg_lo:[1,0,0]
	v_pk_mul_f32 v[4:5], v[2:3], v[2:3] op_sel_hi:[1,0]
	ds_read2_b64 v[104:107], v133 offset0:144 offset1:216
	v_pk_fma_f32 v[4:5], v[2:3], v[2:3], v[4:5] op_sel:[1,1,0] op_sel_hi:[0,1,1] neg_lo:[1,0,0]
	v_add_u32_e32 v135, 0x1000, v133
	s_waitcnt lgkmcnt(0)
	v_pk_mul_f32 v[108:109], v[104:105], v[4:5] op_sel_hi:[1,0]
	v_add_u32_e32 v136, 0x1400, v133
	v_pk_fma_f32 v[120:121], v[104:105], v[4:5], v[108:109] op_sel:[1,1,0] op_sel_hi:[0,1,1] neg_lo:[1,0,0]
	v_pk_mul_f32 v[104:105], v[4:5], v[2:3] op_sel_hi:[1,0]
	v_add_u32_e32 v137, 0x1800, v133
	v_pk_fma_f32 v[4:5], v[4:5], v[2:3], v[104:105] op_sel:[1,1,0] op_sel_hi:[0,1,1] neg_lo:[1,0,0]
	v_add_u32_e32 v138, 0x1c00, v133
	v_pk_mul_f32 v[104:105], v[106:107], v[4:5] op_sel_hi:[1,0]
	s_movk_i32 s85, 0x2000
	v_pk_fma_f32 v[118:119], v[106:107], v[4:5], v[104:105] op_sel:[1,1,0] op_sel_hi:[0,1,1] neg_lo:[1,0,0]
	v_pk_mul_f32 v[104:105], v[4:5], v[2:3] op_sel_hi:[1,0]
	s_and_b64 vcc, exec, s[86:87]
	v_pk_fma_f32 v[4:5], v[4:5], v[2:3], v[104:105] op_sel:[1,1,0] op_sel_hi:[0,1,1] neg_lo:[1,0,0]
	ds_read2_b64 v[104:107], v134 offset0:32 offset1:104
	s_waitcnt lgkmcnt(0)
	v_pk_mul_f32 v[108:109], v[104:105], v[4:5] op_sel_hi:[1,0]
	s_mov_b64 s[86:87], 0
	v_pk_fma_f32 v[112:113], v[104:105], v[4:5], v[108:109] op_sel:[1,1,0] op_sel_hi:[0,1,1] neg_lo:[1,0,0]
	v_pk_mul_f32 v[104:105], v[4:5], v[2:3] op_sel_hi:[1,0]
	v_pk_fma_f32 v[4:5], v[4:5], v[2:3], v[104:105] op_sel:[1,1,0] op_sel_hi:[0,1,1] neg_lo:[1,0,0]
	v_pk_mul_f32 v[104:105], v[106:107], v[4:5] op_sel_hi:[1,0]
	v_pk_fma_f32 v[114:115], v[106:107], v[4:5], v[104:105] op_sel:[1,1,0] op_sel_hi:[0,1,1] neg_lo:[1,0,0]
	v_pk_mul_f32 v[104:105], v[4:5], v[2:3] op_sel_hi:[1,0]
	v_pk_fma_f32 v[4:5], v[4:5], v[2:3], v[104:105] op_sel:[1,1,0] op_sel_hi:[0,1,1] neg_lo:[1,0,0]
	ds_read2_b64 v[104:107], v134 offset0:176 offset1:248
	s_waitcnt lgkmcnt(0)
	v_pk_mul_f32 v[108:109], v[104:105], v[4:5] op_sel_hi:[1,0]
	v_pk_fma_f32 v[104:105], v[104:105], v[4:5], v[108:109] op_sel:[1,1,0] op_sel_hi:[0,1,1] neg_lo:[1,0,0]
	v_pk_mul_f32 v[108:109], v[4:5], v[2:3] op_sel_hi:[1,0]
	v_pk_fma_f32 v[108:109], v[4:5], v[2:3], v[108:109] op_sel:[1,1,0] op_sel_hi:[0,1,1] neg_lo:[1,0,0]
	v_pk_mul_f32 v[4:5], v[106:107], v[108:109] op_sel_hi:[1,0]
	v_pk_fma_f32 v[4:5], v[106:107], v[108:109], v[4:5] op_sel:[1,1,0] op_sel_hi:[0,1,1] neg_lo:[1,0,0]
	v_pk_mul_f32 v[106:107], v[108:109], v[2:3] op_sel_hi:[1,0]
	v_pk_fma_f32 v[110:111], v[108:109], v[2:3], v[106:107] op_sel:[1,1,0] op_sel_hi:[0,1,1] neg_lo:[1,0,0]
	ds_read2_b64 v[106:109], v135 offset0:64 offset1:136
	s_waitcnt lgkmcnt(0)
	v_pk_mul_f32 v[116:117], v[106:107], v[110:111] op_sel_hi:[1,0]
	v_pk_fma_f32 v[140:141], v[106:107], v[110:111], v[116:117] op_sel:[1,1,0] op_sel_hi:[0,1,1] neg_lo:[1,0,0]
	v_pk_mul_f32 v[106:107], v[110:111], v[2:3] op_sel_hi:[1,0]
	v_pk_fma_f32 v[106:107], v[110:111], v[2:3], v[106:107] op_sel:[1,1,0] op_sel_hi:[0,1,1] neg_lo:[1,0,0]
	v_pk_mul_f32 v[110:111], v[108:109], v[106:107] op_sel_hi:[1,0]
	v_pk_fma_f32 v[142:143], v[108:109], v[106:107], v[110:111] op_sel:[1,1,0] op_sel_hi:[0,1,1] neg_lo:[1,0,0]
	v_pk_mul_f32 v[108:109], v[106:107], v[2:3] op_sel_hi:[1,0]
	v_pk_fma_f32 v[110:111], v[106:107], v[2:3], v[108:109] op_sel:[1,1,0] op_sel_hi:[0,1,1] neg_lo:[1,0,0]
	ds_read2_b64 v[106:109], v136 offset0:80 offset1:152
	s_waitcnt lgkmcnt(0)
	v_pk_mul_f32 v[116:117], v[106:107], v[110:111] op_sel_hi:[1,0]
	v_pk_fma_f32 v[128:129], v[106:107], v[110:111], v[116:117] op_sel:[1,1,0] op_sel_hi:[0,1,1] neg_lo:[1,0,0]
	v_pk_mul_f32 v[106:107], v[110:111], v[2:3] op_sel_hi:[1,0]
	v_pk_fma_f32 v[106:107], v[110:111], v[2:3], v[106:107] op_sel:[1,1,0] op_sel_hi:[0,1,1] neg_lo:[1,0,0]
	v_pk_mul_f32 v[110:111], v[108:109], v[106:107] op_sel_hi:[1,0]
	v_pk_fma_f32 v[126:127], v[108:109], v[106:107], v[110:111] op_sel:[1,1,0] op_sel_hi:[0,1,1] neg_lo:[1,0,0]
	v_pk_mul_f32 v[108:109], v[106:107], v[2:3] op_sel_hi:[1,0]
	v_pk_fma_f32 v[110:111], v[106:107], v[2:3], v[108:109] op_sel:[1,1,0] op_sel_hi:[0,1,1] neg_lo:[1,0,0]
	ds_read2_b64 v[106:109], v137 offset0:96 offset1:168
	s_waitcnt lgkmcnt(0)
	v_pk_mul_f32 v[116:117], v[106:107], v[110:111] op_sel_hi:[1,0]
	v_pk_fma_f32 v[122:123], v[106:107], v[110:111], v[116:117] op_sel:[1,1,0] op_sel_hi:[0,1,1] neg_lo:[1,0,0]
	v_pk_mul_f32 v[106:107], v[110:111], v[2:3] op_sel_hi:[1,0]
	v_pk_fma_f32 v[106:107], v[110:111], v[2:3], v[106:107] op_sel:[1,1,0] op_sel_hi:[0,1,1] neg_lo:[1,0,0]
	v_pk_mul_f32 v[110:111], v[108:109], v[106:107] op_sel_hi:[1,0]
	v_pk_fma_f32 v[124:125], v[108:109], v[106:107], v[110:111] op_sel:[1,1,0] op_sel_hi:[0,1,1] neg_lo:[1,0,0]
	v_pk_mul_f32 v[108:109], v[106:107], v[2:3] op_sel_hi:[1,0]
	v_pk_fma_f32 v[110:111], v[106:107], v[2:3], v[108:109] op_sel:[1,1,0] op_sel_hi:[0,1,1] neg_lo:[1,0,0]
	ds_read2_b64 v[106:109], v138 offset0:112 offset1:184
	s_waitcnt lgkmcnt(0)
	v_pk_mul_f32 v[116:117], v[106:107], v[110:111] op_sel_hi:[1,0]
	v_pk_fma_f32 v[116:117], v[106:107], v[110:111], v[116:117] op_sel:[1,1,0] op_sel_hi:[0,1,1] neg_lo:[1,0,0]
	v_pk_mul_f32 v[106:107], v[110:111], v[2:3] op_sel_hi:[1,0]
	v_pk_fma_f32 v[106:107], v[110:111], v[2:3], v[106:107] op_sel:[1,1,0] op_sel_hi:[0,1,1] neg_lo:[1,0,0]
	v_pk_mul_f32 v[110:111], v[108:109], v[106:107] op_sel_hi:[1,0]
	v_pk_fma_f32 v[110:111], v[108:109], v[106:107], v[110:111] op_sel:[1,1,0] op_sel_hi:[0,1,1] neg_lo:[1,0,0]
	v_pk_add_f32 v[106:107], v[102:103], v[140:141]
	v_pk_add_f32 v[102:103], v[102:103], v[140:141] neg_lo:[0,1] neg_hi:[0,1]
	v_pk_add_f32 v[108:109], v[130:131], v[142:143]
	v_pk_add_f32 v[130:131], v[130:131], v[142:143] neg_lo:[0,1] neg_hi:[0,1]
	v_mov_b64_e32 v[140:141], s[4:5]
	v_pk_mul_f32 v[142:143], v[130:131], v[140:141] op_sel_hi:[1,0]
	v_pk_fma_f32 v[130:131], v[130:131], v[140:141], v[142:143] op_sel:[1,1,0] op_sel_hi:[0,1,1] neg_lo:[1,0,0]
	v_pk_add_f32 v[140:141], v[120:121], v[128:129]
	v_pk_add_f32 v[120:121], v[120:121], v[128:129] neg_lo:[0,1] neg_hi:[0,1]
	v_mov_b64_e32 v[128:129], s[6:7]
	v_pk_mul_f32 v[142:143], v[120:121], v[128:129] op_sel_hi:[1,0]
	v_pk_fma_f32 v[120:121], v[120:121], v[128:129], v[142:143] op_sel:[1,1,0] op_sel_hi:[0,1,1] neg_lo:[1,0,0]
	v_pk_add_f32 v[142:143], v[118:119], v[126:127]
	v_pk_add_f32 v[118:119], v[118:119], v[126:127] neg_lo:[0,1] neg_hi:[0,1]
	v_mov_b64_e32 v[126:127], s[10:11]
	v_pk_mul_f32 v[144:145], v[118:119], v[126:127] op_sel_hi:[1,0]
	v_pk_fma_f32 v[118:119], v[118:119], v[126:127], v[144:145] op_sel:[1,1,0] op_sel_hi:[0,1,1] neg_lo:[1,0,0]
	v_pk_add_f32 v[126:127], v[112:113], v[122:123]
	v_pk_add_f32 v[112:113], v[112:113], v[122:123] op_sel:[1,1] op_sel_hi:[0,0] neg_lo:[1,0] neg_hi:[0,1]
	v_pk_add_f32 v[122:123], v[114:115], v[124:125]
	v_pk_add_f32 v[114:115], v[114:115], v[124:125] neg_lo:[0,1] neg_hi:[0,1]
	v_mov_b64_e32 v[124:125], s[12:13]
	v_pk_mul_f32 v[144:145], v[114:115], v[124:125] op_sel_hi:[1,0]
	v_pk_fma_f32 v[114:115], v[114:115], v[124:125], v[144:145] op_sel:[1,1,0] op_sel_hi:[0,1,1] neg_lo:[1,0,0]
	v_pk_add_f32 v[124:125], v[104:105], v[116:117]
	v_pk_add_f32 v[104:105], v[104:105], v[116:117] neg_lo:[0,1] neg_hi:[0,1]
	v_mov_b64_e32 v[116:117], s[14:15]
	v_pk_mul_f32 v[144:145], v[104:105], v[116:117] op_sel_hi:[1,0]
	v_pk_fma_f32 v[104:105], v[104:105], v[116:117], v[144:145] op_sel:[1,1,0] op_sel_hi:[0,1,1] neg_lo:[1,0,0]
	v_pk_add_f32 v[144:145], v[4:5], v[110:111]
	v_pk_add_f32 v[4:5], v[4:5], v[110:111] neg_lo:[0,1] neg_hi:[0,1]
	v_mov_b64_e32 v[110:111], s[16:17]
	v_pk_mul_f32 v[146:147], v[4:5], v[110:111] op_sel_hi:[1,0]
	v_pk_fma_f32 v[4:5], v[4:5], v[110:111], v[146:147] op_sel:[1,1,0] op_sel_hi:[0,1,1] neg_lo:[1,0,0]
	v_pk_add_f32 v[110:111], v[106:107], v[126:127]
	v_pk_add_f32 v[106:107], v[106:107], v[126:127] neg_lo:[0,1] neg_hi:[0,1]
	v_pk_add_f32 v[126:127], v[108:109], v[122:123]
	v_pk_add_f32 v[108:109], v[108:109], v[122:123] neg_lo:[0,1] neg_hi:[0,1]
	s_nop 0
	v_pk_mul_f32 v[122:123], v[108:109], v[128:129] op_sel_hi:[1,0]
	v_pk_fma_f32 v[108:109], v[108:109], v[128:129], v[122:123] op_sel:[1,1,0] op_sel_hi:[0,1,1] neg_lo:[1,0,0]
	v_pk_add_f32 v[122:123], v[140:141], v[124:125]
	v_pk_add_f32 v[124:125], v[140:141], v[124:125] op_sel:[1,1] op_sel_hi:[0,0] neg_lo:[1,0] neg_hi:[0,1]
	v_pk_add_f32 v[140:141], v[142:143], v[144:145]
	v_pk_add_f32 v[142:143], v[142:143], v[144:145] neg_lo:[0,1] neg_hi:[0,1]
	s_nop 0
	v_pk_mul_f32 v[144:145], v[142:143], v[116:117] op_sel_hi:[1,0]
	v_pk_fma_f32 v[142:143], v[142:143], v[116:117], v[144:145] op_sel:[1,1,0] op_sel_hi:[0,1,1] neg_lo:[1,0,0]
	v_pk_add_f32 v[144:145], v[102:103], v[112:113]
	v_pk_add_f32 v[102:103], v[102:103], v[112:113] neg_lo:[0,1] neg_hi:[0,1]
	v_pk_add_f32 v[112:113], v[130:131], v[114:115]
	v_pk_add_f32 v[114:115], v[130:131], v[114:115] neg_lo:[0,1] neg_hi:[0,1]
	s_nop 0
	v_pk_mul_f32 v[130:131], v[114:115], v[128:129] op_sel_hi:[1,0]
	v_pk_fma_f32 v[114:115], v[114:115], v[128:129], v[130:131] op_sel:[1,1,0] op_sel_hi:[0,1,1] neg_lo:[1,0,0]
	v_pk_add_f32 v[128:129], v[120:121], v[104:105]
	v_pk_add_f32 v[104:105], v[120:121], v[104:105] op_sel:[1,1] op_sel_hi:[0,0] neg_lo:[1,0] neg_hi:[0,1]
	v_pk_add_f32 v[120:121], v[118:119], v[4:5]
	v_pk_add_f32 v[4:5], v[118:119], v[4:5] neg_lo:[0,1] neg_hi:[0,1]
	v_pk_add_f32 v[130:131], v[144:145], v[128:129]
	v_pk_mul_f32 v[118:119], v[4:5], v[116:117] op_sel_hi:[1,0]
	v_pk_add_f32 v[128:129], v[144:145], v[128:129] neg_lo:[0,1] neg_hi:[0,1]
	v_pk_fma_f32 v[4:5], v[4:5], v[116:117], v[118:119] op_sel:[1,1,0] op_sel_hi:[0,1,1] neg_lo:[1,0,0]
	v_pk_add_f32 v[116:117], v[110:111], v[122:123]
	v_pk_add_f32 v[110:111], v[110:111], v[122:123] neg_lo:[0,1] neg_hi:[0,1]
	v_pk_add_f32 v[118:119], v[126:127], v[140:141]
	v_pk_add_f32 v[122:123], v[126:127], v[140:141] op_sel:[1,1] op_sel_hi:[0,0] neg_lo:[1,0] neg_hi:[0,1]
	v_pk_add_f32 v[126:127], v[106:107], v[124:125]
	v_pk_add_f32 v[106:107], v[106:107], v[124:125] neg_lo:[0,1] neg_hi:[0,1]
	v_pk_add_f32 v[124:125], v[108:109], v[142:143]
	v_pk_add_f32 v[108:109], v[108:109], v[142:143] op_sel:[1,1] op_sel_hi:[0,0] neg_lo:[1,0] neg_hi:[0,1]
	v_pk_add_f32 v[140:141], v[112:113], v[120:121]
	v_pk_add_f32 v[112:113], v[112:113], v[120:121] op_sel:[1,1] op_sel_hi:[0,0] neg_lo:[1,0] neg_hi:[0,1]
	v_pk_add_f32 v[120:121], v[102:103], v[104:105]
	v_pk_add_f32 v[102:103], v[102:103], v[104:105] neg_lo:[0,1] neg_hi:[0,1]
	v_pk_add_f32 v[104:105], v[114:115], v[4:5]
	v_pk_add_f32 v[4:5], v[114:115], v[4:5] op_sel:[1,1] op_sel_hi:[0,0] neg_lo:[1,0] neg_hi:[0,1]
	v_pk_add_f32 v[114:115], v[116:117], v[118:119]
	v_pk_add_f32 v[116:117], v[116:117], v[118:119] neg_lo:[0,1] neg_hi:[0,1]
	v_pk_add_f32 v[118:119], v[110:111], v[122:123]
	v_pk_add_f32 v[110:111], v[110:111], v[122:123] neg_lo:[0,1] neg_hi:[0,1]
	v_pk_add_f32 v[122:123], v[126:127], v[124:125]
	v_pk_add_f32 v[124:125], v[126:127], v[124:125] neg_lo:[0,1] neg_hi:[0,1]
	v_pk_add_f32 v[126:127], v[106:107], v[108:109]
	v_pk_add_f32 v[106:107], v[106:107], v[108:109] neg_lo:[0,1] neg_hi:[0,1]
	v_pk_add_f32 v[108:109], v[130:131], v[140:141]
	v_pk_add_f32 v[130:131], v[130:131], v[140:141] neg_lo:[0,1] neg_hi:[0,1]
	v_pk_add_f32 v[140:141], v[128:129], v[112:113]
	v_pk_add_f32 v[112:113], v[128:129], v[112:113] neg_lo:[0,1] neg_hi:[0,1]
	v_pk_add_f32 v[128:129], v[120:121], v[104:105]
	v_pk_add_f32 v[104:105], v[120:121], v[104:105] neg_lo:[0,1] neg_hi:[0,1]
	v_pk_add_f32 v[120:121], v[102:103], v[4:5]
	v_pk_add_f32 v[4:5], v[102:103], v[4:5] neg_lo:[0,1] neg_hi:[0,1]
	ds_write2_b64 v133, v[114:115], v[108:109] offset1:72
	ds_write2_b64 v133, v[122:123], v[128:129] offset0:144 offset1:216
	ds_write2_b64 v134, v[118:119], v[140:141] offset0:32 offset1:104
	ds_write2_b64 v134, v[126:127], v[120:121] offset0:176 offset1:248
	ds_write2_b64 v135, v[116:117], v[130:131] offset0:64 offset1:136
	ds_write2_b64 v136, v[124:125], v[104:105] offset0:80 offset1:152
	ds_write2_b64 v137, v[110:111], v[112:113] offset0:96 offset1:168
	ds_write2_b64 v138, v[106:107], v[4:5] offset0:112 offset1:184
	s_cbranch_vccnz .LBB0_778
	s_lshl_b32 s85, s83, 2
	s_add_i32 s85, s85, 0
	s_add_i32 s85, s85, 0x24400
	s_waitcnt lgkmcnt(0)
	s_barrier
	v_mov_b32_e32 v2, s85
	v_mov_b32_e32 v118, v204
	ds_read_b32 v38, v2
	s_ashr_i32 s85, s84, 31
	v_cvt_f32_i32_e32 v102, v118
	v_and_b32_e32 v2, -8, v118
	v_lshlrev_b32_e32 v119, 3, v118
	v_add3_u32 v116, 0, v2, v119
	v_mul_f32_e32 v102, 0x38800000, v102
	ds_read2st64_b64 v[2:5], v116 offset1:18
	v_cos_f32_e32 v106, v102
	v_sin_f32_e32 v107, v102
	s_waitcnt lgkmcnt(0)
	v_pk_mul_f32 v[102:103], v[4:5], v[106:107] op_sel_hi:[1,0]
	v_add_u32_e32 v122, 0x12000, v116
	v_pk_fma_f32 v[4:5], v[4:5], v[106:107], v[102:103] op_sel:[1,1,0] op_sel_hi:[0,1,1] neg_lo:[1,0,0]
	v_pk_mul_f32 v[102:103], v[106:107], v[106:107] op_sel_hi:[1,0]
	v_add_u32_e32 v124, 0x14400, v116
	v_pk_fma_f32 v[108:109], v[106:107], v[106:107], v[102:103] op_sel:[1,1,0] op_sel_hi:[0,1,1] neg_lo:[1,0,0]
	ds_read2st64_b64 v[102:105], v116 offset0:36 offset1:54
	s_waitcnt lgkmcnt(0)
	v_pk_mul_f32 v[110:111], v[102:103], v[108:109] op_sel_hi:[1,0]
	v_add_u32_e32 v126, 0x16800, v116
	v_pk_fma_f32 v[102:103], v[102:103], v[108:109], v[110:111] op_sel:[1,1,0] op_sel_hi:[0,1,1] neg_lo:[1,0,0]
	v_pk_mul_f32 v[110:111], v[108:109], v[106:107] op_sel_hi:[1,0]
	v_add_u32_e32 v128, 0x18c00, v116
	v_pk_fma_f32 v[108:109], v[108:109], v[106:107], v[110:111] op_sel:[1,1,0] op_sel_hi:[0,1,1] neg_lo:[1,0,0]
	v_add_u32_e32 v130, 0x1b000, v116
	v_pk_mul_f32 v[110:111], v[104:105], v[108:109] op_sel_hi:[1,0]
	v_add_u32_e32 v132, 0x1d400, v116
	v_pk_fma_f32 v[104:105], v[104:105], v[108:109], v[110:111] op_sel:[1,1,0] op_sel_hi:[0,1,1] neg_lo:[1,0,0]
	v_pk_mul_f32 v[110:111], v[108:109], v[106:107] op_sel_hi:[1,0]
	v_add_u32_e32 v134, 0x1f800, v116
	v_pk_fma_f32 v[108:109], v[108:109], v[106:107], v[110:111] op_sel:[1,1,0] op_sel_hi:[0,1,1] neg_lo:[1,0,0]
	ds_read2st64_b64 v[110:113], v116 offset0:72 offset1:90
	s_waitcnt lgkmcnt(0)
	v_pk_mul_f32 v[114:115], v[110:111], v[108:109] op_sel_hi:[1,0]
	v_add_u32_e32 v136, 0x21c00, v116
	v_pk_fma_f32 v[110:111], v[110:111], v[108:109], v[114:115] op_sel:[1,1,0] op_sel_hi:[0,1,1] neg_lo:[1,0,0]
	v_pk_mul_f32 v[114:115], v[108:109], v[106:107] op_sel_hi:[1,0]
	s_lshl_b64 s[84:85], s[84:85], 16
	v_pk_fma_f32 v[108:109], v[108:109], v[106:107], v[114:115] op_sel:[1,1,0] op_sel_hi:[0,1,1] neg_lo:[1,0,0]
	s_add_u32 s84, s88, s84
	v_pk_mul_f32 v[114:115], v[112:113], v[108:109] op_sel_hi:[1,0]
	s_addc_u32 s85, s89, s85
	v_pk_fma_f32 v[112:113], v[112:113], v[108:109], v[114:115] op_sel:[1,1,0] op_sel_hi:[0,1,1] neg_lo:[1,0,0]
	v_pk_mul_f32 v[114:115], v[108:109], v[106:107] op_sel_hi:[1,0]
	s_add_i32 s83, s83, 1
	v_pk_fma_f32 v[108:109], v[108:109], v[106:107], v[114:115] op_sel:[1,1,0] op_sel_hi:[0,1,1] neg_lo:[1,0,0]
	ds_read2st64_b64 v[114:117], v116 offset0:108 offset1:126
	s_waitcnt lgkmcnt(0)
	v_pk_mul_f32 v[120:121], v[114:115], v[108:109] op_sel_hi:[1,0]
	s_cmp_lg_u32 s83, 4
	v_pk_fma_f32 v[114:115], v[114:115], v[108:109], v[120:121] op_sel:[1,1,0] op_sel_hi:[0,1,1] neg_lo:[1,0,0]
	v_pk_mul_f32 v[120:121], v[108:109], v[106:107] op_sel_hi:[1,0]
	v_pk_fma_f32 v[108:109], v[108:109], v[106:107], v[120:121] op_sel:[1,1,0] op_sel_hi:[0,1,1] neg_lo:[1,0,0]
	v_pk_mul_f32 v[120:121], v[116:117], v[108:109] op_sel_hi:[1,0]
	v_pk_fma_f32 v[116:117], v[116:117], v[108:109], v[120:121] op_sel:[1,1,0] op_sel_hi:[0,1,1] neg_lo:[1,0,0]
	v_pk_mul_f32 v[120:121], v[108:109], v[106:107] op_sel_hi:[1,0]
	v_pk_fma_f32 v[120:121], v[108:109], v[106:107], v[120:121] op_sel:[1,1,0] op_sel_hi:[0,1,1] neg_lo:[1,0,0]
	ds_read_b64 v[108:109], v122
	s_waitcnt lgkmcnt(0)
	v_pk_mul_f32 v[122:123], v[108:109], v[120:121] op_sel_hi:[1,0]
	v_pk_fma_f32 v[108:109], v[108:109], v[120:121], v[122:123] op_sel:[1,1,0] op_sel_hi:[0,1,1] neg_lo:[1,0,0]
	v_pk_mul_f32 v[122:123], v[120:121], v[106:107] op_sel_hi:[1,0]
	v_pk_fma_f32 v[120:121], v[120:121], v[106:107], v[122:123] op_sel:[1,1,0] op_sel_hi:[0,1,1] neg_lo:[1,0,0]
	ds_read_b64 v[122:123], v124
	s_waitcnt lgkmcnt(0)
	v_pk_mul_f32 v[124:125], v[122:123], v[120:121] op_sel_hi:[1,0]
	v_pk_fma_f32 v[122:123], v[122:123], v[120:121], v[124:125] op_sel:[1,1,0] op_sel_hi:[0,1,1] neg_lo:[1,0,0]
	v_pk_mul_f32 v[124:125], v[120:121], v[106:107] op_sel_hi:[1,0]
	v_pk_fma_f32 v[120:121], v[120:121], v[106:107], v[124:125] op_sel:[1,1,0] op_sel_hi:[0,1,1] neg_lo:[1,0,0]
	ds_read_b64 v[124:125], v126
	s_waitcnt lgkmcnt(0)
	v_pk_mul_f32 v[126:127], v[124:125], v[120:121] op_sel_hi:[1,0]
	v_pk_fma_f32 v[124:125], v[124:125], v[120:121], v[126:127] op_sel:[1,1,0] op_sel_hi:[0,1,1] neg_lo:[1,0,0]
	v_pk_mul_f32 v[126:127], v[120:121], v[106:107] op_sel_hi:[1,0]
	v_pk_fma_f32 v[120:121], v[120:121], v[106:107], v[126:127] op_sel:[1,1,0] op_sel_hi:[0,1,1] neg_lo:[1,0,0]
	ds_read_b64 v[126:127], v128
	s_waitcnt lgkmcnt(0)
	v_pk_mul_f32 v[128:129], v[126:127], v[120:121] op_sel_hi:[1,0]
	v_pk_fma_f32 v[126:127], v[126:127], v[120:121], v[128:129] op_sel:[1,1,0] op_sel_hi:[0,1,1] neg_lo:[1,0,0]
	v_pk_mul_f32 v[128:129], v[120:121], v[106:107] op_sel_hi:[1,0]
	v_pk_fma_f32 v[120:121], v[120:121], v[106:107], v[128:129] op_sel:[1,1,0] op_sel_hi:[0,1,1] neg_lo:[1,0,0]
	ds_read_b64 v[128:129], v130
	s_waitcnt lgkmcnt(0)
	v_pk_mul_f32 v[130:131], v[128:129], v[120:121] op_sel_hi:[1,0]
	v_pk_add_f32 v[138:139], v[104:105], v[126:127]
	v_pk_fma_f32 v[128:129], v[128:129], v[120:121], v[130:131] op_sel:[1,1,0] op_sel_hi:[0,1,1] neg_lo:[1,0,0]
	v_pk_mul_f32 v[130:131], v[120:121], v[106:107] op_sel_hi:[1,0]
	v_pk_add_f32 v[104:105], v[104:105], v[126:127] neg_lo:[0,1] neg_hi:[0,1]
	v_pk_fma_f32 v[120:121], v[120:121], v[106:107], v[130:131] op_sel:[1,1,0] op_sel_hi:[0,1,1] neg_lo:[1,0,0]
	ds_read_b64 v[130:131], v132
	s_waitcnt lgkmcnt(0)
	v_pk_mul_f32 v[132:133], v[130:131], v[120:121] op_sel_hi:[1,0]
	v_pk_add_f32 v[140:141], v[110:111], v[128:129]
	v_pk_fma_f32 v[130:131], v[130:131], v[120:121], v[132:133] op_sel:[1,1,0] op_sel_hi:[0,1,1] neg_lo:[1,0,0]
	v_pk_mul_f32 v[132:133], v[120:121], v[106:107] op_sel_hi:[1,0]
	v_pk_add_f32 v[128:129], v[110:111], v[128:129] op_sel:[1,1] op_sel_hi:[0,0] neg_lo:[1,0] neg_hi:[0,1]
	v_mov_b64_e32 v[110:111], s[12:13]
	v_pk_fma_f32 v[120:121], v[120:121], v[106:107], v[132:133] op_sel:[1,1,0] op_sel_hi:[0,1,1] neg_lo:[1,0,0]
	ds_read_b64 v[132:133], v134
	s_waitcnt lgkmcnt(0)
	v_pk_mul_f32 v[134:135], v[132:133], v[120:121] op_sel_hi:[1,0]
	v_pk_add_f32 v[142:143], v[112:113], v[130:131]
	v_pk_fma_f32 v[132:133], v[132:133], v[120:121], v[134:135] op_sel:[1,1,0] op_sel_hi:[0,1,1] neg_lo:[1,0,0]
	v_pk_mul_f32 v[134:135], v[120:121], v[106:107] op_sel_hi:[1,0]
	v_pk_fma_f32 v[106:107], v[120:121], v[106:107], v[134:135] op_sel:[1,1,0] op_sel_hi:[0,1,1] neg_lo:[1,0,0]
	ds_read_b64 v[120:121], v136
	s_waitcnt lgkmcnt(0)
	v_pk_mul_f32 v[134:135], v[120:121], v[106:107] op_sel_hi:[1,0]
	v_pk_add_f32 v[136:137], v[4:5], v[122:123]
	v_pk_fma_f32 v[120:121], v[120:121], v[106:107], v[134:135] op_sel:[1,1,0] op_sel_hi:[0,1,1] neg_lo:[1,0,0]
	v_pk_add_f32 v[134:135], v[2:3], v[108:109]
	v_pk_add_f32 v[2:3], v[2:3], v[108:109] neg_lo:[0,1] neg_hi:[0,1]
	v_pk_add_f32 v[4:5], v[4:5], v[122:123] neg_lo:[0,1] neg_hi:[0,1]
	v_mov_b64_e32 v[106:107], s[4:5]
	v_pk_mul_f32 v[108:109], v[4:5], v[106:107] op_sel_hi:[1,0]
	v_pk_add_f32 v[122:123], v[102:103], v[124:125]
	v_pk_fma_f32 v[4:5], v[4:5], v[106:107], v[108:109] op_sel:[1,1,0] op_sel_hi:[0,1,1] neg_lo:[1,0,0]
	v_pk_add_f32 v[108:109], v[102:103], v[124:125] neg_lo:[0,1] neg_hi:[0,1]
	v_mov_b64_e32 v[102:103], s[6:7]
	v_pk_mul_f32 v[124:125], v[108:109], v[102:103] op_sel_hi:[1,0]
	v_pk_add_f32 v[144:145], v[114:115], v[132:133]
	v_pk_fma_f32 v[124:125], v[108:109], v[102:103], v[124:125] op_sel:[1,1,0] op_sel_hi:[0,1,1] neg_lo:[1,0,0]
	v_mov_b64_e32 v[108:109], s[10:11]
	v_pk_mul_f32 v[126:127], v[104:105], v[108:109] op_sel_hi:[1,0]
	v_pk_fma_f32 v[126:127], v[104:105], v[108:109], v[126:127] op_sel:[1,1,0] op_sel_hi:[0,1,1] neg_lo:[1,0,0]
	v_pk_add_f32 v[104:105], v[112:113], v[130:131] neg_lo:[0,1] neg_hi:[0,1]
	s_nop 0
	v_pk_mul_f32 v[112:113], v[104:105], v[110:111] op_sel_hi:[1,0]
	v_pk_fma_f32 v[130:131], v[104:105], v[110:111], v[112:113] op_sel:[1,1,0] op_sel_hi:[0,1,1] neg_lo:[1,0,0]
	v_pk_add_f32 v[112:113], v[114:115], v[132:133] neg_lo:[0,1] neg_hi:[0,1]
	v_mov_b64_e32 v[104:105], s[14:15]
	v_pk_mul_f32 v[114:115], v[112:113], v[104:105] op_sel_hi:[1,0]
	v_pk_add_f32 v[132:133], v[116:117], v[120:121]
	v_pk_fma_f32 v[114:115], v[112:113], v[104:105], v[114:115] op_sel:[1,1,0] op_sel_hi:[0,1,1] neg_lo:[1,0,0]
	v_pk_add_f32 v[116:117], v[116:117], v[120:121] neg_lo:[0,1] neg_hi:[0,1]
	v_mov_b64_e32 v[112:113], s[16:17]
	v_pk_mul_f32 v[120:121], v[116:117], v[112:113] op_sel_hi:[1,0]
	v_pk_fma_f32 v[116:117], v[116:117], v[112:113], v[120:121] op_sel:[1,1,0] op_sel_hi:[0,1,1] neg_lo:[1,0,0]
	v_pk_add_f32 v[120:121], v[134:135], v[140:141]
	v_pk_add_f32 v[134:135], v[134:135], v[140:141] neg_lo:[0,1] neg_hi:[0,1]
	v_pk_add_f32 v[140:141], v[136:137], v[142:143]
	v_pk_add_f32 v[136:137], v[136:137], v[142:143] neg_lo:[0,1] neg_hi:[0,1]
	s_nop 0
	v_pk_mul_f32 v[142:143], v[136:137], v[102:103] op_sel_hi:[1,0]
	v_pk_fma_f32 v[136:137], v[136:137], v[102:103], v[142:143] op_sel:[1,1,0] op_sel_hi:[0,1,1] neg_lo:[1,0,0]
	v_pk_add_f32 v[142:143], v[122:123], v[144:145]
	v_pk_add_f32 v[122:123], v[122:123], v[144:145] op_sel:[1,1] op_sel_hi:[0,0] neg_lo:[1,0] neg_hi:[0,1]
	v_pk_add_f32 v[144:145], v[138:139], v[132:133]
	v_pk_add_f32 v[132:133], v[138:139], v[132:133] neg_lo:[0,1] neg_hi:[0,1]
	s_nop 0
	v_pk_mul_f32 v[138:139], v[132:133], v[104:105] op_sel_hi:[1,0]
	v_pk_fma_f32 v[132:133], v[132:133], v[104:105], v[138:139] op_sel:[1,1,0] op_sel_hi:[0,1,1] neg_lo:[1,0,0]
	v_pk_add_f32 v[138:139], v[2:3], v[128:129]
	v_pk_add_f32 v[2:3], v[2:3], v[128:129] neg_lo:[0,1] neg_hi:[0,1]
	v_pk_add_f32 v[128:129], v[4:5], v[130:131]
	v_pk_add_f32 v[4:5], v[4:5], v[130:131] neg_lo:[0,1] neg_hi:[0,1]
	s_nop 0
	v_pk_mul_f32 v[130:131], v[4:5], v[102:103] op_sel_hi:[1,0]
	v_pk_fma_f32 v[4:5], v[4:5], v[102:103], v[130:131] op_sel:[1,1,0] op_sel_hi:[0,1,1] neg_lo:[1,0,0]
	v_pk_add_f32 v[130:131], v[124:125], v[114:115]
	v_pk_add_f32 v[114:115], v[124:125], v[114:115] op_sel:[1,1] op_sel_hi:[0,0] neg_lo:[1,0] neg_hi:[0,1]
	v_pk_add_f32 v[124:125], v[126:127], v[116:117]
	v_pk_add_f32 v[116:117], v[126:127], v[116:117] neg_lo:[0,1] neg_hi:[0,1]
	s_nop 0
	v_pk_mul_f32 v[126:127], v[116:117], v[104:105] op_sel_hi:[1,0]
	v_pk_fma_f32 v[116:117], v[116:117], v[104:105], v[126:127] op_sel:[1,1,0] op_sel_hi:[0,1,1] neg_lo:[1,0,0]
	v_pk_add_f32 v[126:127], v[120:121], v[142:143]
	v_pk_add_f32 v[120:121], v[120:121], v[142:143] neg_lo:[0,1] neg_hi:[0,1]
	v_pk_add_f32 v[142:143], v[140:141], v[144:145]
	v_pk_add_f32 v[140:141], v[140:141], v[144:145] op_sel:[1,1] op_sel_hi:[0,0] neg_lo:[1,0] neg_hi:[0,1]
	v_pk_add_f32 v[144:145], v[134:135], v[122:123]
	v_pk_add_f32 v[122:123], v[134:135], v[122:123] neg_lo:[0,1] neg_hi:[0,1]
	v_pk_add_f32 v[134:135], v[136:137], v[132:133]
	v_pk_add_f32 v[132:133], v[136:137], v[132:133] op_sel:[1,1] op_sel_hi:[0,0] neg_lo:[1,0] neg_hi:[0,1]
	v_pk_add_f32 v[136:137], v[138:139], v[130:131]
	v_pk_add_f32 v[130:131], v[138:139], v[130:131] neg_lo:[0,1] neg_hi:[0,1]
	v_pk_add_f32 v[138:139], v[128:129], v[124:125]
	v_pk_add_f32 v[124:125], v[128:129], v[124:125] op_sel:[1,1] op_sel_hi:[0,0] neg_lo:[1,0] neg_hi:[0,1]
	v_pk_add_f32 v[128:129], v[2:3], v[114:115]
	v_pk_add_f32 v[2:3], v[2:3], v[114:115] neg_lo:[0,1] neg_hi:[0,1]
	v_pk_add_f32 v[114:115], v[4:5], v[116:117]
	v_pk_add_f32 v[4:5], v[4:5], v[116:117] op_sel:[1,1] op_sel_hi:[0,0] neg_lo:[1,0] neg_hi:[0,1]
	v_pk_add_f32 v[116:117], v[126:127], v[142:143]
	v_pk_add_f32 v[2:3], v[2:3], v[4:5]
	s_waitcnt vmcnt(47)
	v_pk_mul_f32 v[4:5], v[38:39], v[116:117] op_sel_hi:[0,1]
	v_lshlrev_b32_e32 v116, 1, v118
	v_ashrrev_i32_e32 v117, 31, v116
	v_pk_add_f32 v[114:115], v[128:129], v[114:115]
	v_lshl_add_u64 v[128:129], v[116:117], 2, s[84:85]
	global_store_dwordx2 v[128:129], v[4:5], off
	v_add_u32_e32 v128, 0x800, v116
	v_pk_add_f32 v[122:123], v[122:123], v[132:133]
	v_pk_add_f32 v[132:133], v[136:137], v[138:139]
	v_ashrrev_i32_e32 v129, 31, v128
	v_pk_add_f32 v[126:127], v[144:145], v[134:135]
	v_pk_mul_f32 v[4:5], v[38:39], v[132:133] op_sel_hi:[0,1]
	v_lshl_add_u64 v[128:129], v[128:129], 2, s[84:85]
	global_store_dwordx2 v[128:129], v[4:5], off
	v_pk_mul_f32 v[4:5], v[38:39], v[126:127] op_sel_hi:[0,1]
	v_add_u32_e32 v126, 0x1000, v116
	v_ashrrev_i32_e32 v127, 31, v126
	v_lshl_add_u64 v[126:127], v[126:127], 2, s[84:85]
	global_store_dwordx2 v[126:127], v[4:5], off
	v_pk_mul_f32 v[4:5], v[38:39], v[114:115] op_sel_hi:[0,1]
	v_add_u32_e32 v114, 0x1800, v116
	v_ashrrev_i32_e32 v115, 31, v114
	v_lshl_add_u64 v[114:115], v[114:115], 2, s[84:85]
	global_store_dwordx2 v[114:115], v[4:5], off
	v_add_u32_e32 v114, 0x2000, v116
	v_pk_add_f32 v[120:121], v[120:121], v[140:141]
	v_ashrrev_i32_e32 v115, 31, v114
	v_pk_mul_f32 v[4:5], v[38:39], v[120:121] op_sel_hi:[0,1]
	v_lshl_add_u64 v[114:115], v[114:115], 2, s[84:85]
	global_store_dwordx2 v[114:115], v[4:5], off
	v_add_u32_e32 v114, 0x2800, v116
	v_pk_add_f32 v[124:125], v[130:131], v[124:125]
	v_ashrrev_i32_e32 v115, 31, v114
	v_pk_mul_f32 v[4:5], v[38:39], v[124:125] op_sel_hi:[0,1]
	v_lshl_add_u64 v[114:115], v[114:115], 2, s[84:85]
	global_store_dwordx2 v[114:115], v[4:5], off
	v_add_u32_e32 v114, 0x3000, v116
	v_ashrrev_i32_e32 v115, 31, v114
	v_pk_mul_f32 v[4:5], v[38:39], v[122:123] op_sel_hi:[0,1]
	v_lshl_add_u64 v[114:115], v[114:115], 2, s[84:85]
	v_add_u32_e32 v130, 0x200, v118
	global_store_dwordx2 v[114:115], v[4:5], off
	v_add_u32_e32 v4, 0x3800, v116
	v_cvt_f32_i32_e32 v114, v130
	v_ashrrev_i32_e32 v5, 31, v4
	v_pk_mul_f32 v[2:3], v[38:39], v[2:3] op_sel_hi:[0,1]
	v_lshl_add_u64 v[4:5], v[4:5], 2, s[84:85]
	global_store_dwordx2 v[4:5], v[2:3], off
	v_and_b32_e32 v2, -8, v130
	v_add3_u32 v128, 0, v2, v119
	v_mul_f32_e32 v114, 0x38800000, v114
	ds_read2st64_b64 v[2:5], v128 offset0:8 offset1:26
	v_cos_f32_e32 v118, v114
	v_sin_f32_e32 v119, v114
	s_waitcnt lgkmcnt(0)
	v_pk_mul_f32 v[114:115], v[4:5], v[118:119] op_sel_hi:[1,0]
	ds_read2st64_b64 v[120:123], v128 offset0:44 offset1:62
	v_pk_fma_f32 v[4:5], v[4:5], v[118:119], v[114:115] op_sel:[1,1,0] op_sel_hi:[0,1,1] neg_lo:[1,0,0]
	v_pk_mul_f32 v[114:115], v[118:119], v[118:119] op_sel_hi:[1,0]
	v_add_u32_e32 v131, 0x1000, v128
	v_pk_fma_f32 v[114:115], v[118:119], v[118:119], v[114:115] op_sel:[1,1,0] op_sel_hi:[0,1,1] neg_lo:[1,0,0]
	v_add_u32_e32 v134, 0x13000, v128
	s_waitcnt lgkmcnt(0)
	v_pk_mul_f32 v[116:117], v[120:121], v[114:115] op_sel_hi:[1,0]
	v_add_u32_e32 v136, 0x15400, v128
	v_pk_fma_f32 v[116:117], v[120:121], v[114:115], v[116:117] op_sel:[1,1,0] op_sel_hi:[0,1,1] neg_lo:[1,0,0]
	v_pk_mul_f32 v[120:121], v[114:115], v[118:119] op_sel_hi:[1,0]
	v_add_u32_e32 v138, 0x17800, v128
	v_pk_fma_f32 v[120:121], v[114:115], v[118:119], v[120:121] op_sel:[1,1,0] op_sel_hi:[0,1,1] neg_lo:[1,0,0]
	v_add_u32_e32 v140, 0x19c00, v128
	v_pk_mul_f32 v[114:115], v[122:123], v[120:121] op_sel_hi:[1,0]
	v_add_u32_e32 v142, 0x1c000, v128
	v_pk_fma_f32 v[114:115], v[122:123], v[120:121], v[114:115] op_sel:[1,1,0] op_sel_hi:[0,1,1] neg_lo:[1,0,0]
	v_pk_mul_f32 v[122:123], v[120:121], v[118:119] op_sel_hi:[1,0]
	v_add_u32_e32 v144, 0x1e400, v128
	v_pk_fma_f32 v[124:125], v[120:121], v[118:119], v[122:123] op_sel:[1,1,0] op_sel_hi:[0,1,1] neg_lo:[1,0,0]
	ds_read2st64_b64 v[120:123], v128 offset0:80 offset1:98
	s_waitcnt lgkmcnt(0)
	v_pk_mul_f32 v[126:127], v[120:121], v[124:125] op_sel_hi:[1,0]
	v_add_u32_e32 v146, 0x20800, v128
	v_pk_fma_f32 v[120:121], v[120:121], v[124:125], v[126:127] op_sel:[1,1,0] op_sel_hi:[0,1,1] neg_lo:[1,0,0]
	v_pk_mul_f32 v[126:127], v[124:125], v[118:119] op_sel_hi:[1,0]
	v_add_u32_e32 v148, 0x22c00, v128
	v_pk_fma_f32 v[124:125], v[124:125], v[118:119], v[126:127] op_sel:[1,1,0] op_sel_hi:[0,1,1] neg_lo:[1,0,0]
	v_pk_mul_f32 v[126:127], v[122:123], v[124:125] op_sel_hi:[1,0]
	v_pk_fma_f32 v[122:123], v[122:123], v[124:125], v[126:127] op_sel:[1,1,0] op_sel_hi:[0,1,1] neg_lo:[1,0,0]
	v_pk_mul_f32 v[126:127], v[124:125], v[118:119] op_sel_hi:[1,0]
	v_pk_fma_f32 v[126:127], v[124:125], v[118:119], v[126:127] op_sel:[1,1,0] op_sel_hi:[0,1,1] neg_lo:[1,0,0]
	ds_read_b64 v[124:125], v128 offset:59392
	s_waitcnt lgkmcnt(0)
	v_pk_mul_f32 v[128:129], v[124:125], v[126:127] op_sel_hi:[1,0]
	v_pk_fma_f32 v[124:125], v[124:125], v[126:127], v[128:129] op_sel:[1,1,0] op_sel_hi:[0,1,1] neg_lo:[1,0,0]
	v_pk_mul_f32 v[128:129], v[126:127], v[118:119] op_sel_hi:[1,0]
	v_pk_fma_f32 v[128:129], v[126:127], v[118:119], v[128:129] op_sel:[1,1,0] op_sel_hi:[0,1,1] neg_lo:[1,0,0]
	ds_read_b64 v[126:127], v131 offset:64512
	s_waitcnt lgkmcnt(0)
	v_pk_mul_f32 v[132:133], v[126:127], v[128:129] op_sel_hi:[1,0]
	v_pk_fma_f32 v[126:127], v[126:127], v[128:129], v[132:133] op_sel:[1,1,0] op_sel_hi:[0,1,1] neg_lo:[1,0,0]
	v_pk_mul_f32 v[132:133], v[128:129], v[118:119] op_sel_hi:[1,0]
	v_pk_fma_f32 v[132:133], v[128:129], v[118:119], v[132:133] op_sel:[1,1,0] op_sel_hi:[0,1,1] neg_lo:[1,0,0]
	ds_read_b64 v[128:129], v134
	s_waitcnt lgkmcnt(0)
	v_pk_mul_f32 v[134:135], v[128:129], v[132:133] op_sel_hi:[1,0]
	v_pk_fma_f32 v[128:129], v[128:129], v[132:133], v[134:135] op_sel:[1,1,0] op_sel_hi:[0,1,1] neg_lo:[1,0,0]
	v_pk_mul_f32 v[134:135], v[132:133], v[118:119] op_sel_hi:[1,0]
	v_pk_fma_f32 v[132:133], v[132:133], v[118:119], v[134:135] op_sel:[1,1,0] op_sel_hi:[0,1,1] neg_lo:[1,0,0]
	ds_read_b64 v[134:135], v136
	s_waitcnt lgkmcnt(0)
	v_pk_mul_f32 v[136:137], v[134:135], v[132:133] op_sel_hi:[1,0]
	v_pk_fma_f32 v[134:135], v[134:135], v[132:133], v[136:137] op_sel:[1,1,0] op_sel_hi:[0,1,1] neg_lo:[1,0,0]
	v_pk_mul_f32 v[136:137], v[132:133], v[118:119] op_sel_hi:[1,0]
	v_pk_fma_f32 v[132:133], v[132:133], v[118:119], v[136:137] op_sel:[1,1,0] op_sel_hi:[0,1,1] neg_lo:[1,0,0]
	ds_read_b64 v[136:137], v138
	s_waitcnt lgkmcnt(0)
	v_pk_mul_f32 v[138:139], v[136:137], v[132:133] op_sel_hi:[1,0]
	v_pk_fma_f32 v[136:137], v[136:137], v[132:133], v[138:139] op_sel:[1,1,0] op_sel_hi:[0,1,1] neg_lo:[1,0,0]
	v_pk_mul_f32 v[138:139], v[132:133], v[118:119] op_sel_hi:[1,0]
	v_pk_fma_f32 v[132:133], v[132:133], v[118:119], v[138:139] op_sel:[1,1,0] op_sel_hi:[0,1,1] neg_lo:[1,0,0]
	ds_read_b64 v[138:139], v140
	s_waitcnt lgkmcnt(0)
	v_pk_mul_f32 v[140:141], v[138:139], v[132:133] op_sel_hi:[1,0]
	v_pk_fma_f32 v[138:139], v[138:139], v[132:133], v[140:141] op_sel:[1,1,0] op_sel_hi:[0,1,1] neg_lo:[1,0,0]
	v_pk_mul_f32 v[140:141], v[132:133], v[118:119] op_sel_hi:[1,0]
	v_pk_fma_f32 v[132:133], v[132:133], v[118:119], v[140:141] op_sel:[1,1,0] op_sel_hi:[0,1,1] neg_lo:[1,0,0]
	ds_read_b64 v[140:141], v142
	s_waitcnt lgkmcnt(0)
	v_pk_mul_f32 v[142:143], v[140:141], v[132:133] op_sel_hi:[1,0]
	v_pk_fma_f32 v[140:141], v[140:141], v[132:133], v[142:143] op_sel:[1,1,0] op_sel_hi:[0,1,1] neg_lo:[1,0,0]
	v_pk_mul_f32 v[142:143], v[132:133], v[118:119] op_sel_hi:[1,0]
	v_pk_fma_f32 v[132:133], v[132:133], v[118:119], v[142:143] op_sel:[1,1,0] op_sel_hi:[0,1,1] neg_lo:[1,0,0]
	ds_read_b64 v[142:143], v144
	s_waitcnt lgkmcnt(0)
	v_pk_mul_f32 v[144:145], v[142:143], v[132:133] op_sel_hi:[1,0]
	v_pk_fma_f32 v[142:143], v[142:143], v[132:133], v[144:145] op_sel:[1,1,0] op_sel_hi:[0,1,1] neg_lo:[1,0,0]
	v_pk_mul_f32 v[144:145], v[132:133], v[118:119] op_sel_hi:[1,0]
	v_pk_fma_f32 v[132:133], v[132:133], v[118:119], v[144:145] op_sel:[1,1,0] op_sel_hi:[0,1,1] neg_lo:[1,0,0]
	ds_read_b64 v[144:145], v146
	s_waitcnt lgkmcnt(0)
	v_pk_mul_f32 v[146:147], v[144:145], v[132:133] op_sel_hi:[1,0]
	v_pk_fma_f32 v[144:145], v[144:145], v[132:133], v[146:147] op_sel:[1,1,0] op_sel_hi:[0,1,1] neg_lo:[1,0,0]
	v_pk_mul_f32 v[146:147], v[132:133], v[118:119] op_sel_hi:[1,0]
	v_pk_fma_f32 v[118:119], v[132:133], v[118:119], v[146:147] op_sel:[1,1,0] op_sel_hi:[0,1,1] neg_lo:[1,0,0]
	ds_read_b64 v[132:133], v148
	s_waitcnt lgkmcnt(0)
	v_pk_mul_f32 v[146:147], v[132:133], v[118:119] op_sel_hi:[1,0]
	v_pk_fma_f32 v[118:119], v[132:133], v[118:119], v[146:147] op_sel:[1,1,0] op_sel_hi:[0,1,1] neg_lo:[1,0,0]
	v_pk_add_f32 v[132:133], v[2:3], v[128:129]
	v_pk_add_f32 v[2:3], v[2:3], v[128:129] neg_lo:[0,1] neg_hi:[0,1]
	v_pk_add_f32 v[128:129], v[4:5], v[134:135]
	v_pk_add_f32 v[4:5], v[4:5], v[134:135] neg_lo:[0,1] neg_hi:[0,1]
	s_nop 0
	v_pk_mul_f32 v[134:135], v[4:5], v[106:107] op_sel_hi:[1,0]
	v_pk_fma_f32 v[4:5], v[4:5], v[106:107], v[134:135] op_sel:[1,1,0] op_sel_hi:[0,1,1] neg_lo:[1,0,0]
	v_pk_add_f32 v[106:107], v[116:117], v[136:137]
	v_pk_add_f32 v[116:117], v[116:117], v[136:137] neg_lo:[0,1] neg_hi:[0,1]
	s_nop 0
	v_pk_mul_f32 v[134:135], v[116:117], v[102:103] op_sel_hi:[1,0]
	v_pk_fma_f32 v[116:117], v[116:117], v[102:103], v[134:135] op_sel:[1,1,0] op_sel_hi:[0,1,1] neg_lo:[1,0,0]
	v_pk_add_f32 v[134:135], v[114:115], v[138:139]
	v_pk_add_f32 v[114:115], v[114:115], v[138:139] neg_lo:[0,1] neg_hi:[0,1]
	s_nop 0
	v_pk_mul_f32 v[136:137], v[114:115], v[108:109] op_sel_hi:[1,0]
	v_pk_fma_f32 v[108:109], v[114:115], v[108:109], v[136:137] op_sel:[1,1,0] op_sel_hi:[0,1,1] neg_lo:[1,0,0]
	v_pk_add_f32 v[136:137], v[122:123], v[142:143]
	v_pk_add_f32 v[122:123], v[122:123], v[142:143] neg_lo:[0,1] neg_hi:[0,1]
	v_pk_add_f32 v[114:115], v[120:121], v[140:141]
	v_pk_mul_f32 v[138:139], v[122:123], v[110:111] op_sel_hi:[1,0]
	v_pk_add_f32 v[120:121], v[120:121], v[140:141] op_sel:[1,1] op_sel_hi:[0,0] neg_lo:[1,0] neg_hi:[0,1]
	v_pk_fma_f32 v[110:111], v[122:123], v[110:111], v[138:139] op_sel:[1,1,0] op_sel_hi:[0,1,1] neg_lo:[1,0,0]
	v_pk_add_f32 v[122:123], v[124:125], v[144:145]
	v_pk_add_f32 v[124:125], v[124:125], v[144:145] neg_lo:[0,1] neg_hi:[0,1]
	s_nop 0
	v_pk_mul_f32 v[138:139], v[124:125], v[104:105] op_sel_hi:[1,0]
	v_pk_fma_f32 v[124:125], v[124:125], v[104:105], v[138:139] op_sel:[1,1,0] op_sel_hi:[0,1,1] neg_lo:[1,0,0]
	v_pk_add_f32 v[138:139], v[126:127], v[118:119]
	v_pk_add_f32 v[118:119], v[126:127], v[118:119] neg_lo:[0,1] neg_hi:[0,1]
	s_nop 0
	v_pk_mul_f32 v[126:127], v[118:119], v[112:113] op_sel_hi:[1,0]
	v_pk_fma_f32 v[112:113], v[118:119], v[112:113], v[126:127] op_sel:[1,1,0] op_sel_hi:[0,1,1] neg_lo:[1,0,0]
	v_pk_add_f32 v[118:119], v[132:133], v[114:115]
	v_pk_add_f32 v[114:115], v[132:133], v[114:115] neg_lo:[0,1] neg_hi:[0,1]
	v_pk_add_f32 v[126:127], v[128:129], v[136:137]
	v_pk_add_f32 v[128:129], v[128:129], v[136:137] neg_lo:[0,1] neg_hi:[0,1]
	s_nop 0
	v_pk_mul_f32 v[132:133], v[128:129], v[102:103] op_sel_hi:[1,0]
	v_pk_fma_f32 v[128:129], v[128:129], v[102:103], v[132:133] op_sel:[1,1,0] op_sel_hi:[0,1,1] neg_lo:[1,0,0]
	v_pk_add_f32 v[132:133], v[106:107], v[122:123]
	v_pk_add_f32 v[106:107], v[106:107], v[122:123] op_sel:[1,1] op_sel_hi:[0,0] neg_lo:[1,0] neg_hi:[0,1]
	v_pk_add_f32 v[122:123], v[134:135], v[138:139]
	v_pk_add_f32 v[134:135], v[134:135], v[138:139] neg_lo:[0,1] neg_hi:[0,1]
	s_nop 0
	v_pk_mul_f32 v[136:137], v[134:135], v[104:105] op_sel_hi:[1,0]
	v_pk_fma_f32 v[134:135], v[134:135], v[104:105], v[136:137] op_sel:[1,1,0] op_sel_hi:[0,1,1] neg_lo:[1,0,0]
	v_pk_add_f32 v[136:137], v[2:3], v[120:121]
	v_pk_add_f32 v[2:3], v[2:3], v[120:121] neg_lo:[0,1] neg_hi:[0,1]
	v_pk_add_f32 v[120:121], v[4:5], v[110:111]
	v_pk_add_f32 v[4:5], v[4:5], v[110:111] neg_lo:[0,1] neg_hi:[0,1]
	s_nop 0
	v_pk_mul_f32 v[110:111], v[4:5], v[102:103] op_sel_hi:[1,0]
	v_pk_fma_f32 v[4:5], v[4:5], v[102:103], v[110:111] op_sel:[1,1,0] op_sel_hi:[0,1,1] neg_lo:[1,0,0]
	v_pk_add_f32 v[102:103], v[116:117], v[124:125]
	v_pk_add_f32 v[110:111], v[116:117], v[124:125] op_sel:[1,1] op_sel_hi:[0,0] neg_lo:[1,0] neg_hi:[0,1]
	v_pk_add_f32 v[116:117], v[108:109], v[112:113]
	v_pk_add_f32 v[108:109], v[108:109], v[112:113] neg_lo:[0,1] neg_hi:[0,1]
	v_pk_add_f32 v[124:125], v[114:115], v[106:107]
	v_pk_mul_f32 v[112:113], v[108:109], v[104:105] op_sel_hi:[1,0]
	v_pk_add_f32 v[106:107], v[114:115], v[106:107] neg_lo:[0,1] neg_hi:[0,1]
	v_pk_fma_f32 v[104:105], v[108:109], v[104:105], v[112:113] op_sel:[1,1,0] op_sel_hi:[0,1,1] neg_lo:[1,0,0]
	v_pk_add_f32 v[108:109], v[118:119], v[132:133]
	v_pk_add_f32 v[112:113], v[118:119], v[132:133] neg_lo:[0,1] neg_hi:[0,1]
	v_pk_add_f32 v[118:119], v[126:127], v[122:123]
	v_pk_add_f32 v[132:133], v[120:121], v[116:117]
	v_pk_add_f32 v[116:117], v[120:121], v[116:117] op_sel:[1,1] op_sel_hi:[0,0] neg_lo:[1,0] neg_hi:[0,1]
	v_pk_add_f32 v[120:121], v[2:3], v[110:111]
	v_pk_add_f32 v[2:3], v[2:3], v[110:111] neg_lo:[0,1] neg_hi:[0,1]
	v_pk_add_f32 v[110:111], v[4:5], v[104:105]
	v_pk_add_f32 v[4:5], v[4:5], v[104:105] op_sel:[1,1] op_sel_hi:[0,0] neg_lo:[1,0] neg_hi:[0,1]
	v_pk_add_f32 v[104:105], v[108:109], v[118:119]
	v_pk_add_f32 v[2:3], v[2:3], v[4:5]
	v_pk_mul_f32 v[4:5], v[38:39], v[104:105] op_sel_hi:[0,1]
	v_lshlrev_b32_e32 v104, 1, v130
	v_pk_add_f32 v[122:123], v[126:127], v[122:123] op_sel:[1,1] op_sel_hi:[0,0] neg_lo:[1,0] neg_hi:[0,1]
	v_pk_add_f32 v[114:115], v[128:129], v[134:135]
	v_pk_add_f32 v[126:127], v[128:129], v[134:135] op_sel:[1,1] op_sel_hi:[0,0] neg_lo:[1,0] neg_hi:[0,1]
	v_pk_add_f32 v[128:129], v[136:137], v[102:103]
	v_pk_add_f32 v[102:103], v[136:137], v[102:103] neg_lo:[0,1] neg_hi:[0,1]
	v_ashrrev_i32_e32 v105, 31, v104
	v_pk_add_f32 v[108:109], v[112:113], v[122:123]
	v_pk_add_f32 v[112:113], v[124:125], v[114:115]
	v_pk_add_f32 v[114:115], v[128:129], v[132:133]
	v_pk_add_f32 v[102:103], v[102:103], v[116:117]
	v_lshl_add_u64 v[116:117], v[104:105], 2, s[84:85]
	global_store_dwordx2 v[116:117], v[4:5], off
	v_pk_mul_f32 v[4:5], v[38:39], v[114:115] op_sel_hi:[0,1]
	v_add_u32_e32 v114, 0x800, v104
	v_ashrrev_i32_e32 v115, 31, v114
	v_lshl_add_u64 v[114:115], v[114:115], 2, s[84:85]
	global_store_dwordx2 v[114:115], v[4:5], off
	v_pk_mul_f32 v[4:5], v[38:39], v[112:113] op_sel_hi:[0,1]
	v_add_u32_e32 v112, 0x1000, v104
	v_ashrrev_i32_e32 v113, 31, v112
	v_pk_add_f32 v[110:111], v[120:121], v[110:111]
	v_lshl_add_u64 v[112:113], v[112:113], 2, s[84:85]
	global_store_dwordx2 v[112:113], v[4:5], off
	v_pk_mul_f32 v[4:5], v[38:39], v[110:111] op_sel_hi:[0,1]
	v_add_u32_e32 v110, 0x1800, v104
	v_ashrrev_i32_e32 v111, 31, v110
	v_lshl_add_u64 v[110:111], v[110:111], 2, s[84:85]
	global_store_dwordx2 v[110:111], v[4:5], off
	v_pk_mul_f32 v[4:5], v[38:39], v[108:109] op_sel_hi:[0,1]
	v_add_u32_e32 v108, 0x2000, v104
	v_ashrrev_i32_e32 v109, 31, v108
	v_lshl_add_u64 v[108:109], v[108:109], 2, s[84:85]
	global_store_dwordx2 v[108:109], v[4:5], off
	v_pk_mul_f32 v[4:5], v[38:39], v[102:103] op_sel_hi:[0,1]
	v_add_u32_e32 v102, 0x2800, v104
	v_ashrrev_i32_e32 v103, 31, v102
	v_lshl_add_u64 v[102:103], v[102:103], 2, s[84:85]
	global_store_dwordx2 v[102:103], v[4:5], off
	v_add_u32_e32 v102, 0x3000, v104
	v_pk_add_f32 v[106:107], v[106:107], v[126:127]
	v_ashrrev_i32_e32 v103, 31, v102
	v_pk_mul_f32 v[4:5], v[38:39], v[106:107] op_sel_hi:[0,1]
	v_lshl_add_u64 v[102:103], v[102:103], 2, s[84:85]
	global_store_dwordx2 v[102:103], v[4:5], off
	v_add_u32_e32 v4, 0x3800, v104
	v_ashrrev_i32_e32 v5, 31, v4
	v_pk_mul_f32 v[2:3], v[38:39], v[2:3] op_sel_hi:[0,1]
	v_lshl_add_u64 v[4:5], v[4:5], 2, s[84:85]
	global_store_dwordx2 v[4:5], v[2:3], off
	s_waitcnt lgkmcnt(0)
	s_barrier
	s_cbranch_scc1 .LBB0_755
	v_readlane_b32 s86, v253, 12
	s_add_i32 s95, s95, s86
	s_cmpk_lt_i32 s95, 0x100
	s_barrier
	v_readlane_b32 s87, v253, 13
	s_cbranch_scc1 .LBB0_750
	v_readlane_b32 s88, v253, 16
	v_readlane_b32 s84, v253, 31
	v_readlane_b32 s92, v253, 20
	v_readlane_b32 s60, v252, 57
	v_readlane_b32 s64, v252, 41
	v_readlane_b32 s36, v253, 14
	v_readlane_b32 s94, v253, 22
	v_readlane_b32 s95, v253, 23
	s_mov_b32 s92, s84
	v_readlane_b32 s97, v253, 28
	v_readlane_b32 s63, v253, 27
	v_readlane_b32 s61, v252, 58
	v_readlane_b32 s56, v252, 59
	v_readlane_b32 s72, v252, 49
	v_readlane_b32 s73, v252, 50
	s_mov_b32 s62, s86
	v_readlane_b32 s37, v253, 15
	v_readlane_b32 s85, v253, 32
	v_readlane_b32 s89, v253, 17
	v_readlane_b32 s90, v253, 18
	v_readlane_b32 s91, v253, 19
	v_readlane_b32 s93, v253, 21
	v_readlane_b32 s65, v252, 42
	v_readlane_b32 s66, v252, 43
	v_readlane_b32 s67, v252, 44
	v_readlane_b32 s68, v252, 45
	v_readlane_b32 s69, v252, 46
	v_readlane_b32 s70, v252, 47
	v_readlane_b32 s71, v252, 48
	v_readlane_b32 s74, v252, 51
	v_readlane_b32 s75, v252, 52
	v_readlane_b32 s76, v252, 53
	v_readlane_b32 s77, v252, 54
	v_readlane_b32 s78, v252, 55
	v_readlane_b32 s79, v252, 56
